# GEMM K-loops: the back-to-back s_setprio 0 / s_setprio 1 pair between the two 16-MFMA groups of every sub-phase removed (priority stays raised across the 32 MFMAs)
# baseline (speedup 1.0000x reference)
; #define G8_STAGE(bufoff, gbase, v0, v1) do { \
;         __builtin_amdgcn_global_load_lds((const unsigned*)((const char*)(gbase) + (v0)), (LAS unsigned*)(lds + (bufoff) + ldsw), 16, 0, 0); \
;         __builtin_amdgcn_global_load_lds((const unsigned*)((const char*)(gbase) + (v1)), (LAS unsigned*)(lds + (bufoff) + ldsw + 8192), 16, 0, 0); } while (0)
; #define G8_LDA(dst, b, h) do { _Pragma("unroll") for (int m = 0; m < 4; ++m) _Pragma("unroll") for (int k = 0; k < 2; ++k) dst[m][k] = *(const LAS bf16x8*)(lds + G8_SA(b, h) + aoff + m * 2048 + k * 1024); } while (0)
; #define G8_LDB(dst, b, h) do { _Pragma("unroll") for (int n = 0; n < 2; ++n) _Pragma("unroll") for (int k = 0; k < 2; ++k) dst[n][k] = *(const LAS bf16x8*)(lds + G8_SB(b, h) + boff + n * 2048 + k * 1024); } while (0)
; #define G8_WAIT_V(n) asm volatile("s_waitcnt vmcnt(" #n ")" ::: "memory")
; #define G8_WAIT_L(n) asm volatile("s_waitcnt lgkmcnt(" #n ")" ::: "memory")
; #define G8_BAR __builtin_amdgcn_s_barrier()
; #define G8_SCHED __builtin_amdgcn_sched_barrier(0)
; template <class Epi, class Sched, bool GATHER, bool ALIGN_EPI, bool PFB = false>
; __device__ __forceinline__ void gemm_phase(LAS unsigned char* lds, const int lda, const int K, const Sched& S, const Epi& E) {
;     ...
;             G8_LDB(B0, 0, 0); G8_LDB(B1, 0, 1); G8_SCHED; G8_LDA(At, 0, 0); G8_STAGE(G8_SA(1, 1), a1, vA1[0], vA1[1]);
;             G8_WAIT_V(8); if (PFB) asm volatile("" : "+v"(pf_dummy)); G8_WAIT_L(0); G8_BAR; G8_MMA(0, 0, At, B0); G8_MMA(0, 1, At, B1); G8_BAR; G8_SCHED;
;             G8_LDA(At, 0, 1); G8_STAGE(G8_SB(0, 0), b2, voffB[0], voffB[1]); G8_STAGE(G8_SB(0, 1), b2 + hstepB, voffB[0], voffB[1]); G8_STAGE(G8_SA(0, 0), a2, x00, x01);
;             G8_WAIT_V(8); G8_WAIT_L(0); G8_BAR; G8_MMA(1, 0, At, B0); G8_MMA(1, 1, At, B1); G8_BAR; G8_SCHED;
;             G8_LDB(B0, 1, 0); G8_LDB(B1, 1, 1); G8_SCHED; G8_LDA(At, 1, 0); G8_STAGE(G8_SA(0, 1), a2, x10, x11);
;             G8_WAIT_V(8); G8_WAIT_L(0); G8_BAR; G8_MMA(0, 0, At, B0); G8_MMA(0, 1, At, B1); G8_BAR; G8_SCHED;
;             G8_LDA(At, 1, 1); G8_STAGE(G8_SB(1, 0), b3, voffB[0], voffB[1]); G8_STAGE(G8_SB(1, 1), b3 + hstepB, voffB[0], voffB[1]); G8_STAGE(G8_SA(1, 0), a3, x00, x01);
;             G8_WAIT_V(8); G8_WAIT_L(0); G8_BAR; G8_MMA(1, 0, At, B0); G8_MMA(1, 1, At, B1); G8_BAR; G8_SCHED;
.LBB0_772:
	ds_read_b128 v[150:153], v159
	ds_read_b128 v[162:165], v159 offset:1024
	ds_read_b128 v[166:169], v159 offset:2048
	ds_read_b128 v[170:173], v159 offset:3072
	ds_read_b128 v[174:177], v160
	ds_read_b128 v[178:181], v160 offset:1024
	ds_read_b128 v[184:187], v160 offset:2048
	ds_read_b128 v[188:191], v160 offset:3072
	s_add_u32 s28, s26, 0x80
	s_addc_u32 s29, s27, 0
	s_cmp_eq_u32 s56, 12
	s_cselect_b32 s31, s17, s29
	s_cselect_b32 s30, s16, s28
	s_cselect_b32 s29, s19, s15
	s_cselect_b32 s28, s18, s13
	v_lshl_add_u64 v[224:225], s[26:27], 0, v[142:143]
	s_add_i32 m0, s21, 0xc000
	ds_read_b128 v[192:195], v161
	ds_read_b128 v[196:199], v161 offset:1024
	ds_read_b128 v[200:203], v161 offset:2048
	ds_read_b128 v[204:207], v161 offset:3072
	ds_read_b128 v[208:211], v161 offset:4096
	ds_read_b128 v[212:215], v161 offset:5120
	ds_read_b128 v[216:219], v161 offset:6144
	ds_read_b128 v[220:223], v161 offset:7168
	global_load_lds_dwordx4 v[224:225], off
	v_lshl_add_u64 v[224:225], s[26:27], 0, v[144:145]
	s_add_i32 m0, s21, 0xe000
	s_nop 0
	global_load_lds_dwordx4 v[224:225], off
	s_waitcnt vmcnt(8)
	s_waitcnt lgkmcnt(0)
	s_barrier
	s_setprio 1
	s_waitcnt lgkmcnt(0)
	v_mfma_f32_16x16x32_bf16 v[126:129], v[150:153], v[192:195], v[126:129]
	v_mfma_f32_16x16x32_bf16 v[122:125], v[166:169], v[192:195], v[122:125]
	v_mfma_f32_16x16x32_bf16 v[118:121], v[150:153], v[200:203], v[118:121]
	v_mfma_f32_16x16x32_bf16 v[110:113], v[166:169], v[200:203], v[110:113]
	v_mfma_f32_16x16x32_bf16 v[102:105], v[150:153], v[208:211], v[102:105]
	v_mfma_f32_16x16x32_bf16 v[94:97], v[166:169], v[208:211], v[94:97]
	v_mfma_f32_16x16x32_bf16 v[86:89], v[150:153], v[216:219], v[86:89]
	v_mfma_f32_16x16x32_bf16 v[78:81], v[166:169], v[216:219], v[78:81]
	v_mfma_f32_16x16x32_bf16 v[126:129], v[162:165], v[196:199], v[126:129]
	v_mfma_f32_16x16x32_bf16 v[122:125], v[170:173], v[196:199], v[122:125]
	v_mfma_f32_16x16x32_bf16 v[118:121], v[162:165], v[204:207], v[118:121]
	v_mfma_f32_16x16x32_bf16 v[110:113], v[170:173], v[204:207], v[110:113]
	v_mfma_f32_16x16x32_bf16 v[102:105], v[162:165], v[212:215], v[102:105]
	v_mfma_f32_16x16x32_bf16 v[94:97], v[170:173], v[212:215], v[94:97]
	v_mfma_f32_16x16x32_bf16 v[86:89], v[162:165], v[220:223], v[86:89]
	v_mfma_f32_16x16x32_bf16 v[78:81], v[170:173], v[220:223], v[78:81]
	v_mfma_f32_16x16x32_bf16 v[114:117], v[174:177], v[192:195], v[114:117]
	v_mfma_f32_16x16x32_bf16 v[106:109], v[184:187], v[192:195], v[106:109]
	v_mfma_f32_16x16x32_bf16 v[98:101], v[174:177], v[200:203], v[98:101]
	v_mfma_f32_16x16x32_bf16 v[90:93], v[184:187], v[200:203], v[90:93]
	v_mfma_f32_16x16x32_bf16 v[82:85], v[174:177], v[208:211], v[82:85]
	v_mfma_f32_16x16x32_bf16 v[74:77], v[184:187], v[208:211], v[74:77]
	v_mfma_f32_16x16x32_bf16 v[70:73], v[174:177], v[216:219], v[70:73]
	v_mfma_f32_16x16x32_bf16 v[66:69], v[184:187], v[216:219], v[66:69]
	v_mfma_f32_16x16x32_bf16 v[114:117], v[178:181], v[196:199], v[114:117]
	v_mfma_f32_16x16x32_bf16 v[106:109], v[188:191], v[196:199], v[106:109]
	v_mfma_f32_16x16x32_bf16 v[98:101], v[178:181], v[204:207], v[98:101]
	v_mfma_f32_16x16x32_bf16 v[90:93], v[188:191], v[204:207], v[90:93]
	v_mfma_f32_16x16x32_bf16 v[82:85], v[178:181], v[212:215], v[82:85]
	v_mfma_f32_16x16x32_bf16 v[74:77], v[188:191], v[212:215], v[74:77]
	v_mfma_f32_16x16x32_bf16 v[70:73], v[178:181], v[220:223], v[70:73]
	v_mfma_f32_16x16x32_bf16 v[66:69], v[188:191], v[220:223], v[66:69]
	s_setprio 0
	s_barrier
	s_add_i32 s33, s52, s36
	v_lshl_add_u64 v[224:225], s[28:29], 0, v[130:131]
	s_mov_b32 m0, s33
	ds_read_b128 v[192:195], v161 offset:16384
	ds_read_b128 v[196:199], v161 offset:17408
	ds_read_b128 v[200:203], v161 offset:18432
	ds_read_b128 v[204:207], v161 offset:19456
	ds_read_b128 v[208:211], v161 offset:20480
	ds_read_b128 v[212:215], v161 offset:21504
	ds_read_b128 v[216:219], v161 offset:22528
	ds_read_b128 v[220:223], v161 offset:23552
	global_load_lds_dwordx4 v[224:225], off
	s_add_i32 m0, s33, 0x2000
	s_add_u32 s60, s28, 0x4000
	v_lshl_add_u64 v[224:225], s[28:29], 0, v[132:133]
	s_addc_u32 s61, s29, 0
	s_add_i32 s33, s53, s36
	global_load_lds_dwordx4 v[224:225], off
	v_lshl_add_u64 v[224:225], s[60:61], 0, v[130:131]
	s_mov_b32 m0, s33
	v_lshl_add_u64 v[226:227], s[30:31], 0, v[138:139]
	global_load_lds_dwordx4 v[224:225], off
	v_lshl_add_u64 v[224:225], s[60:61], 0, v[132:133]
	s_add_i32 m0, s33, 0x2000
	s_nop 0
	global_load_lds_dwordx4 v[224:225], off
	v_lshl_add_u64 v[224:225], s[30:31], 0, v[134:135]
	s_mov_b32 m0, s21
	s_nop 0
	global_load_lds_dwordx4 v[224:225], off
	s_mov_b32 m0, s37
	s_nop 0
	global_load_lds_dwordx4 v[226:227], off
	s_waitcnt vmcnt(8)
	s_waitcnt lgkmcnt(0)
	s_barrier
; #define G8_STAGE(bufoff, gbase, v0, v1) do { \
;         __builtin_amdgcn_global_load_lds((const unsigned*)((const char*)(gbase) + (v0)), (LAS unsigned*)(lds + (bufoff) + ldsw), 16, 0, 0); \
;         __builtin_amdgcn_global_load_lds((const unsigned*)((const char*)(gbase) + (v1)), (LAS unsigned*)(lds + (bufoff) + ldsw + 8192), 16, 0, 0); } while (0)
; #define G8_LDA(dst, b, h) do { _Pragma("unroll") for (int m = 0; m < 4; ++m) _Pragma("unroll") for (int k = 0; k < 2; ++k) dst[m][k] = *(const LAS bf16x8*)(lds + G8_SA(b, h) + aoff + m * 2048 + k * 1024); } while (0)
; #define G8_LDB(dst, b, h) do { _Pragma("unroll") for (int n = 0; n < 2; ++n) _Pragma("unroll") for (int k = 0; k < 2; ++k) dst[n][k] = *(const LAS bf16x8*)(lds + G8_SB(b, h) + boff + n * 2048 + k * 1024); } while (0)
; #define G8_WAIT_V(n) asm volatile("s_waitcnt vmcnt(" #n ")" ::: "memory")
; #define G8_WAIT_L(n) asm volatile("s_waitcnt lgkmcnt(" #n ")" ::: "memory")
; #define G8_BAR __builtin_amdgcn_s_barrier()
; #define G8_SCHED __builtin_amdgcn_sched_barrier(0)
; template <class Epi, class Sched, bool GATHER, bool ALIGN_EPI, bool PFB = false>
; __device__ __forceinline__ void gemm_phase(LAS unsigned char* lds, const int lda, const int K, const Sched& S, const Epi& E) {
;     ...
;             G8_LDB(B0, 0, 0); G8_LDB(B1, 0, 1); G8_SCHED; G8_LDA(At, 0, 0); G8_STAGE(G8_SA(1, 1), a1, vA1[0], vA1[1]);
;             G8_WAIT_V(8); if (PFB) asm volatile("" : "+v"(pf_dummy)); G8_WAIT_L(0); G8_BAR; G8_MMA(0, 0, At, B0); G8_MMA(0, 1, At, B1); G8_BAR; G8_SCHED;
;             G8_LDA(At, 0, 1); G8_STAGE(G8_SB(0, 0), b2, voffB[0], voffB[1]); G8_STAGE(G8_SB(0, 1), b2 + hstepB, voffB[0], voffB[1]); G8_STAGE(G8_SA(0, 0), a2, x00, x01);
;             G8_WAIT_V(8); G8_WAIT_L(0); G8_BAR; G8_MMA(1, 0, At, B0); G8_MMA(1, 1, At, B1); G8_BAR; G8_SCHED;
;             G8_LDB(B0, 1, 0); G8_LDB(B1, 1, 1); G8_SCHED; G8_LDA(At, 1, 0); G8_STAGE(G8_SA(0, 1), a2, x10, x11);
;             G8_WAIT_V(8); G8_WAIT_L(0); G8_BAR; G8_MMA(0, 0, At, B0); G8_MMA(0, 1, At, B1); G8_BAR; G8_SCHED;
;             G8_LDA(At, 1, 1); G8_STAGE(G8_SB(1, 0), b3, voffB[0], voffB[1]); G8_STAGE(G8_SB(1, 1), b3 + hstepB, voffB[0], voffB[1]); G8_STAGE(G8_SA(1, 0), a3, x00, x01);
;             G8_WAIT_V(8); G8_WAIT_L(0); G8_BAR; G8_MMA(1, 0, At, B0); G8_MMA(1, 1, At, B1); G8_BAR; G8_SCHED;
	s_setprio 1
	s_waitcnt lgkmcnt(0)
	v_mfma_f32_16x16x32_bf16 v[62:65], v[150:153], v[192:195], v[62:65]
	v_mfma_f32_16x16x32_bf16 v[58:61], v[166:169], v[192:195], v[58:61]
	v_mfma_f32_16x16x32_bf16 v[54:57], v[150:153], v[200:203], v[54:57]
	v_mfma_f32_16x16x32_bf16 v[46:49], v[166:169], v[200:203], v[46:49]
	v_mfma_f32_16x16x32_bf16 v[38:41], v[150:153], v[208:211], v[38:41]
	v_mfma_f32_16x16x32_bf16 v[30:33], v[166:169], v[208:211], v[30:33]
	v_mfma_f32_16x16x32_bf16 v[22:25], v[150:153], v[216:219], v[22:25]
	v_mfma_f32_16x16x32_bf16 v[14:17], v[166:169], v[216:219], v[14:17]
	v_mfma_f32_16x16x32_bf16 v[62:65], v[162:165], v[196:199], v[62:65]
	v_mfma_f32_16x16x32_bf16 v[58:61], v[170:173], v[196:199], v[58:61]
	v_mfma_f32_16x16x32_bf16 v[54:57], v[162:165], v[204:207], v[54:57]
	v_mfma_f32_16x16x32_bf16 v[46:49], v[170:173], v[204:207], v[46:49]
	v_mfma_f32_16x16x32_bf16 v[38:41], v[162:165], v[212:215], v[38:41]
	v_mfma_f32_16x16x32_bf16 v[30:33], v[170:173], v[212:215], v[30:33]
	v_mfma_f32_16x16x32_bf16 v[22:25], v[162:165], v[220:223], v[22:25]
	v_mfma_f32_16x16x32_bf16 v[14:17], v[170:173], v[220:223], v[14:17]
	v_mfma_f32_16x16x32_bf16 v[50:53], v[174:177], v[192:195], v[50:53]
	v_mfma_f32_16x16x32_bf16 v[42:45], v[184:187], v[192:195], v[42:45]
	v_mfma_f32_16x16x32_bf16 v[34:37], v[174:177], v[200:203], v[34:37]
	v_mfma_f32_16x16x32_bf16 v[26:29], v[184:187], v[200:203], v[26:29]
	v_mfma_f32_16x16x32_bf16 v[18:21], v[174:177], v[208:211], v[18:21]
	v_mfma_f32_16x16x32_bf16 v[10:13], v[184:187], v[208:211], v[10:13]
	v_mfma_f32_16x16x32_bf16 v[6:9], v[174:177], v[216:219], v[6:9]
	v_mfma_f32_16x16x32_bf16 v[2:5], v[184:187], v[216:219], v[2:5]
	v_mfma_f32_16x16x32_bf16 v[50:53], v[178:181], v[196:199], v[50:53]
	v_mfma_f32_16x16x32_bf16 v[42:45], v[188:191], v[196:199], v[42:45]
	v_mfma_f32_16x16x32_bf16 v[34:37], v[178:181], v[204:207], v[34:37]
	v_mfma_f32_16x16x32_bf16 v[26:29], v[188:191], v[204:207], v[26:29]
	v_mfma_f32_16x16x32_bf16 v[18:21], v[178:181], v[212:215], v[18:21]
	v_mfma_f32_16x16x32_bf16 v[10:13], v[188:191], v[212:215], v[10:13]
	v_mfma_f32_16x16x32_bf16 v[6:9], v[178:181], v[220:223], v[6:9]
	v_mfma_f32_16x16x32_bf16 v[2:5], v[188:191], v[220:223], v[2:5]
	s_setprio 0
	s_barrier
	s_add_i32 s33, 0, 0x18000
	s_add_i32 s57, 0, 0x1c000
	v_add_u32_e32 v170, s33, v157
	v_add_u32_e32 v188, s57, v157
	ds_read_b128 v[150:153], v170
	ds_read_b128 v[162:165], v170 offset:1024
	ds_read_b128 v[166:169], v170 offset:2048
	ds_read_b128 v[170:173], v170 offset:3072
	ds_read_b128 v[174:177], v188
	ds_read_b128 v[178:181], v188 offset:1024
	ds_read_b128 v[184:187], v188 offset:2048
	ds_read_b128 v[188:191], v188 offset:3072
	s_mov_b32 m0, s38
	v_lshl_add_u64 v[228:229], s[30:31], 0, v[136:137]
	ds_read_b128 v[192:195], v161 offset:32768
	ds_read_b128 v[196:199], v161 offset:33792
	ds_read_b128 v[200:203], v161 offset:34816
	ds_read_b128 v[204:207], v161 offset:35840
	ds_read_b128 v[208:211], v161 offset:36864
	ds_read_b128 v[212:215], v161 offset:37888
	ds_read_b128 v[216:219], v161 offset:38912
	ds_read_b128 v[220:223], v161 offset:39936
	global_load_lds_dwordx4 v[228:229], off
	v_lshl_add_u64 v[228:229], s[30:31], 0, v[140:141]
	s_mov_b32 m0, s39
	s_nop 0
	global_load_lds_dwordx4 v[228:229], off
	s_waitcnt vmcnt(8)
	s_waitcnt lgkmcnt(0)
	s_barrier
	s_setprio 1
	s_waitcnt lgkmcnt(0)
	v_mfma_f32_16x16x32_bf16 v[126:129], v[150:153], v[192:195], v[126:129]
	v_mfma_f32_16x16x32_bf16 v[122:125], v[166:169], v[192:195], v[122:125]
	v_mfma_f32_16x16x32_bf16 v[118:121], v[150:153], v[200:203], v[118:121]
	v_mfma_f32_16x16x32_bf16 v[110:113], v[166:169], v[200:203], v[110:113]
	v_mfma_f32_16x16x32_bf16 v[102:105], v[150:153], v[208:211], v[102:105]
	v_mfma_f32_16x16x32_bf16 v[94:97], v[166:169], v[208:211], v[94:97]
	v_mfma_f32_16x16x32_bf16 v[86:89], v[150:153], v[216:219], v[86:89]
	v_mfma_f32_16x16x32_bf16 v[78:81], v[166:169], v[216:219], v[78:81]
	v_mfma_f32_16x16x32_bf16 v[126:129], v[162:165], v[196:199], v[126:129]
	v_mfma_f32_16x16x32_bf16 v[122:125], v[170:173], v[196:199], v[122:125]
	v_mfma_f32_16x16x32_bf16 v[118:121], v[162:165], v[204:207], v[118:121]
	v_mfma_f32_16x16x32_bf16 v[110:113], v[170:173], v[204:207], v[110:113]
	v_mfma_f32_16x16x32_bf16 v[102:105], v[162:165], v[212:215], v[102:105]
	v_mfma_f32_16x16x32_bf16 v[94:97], v[170:173], v[212:215], v[94:97]
	v_mfma_f32_16x16x32_bf16 v[86:89], v[162:165], v[220:223], v[86:89]
	v_mfma_f32_16x16x32_bf16 v[78:81], v[170:173], v[220:223], v[78:81]
	v_mfma_f32_16x16x32_bf16 v[114:117], v[174:177], v[192:195], v[114:117]
	v_mfma_f32_16x16x32_bf16 v[106:109], v[184:187], v[192:195], v[106:109]
	v_mfma_f32_16x16x32_bf16 v[98:101], v[174:177], v[200:203], v[98:101]
	v_mfma_f32_16x16x32_bf16 v[90:93], v[184:187], v[200:203], v[90:93]
	v_mfma_f32_16x16x32_bf16 v[82:85], v[174:177], v[208:211], v[82:85]
	v_mfma_f32_16x16x32_bf16 v[74:77], v[184:187], v[208:211], v[74:77]
	v_mfma_f32_16x16x32_bf16 v[70:73], v[174:177], v[216:219], v[70:73]
	v_mfma_f32_16x16x32_bf16 v[66:69], v[184:187], v[216:219], v[66:69]
	v_mfma_f32_16x16x32_bf16 v[114:117], v[178:181], v[196:199], v[114:117]
	v_mfma_f32_16x16x32_bf16 v[106:109], v[188:191], v[196:199], v[106:109]
	v_mfma_f32_16x16x32_bf16 v[98:101], v[178:181], v[204:207], v[98:101]
	v_mfma_f32_16x16x32_bf16 v[90:93], v[188:191], v[204:207], v[90:93]
	v_mfma_f32_16x16x32_bf16 v[82:85], v[178:181], v[212:215], v[82:85]
	v_mfma_f32_16x16x32_bf16 v[74:77], v[188:191], v[212:215], v[74:77]
	v_mfma_f32_16x16x32_bf16 v[70:73], v[178:181], v[220:223], v[70:73]
	v_mfma_f32_16x16x32_bf16 v[66:69], v[188:191], v[220:223], v[66:69]
	s_setprio 0
	s_barrier
; #define G8_STAGE(bufoff, gbase, v0, v1) do { \
;         __builtin_amdgcn_global_load_lds((const unsigned*)((const char*)(gbase) + (v0)), (LAS unsigned*)(lds + (bufoff) + ldsw), 16, 0, 0); \
;         __builtin_amdgcn_global_load_lds((const unsigned*)((const char*)(gbase) + (v1)), (LAS unsigned*)(lds + (bufoff) + ldsw + 8192), 16, 0, 0); } while (0)
; #define G8_LDA(dst, b, h) do { _Pragma("unroll") for (int m = 0; m < 4; ++m) _Pragma("unroll") for (int k = 0; k < 2; ++k) dst[m][k] = *(const LAS bf16x8*)(lds + G8_SA(b, h) + aoff + m * 2048 + k * 1024); } while (0)
; #define G8_LDB(dst, b, h) do { _Pragma("unroll") for (int n = 0; n < 2; ++n) _Pragma("unroll") for (int k = 0; k < 2; ++k) dst[n][k] = *(const LAS bf16x8*)(lds + G8_SB(b, h) + boff + n * 2048 + k * 1024); } while (0)
; #define G8_MMA(ai, bj, At, Bt) do { __builtin_amdgcn_s_setprio(1); _Pragma("unroll") for (int m = 0; m < 4; ++m) _Pragma("unroll") for (int n = 0; n < 2; ++n) _Pragma("unroll") for (int k = 0; k < 2; ++k) \
;         acc[ai][bj][m][n] = __builtin_amdgcn_mfma_f32_16x16x32_bf16(Bt[n][k], At[m][k], acc[ai][bj][m][n], 0, 0, 0); __builtin_amdgcn_s_setprio(0); } while (0)
; #define G8_WAIT_V(n) asm volatile("s_waitcnt vmcnt(" #n ")" ::: "memory")
; #define G8_WAIT_L(n) asm volatile("s_waitcnt lgkmcnt(" #n ")" ::: "memory")
; #define G8_BAR __builtin_amdgcn_s_barrier()
; #define G8_SCHED __builtin_amdgcn_sched_barrier(0)
; template <class Epi, class Sched, bool GATHER, bool ALIGN_EPI, bool PFB = false>
; __device__ __forceinline__ void gemm_phase(LAS unsigned char* lds, const int lda, const int K, const Sched& S, const Epi& E) {
;     ...
;             G8_LDB(B0, 1, 0); G8_LDB(B1, 1, 1); G8_SCHED; G8_LDA(At, 1, 0); G8_STAGE(G8_SA(0, 1), a2, x10, x11);
;             G8_WAIT_V(8); G8_WAIT_L(0); G8_BAR; G8_MMA(0, 0, At, B0); G8_MMA(0, 1, At, B1); G8_BAR; G8_SCHED;
;             G8_LDA(At, 1, 1); G8_STAGE(G8_SB(1, 0), b3, voffB[0], voffB[1]); G8_STAGE(G8_SB(1, 1), b3 + hstepB, voffB[0], voffB[1]); G8_STAGE(G8_SA(1, 0), a3, x00, x01);
;             G8_WAIT_V(8); G8_WAIT_L(0); G8_BAR; G8_MMA(1, 0, At, B0); G8_MMA(1, 1, At, B1); G8_BAR; G8_SCHED;
;         }
	s_add_u32 s30, s28, 0x8000
	s_addc_u32 s31, s29, 0
	s_add_i32 s33, s33, s36
	v_lshl_add_u64 v[228:229], s[30:31], 0, v[130:131]
	s_mov_b32 m0, s33
	ds_read_b128 v[192:195], v161 offset:49152
	ds_read_b128 v[196:199], v161 offset:50176
	ds_read_b128 v[200:203], v161 offset:51200
	ds_read_b128 v[204:207], v161 offset:52224
	ds_read_b128 v[208:211], v161 offset:53248
	ds_read_b128 v[212:215], v161 offset:54272
	ds_read_b128 v[216:219], v161 offset:55296
	ds_read_b128 v[220:223], v161 offset:56320
	global_load_lds_dwordx4 v[228:229], off
	s_add_i32 m0, s33, 0x2000
	s_add_u32 s28, s28, 0xc000
	v_lshl_add_u64 v[228:229], s[30:31], 0, v[132:133]
	s_addc_u32 s29, s29, 0
	s_add_i32 s30, s57, s36
	global_load_lds_dwordx4 v[228:229], off
	v_lshl_add_u64 v[228:229], s[28:29], 0, v[130:131]
	s_mov_b32 m0, s30
	v_lshl_add_u64 v[224:225], v[224:225], 0, s[8:9]
	global_load_lds_dwordx4 v[228:229], off
	v_lshl_add_u64 v[228:229], s[28:29], 0, v[132:133]
	s_add_i32 m0, s30, 0x2000
	s_nop 0
	global_load_lds_dwordx4 v[228:229], off
	s_mov_b32 m0, s45
	s_nop 0
	global_load_lds_dwordx4 v[224:225], off
	v_lshl_add_u64 v[224:225], v[226:227], 0, s[8:9]
	s_mov_b32 m0, s48
	s_nop 0
	global_load_lds_dwordx4 v[224:225], off
	s_waitcnt vmcnt(8)
	s_waitcnt lgkmcnt(0)
	s_barrier
	s_setprio 1
	s_waitcnt lgkmcnt(0)
	v_mfma_f32_16x16x32_bf16 v[62:65], v[150:153], v[192:195], v[62:65]
	v_mfma_f32_16x16x32_bf16 v[58:61], v[166:169], v[192:195], v[58:61]
	v_mfma_f32_16x16x32_bf16 v[54:57], v[150:153], v[200:203], v[54:57]
	v_mfma_f32_16x16x32_bf16 v[46:49], v[166:169], v[200:203], v[46:49]
	v_mfma_f32_16x16x32_bf16 v[38:41], v[150:153], v[208:211], v[38:41]
	v_mfma_f32_16x16x32_bf16 v[30:33], v[166:169], v[208:211], v[30:33]
	v_mfma_f32_16x16x32_bf16 v[22:25], v[150:153], v[216:219], v[22:25]
	v_mfma_f32_16x16x32_bf16 v[14:17], v[166:169], v[216:219], v[14:17]
	v_mfma_f32_16x16x32_bf16 v[62:65], v[162:165], v[196:199], v[62:65]
	v_mfma_f32_16x16x32_bf16 v[58:61], v[170:173], v[196:199], v[58:61]
	v_mfma_f32_16x16x32_bf16 v[54:57], v[162:165], v[204:207], v[54:57]
	v_mfma_f32_16x16x32_bf16 v[46:49], v[170:173], v[204:207], v[46:49]
	v_mfma_f32_16x16x32_bf16 v[38:41], v[162:165], v[212:215], v[38:41]
	v_mfma_f32_16x16x32_bf16 v[30:33], v[170:173], v[212:215], v[30:33]
	v_mfma_f32_16x16x32_bf16 v[22:25], v[162:165], v[220:223], v[22:25]
	v_mfma_f32_16x16x32_bf16 v[14:17], v[170:173], v[220:223], v[14:17]
	v_mfma_f32_16x16x32_bf16 v[50:53], v[174:177], v[192:195], v[50:53]
	v_mfma_f32_16x16x32_bf16 v[42:45], v[184:187], v[192:195], v[42:45]
	v_mfma_f32_16x16x32_bf16 v[34:37], v[174:177], v[200:203], v[34:37]
	v_mfma_f32_16x16x32_bf16 v[26:29], v[184:187], v[200:203], v[26:29]
	v_mfma_f32_16x16x32_bf16 v[18:21], v[174:177], v[208:211], v[18:21]
	v_mfma_f32_16x16x32_bf16 v[10:13], v[184:187], v[208:211], v[10:13]
	v_mfma_f32_16x16x32_bf16 v[6:9], v[174:177], v[216:219], v[6:9]
	v_mfma_f32_16x16x32_bf16 v[2:5], v[184:187], v[216:219], v[2:5]
	v_mfma_f32_16x16x32_bf16 v[50:53], v[178:181], v[196:199], v[50:53]
	v_mfma_f32_16x16x32_bf16 v[42:45], v[188:191], v[196:199], v[42:45]
	v_mfma_f32_16x16x32_bf16 v[34:37], v[178:181], v[204:207], v[34:37]
	v_mfma_f32_16x16x32_bf16 v[26:29], v[188:191], v[204:207], v[26:29]
	v_mfma_f32_16x16x32_bf16 v[18:21], v[178:181], v[212:215], v[18:21]
	v_mfma_f32_16x16x32_bf16 v[10:13], v[188:191], v[212:215], v[10:13]
	v_mfma_f32_16x16x32_bf16 v[6:9], v[178:181], v[220:223], v[6:9]
	v_mfma_f32_16x16x32_bf16 v[2:5], v[188:191], v[220:223], v[2:5]
	s_setprio 0
	s_barrier
	s_add_i32 s56, s56, 2
	s_add_u32 s13, s13, 0x10000
	s_addc_u32 s15, s15, 0
	s_add_u32 s26, s26, 0x100
	s_addc_u32 s27, s27, 0
	s_cmp_gt_u32 s56, 13
	s_cbranch_scc0 .LBB0_772
	s_and_b64 vcc, exec, s[10:11]
	s_cbranch_vccz .LBB0_775
	s_barrier

; #define G8_STAGE(bufoff, gbase, v0, v1) do { \
;         __builtin_amdgcn_global_load_lds((const unsigned*)((const char*)(gbase) + (v0)), (LAS unsigned*)(lds + (bufoff) + ldsw), 16, 0, 0); \
;         __builtin_amdgcn_global_load_lds((const unsigned*)((const char*)(gbase) + (v1)), (LAS unsigned*)(lds + (bufoff) + ldsw + 8192), 16, 0, 0); } while (0)
; #define G8_LDA(dst, b, h) do { _Pragma("unroll") for (int m = 0; m < 4; ++m) _Pragma("unroll") for (int k = 0; k < 2; ++k) dst[m][k] = *(const LAS bf16x8*)(lds + G8_SA(b, h) + aoff + m * 2048 + k * 1024); } while (0)
; #define G8_LDB(dst, b, h) do { _Pragma("unroll") for (int n = 0; n < 2; ++n) _Pragma("unroll") for (int k = 0; k < 2; ++k) dst[n][k] = *(const LAS bf16x8*)(lds + G8_SB(b, h) + boff + n * 2048 + k * 1024); } while (0)
; #define G8_MMA(ai, bj, At, Bt) do { __builtin_amdgcn_s_setprio(1); _Pragma("unroll") for (int m = 0; m < 4; ++m) _Pragma("unroll") for (int n = 0; n < 2; ++n) _Pragma("unroll") for (int k = 0; k < 2; ++k) \
;         acc[ai][bj][m][n] = __builtin_amdgcn_mfma_f32_16x16x32_bf16(Bt[n][k], At[m][k], acc[ai][bj][m][n], 0, 0, 0); __builtin_amdgcn_s_setprio(0); } while (0)
; #define G8_WAIT_V(n) asm volatile("s_waitcnt vmcnt(" #n ")" ::: "memory")
; #define G8_WAIT_L(n) asm volatile("s_waitcnt lgkmcnt(" #n ")" ::: "memory")
; #define G8_BAR __builtin_amdgcn_s_barrier()
; #define G8_SCHED __builtin_amdgcn_sched_barrier(0)
; template <class Epi, class Sched, bool GATHER, bool ALIGN_EPI, bool PFB = false>
; __device__ __forceinline__ void gemm_phase(LAS unsigned char* lds, const int lda, const int K, const Sched& S, const Epi& E) {
;     ...
;             G8_LDB(B0, 0, 0); G8_LDB(B1, 0, 1); G8_SCHED; G8_LDA(At, 0, 0); G8_STAGE(G8_SA(1, 1), a1, vA1[0], vA1[1]);
;             G8_WAIT_V(8); if (PFB) asm volatile("" : "+v"(pf_dummy)); G8_WAIT_L(0); G8_BAR; G8_MMA(0, 0, At, B0); G8_MMA(0, 1, At, B1); G8_BAR; G8_SCHED;
;             G8_LDA(At, 0, 1); G8_STAGE(G8_SB(0, 0), b2, voffB[0], voffB[1]); G8_STAGE(G8_SB(0, 1), b2 + hstepB, voffB[0], voffB[1]); G8_STAGE(G8_SA(0, 0), a2, x00, x01);
;             G8_WAIT_V(8); G8_WAIT_L(0); G8_BAR; G8_MMA(1, 0, At, B0); G8_MMA(1, 1, At, B1); G8_BAR; G8_SCHED;
.LBB0_853:
	ds_read_b128 v[148:151], v153
	ds_read_b128 v[158:161], v153 offset:1024
	ds_read_b128 v[162:165], v153 offset:2048
	ds_read_b128 v[166:169], v153 offset:3072
	ds_read_b128 v[170:173], v154
	ds_read_b128 v[174:177], v154 offset:1024
	ds_read_b128 v[178:181], v154 offset:2048
	ds_read_b128 v[184:187], v154 offset:3072
	s_add_u32 s26, s20, 0x100
	s_addc_u32 s27, s21, 0
	s_cmp_eq_u32 vcc_lo, 2
	s_cselect_b32 s31, s15, s27
	s_cselect_b32 s30, s14, s26
	s_cselect_b32 s29, s17, s91
	s_cselect_b32 s28, s16, s0
	s_mov_b32 m0, s48
	v_lshl_add_u64 v[220:221], s[20:21], 0, v[144:145]
	ds_read_b128 v[188:191], v155
	ds_read_b128 v[192:195], v155 offset:1024
	ds_read_b128 v[196:199], v155 offset:2048
	ds_read_b128 v[200:203], v155 offset:3072
	ds_read_b128 v[204:207], v155 offset:4096
	ds_read_b128 v[208:211], v155 offset:5120
	ds_read_b128 v[212:215], v155 offset:6144
	ds_read_b128 v[216:219], v155 offset:7168
	global_load_lds_dwordx4 v[220:221], off
	v_lshl_add_u64 v[220:221], s[20:21], 0, v[146:147]
	s_mov_b32 m0, s49
	s_nop 0
	global_load_lds_dwordx4 v[220:221], off
	s_waitcnt vmcnt(8)
	s_waitcnt lgkmcnt(0)
	s_barrier
	s_setprio 1
	s_waitcnt lgkmcnt(0)
	v_mfma_f32_16x16x32_bf16 v[126:129], v[148:151], v[188:191], v[126:129]
	v_mfma_f32_16x16x32_bf16 v[122:125], v[162:165], v[188:191], v[122:125]
	v_mfma_f32_16x16x32_bf16 v[118:121], v[148:151], v[196:199], v[118:121]
	v_mfma_f32_16x16x32_bf16 v[110:113], v[162:165], v[196:199], v[110:113]
	v_mfma_f32_16x16x32_bf16 v[102:105], v[148:151], v[204:207], v[102:105]
	v_mfma_f32_16x16x32_bf16 v[94:97], v[162:165], v[204:207], v[94:97]
	v_mfma_f32_16x16x32_bf16 v[86:89], v[148:151], v[212:215], v[86:89]
	v_mfma_f32_16x16x32_bf16 v[78:81], v[162:165], v[212:215], v[78:81]
	v_mfma_f32_16x16x32_bf16 v[126:129], v[158:161], v[192:195], v[126:129]
	v_mfma_f32_16x16x32_bf16 v[122:125], v[166:169], v[192:195], v[122:125]
	v_mfma_f32_16x16x32_bf16 v[118:121], v[158:161], v[200:203], v[118:121]
	v_mfma_f32_16x16x32_bf16 v[110:113], v[166:169], v[200:203], v[110:113]
	v_mfma_f32_16x16x32_bf16 v[102:105], v[158:161], v[208:211], v[102:105]
	v_mfma_f32_16x16x32_bf16 v[94:97], v[166:169], v[208:211], v[94:97]
	v_mfma_f32_16x16x32_bf16 v[86:89], v[158:161], v[216:219], v[86:89]
	v_mfma_f32_16x16x32_bf16 v[78:81], v[166:169], v[216:219], v[78:81]
	v_mfma_f32_16x16x32_bf16 v[114:117], v[170:173], v[188:191], v[114:117]
	v_mfma_f32_16x16x32_bf16 v[106:109], v[178:181], v[188:191], v[106:109]
	v_mfma_f32_16x16x32_bf16 v[98:101], v[170:173], v[196:199], v[98:101]
	v_mfma_f32_16x16x32_bf16 v[90:93], v[178:181], v[196:199], v[90:93]
	v_mfma_f32_16x16x32_bf16 v[82:85], v[170:173], v[204:207], v[82:85]
	v_mfma_f32_16x16x32_bf16 v[74:77], v[178:181], v[204:207], v[74:77]
	v_mfma_f32_16x16x32_bf16 v[70:73], v[170:173], v[212:215], v[70:73]
	v_mfma_f32_16x16x32_bf16 v[66:69], v[178:181], v[212:215], v[66:69]
	v_mfma_f32_16x16x32_bf16 v[114:117], v[174:177], v[192:195], v[114:117]
	v_mfma_f32_16x16x32_bf16 v[106:109], v[184:187], v[192:195], v[106:109]
	v_mfma_f32_16x16x32_bf16 v[98:101], v[174:177], v[200:203], v[98:101]
	v_mfma_f32_16x16x32_bf16 v[90:93], v[184:187], v[200:203], v[90:93]
	v_mfma_f32_16x16x32_bf16 v[82:85], v[174:177], v[208:211], v[82:85]
	v_mfma_f32_16x16x32_bf16 v[74:77], v[184:187], v[208:211], v[74:77]
	v_mfma_f32_16x16x32_bf16 v[70:73], v[174:177], v[216:219], v[70:73]
	v_mfma_f32_16x16x32_bf16 v[66:69], v[184:187], v[216:219], v[66:69]
	s_setprio 0
	s_barrier
	s_mov_b32 m0, s52
	v_lshl_add_u64 v[220:221], s[28:29], 0, v[134:135]
	s_add_u32 s20, s28, 0x4000
	ds_read_b128 v[188:191], v155 offset:16384
	ds_read_b128 v[192:195], v155 offset:17408
	ds_read_b128 v[196:199], v155 offset:18432
	ds_read_b128 v[200:203], v155 offset:19456
	ds_read_b128 v[204:207], v155 offset:20480
	ds_read_b128 v[208:211], v155 offset:21504
	ds_read_b128 v[212:215], v155 offset:22528
	ds_read_b128 v[216:219], v155 offset:23552
	global_load_lds_dwordx4 v[220:221], off
	v_lshl_add_u64 v[220:221], s[28:29], 0, v[132:133]
	s_mov_b32 m0, s53
	s_addc_u32 s21, s29, 0
	global_load_lds_dwordx4 v[220:221], off
	v_lshl_add_u64 v[220:221], s[20:21], 0, v[134:135]
	s_mov_b32 m0, s54
	v_lshl_add_u64 v[222:223], s[30:31], 0, v[140:141]
	global_load_lds_dwordx4 v[220:221], off
	v_lshl_add_u64 v[220:221], s[20:21], 0, v[132:133]
	s_mov_b32 m0, s55
	s_nop 0
	global_load_lds_dwordx4 v[220:221], off
	v_lshl_add_u64 v[220:221], s[30:31], 0, v[136:137]
	s_mov_b32 m0, s35
	s_nop 0
	global_load_lds_dwordx4 v[220:221], off
	s_mov_b32 m0, s36
	s_nop 0
	global_load_lds_dwordx4 v[222:223], off
	s_waitcnt vmcnt(8)
	s_waitcnt lgkmcnt(0)
	s_barrier
; #define G8_STAGE(bufoff, gbase, v0, v1) do { \
;         __builtin_amdgcn_global_load_lds((const unsigned*)((const char*)(gbase) + (v0)), (LAS unsigned*)(lds + (bufoff) + ldsw), 16, 0, 0); \
;         __builtin_amdgcn_global_load_lds((const unsigned*)((const char*)(gbase) + (v1)), (LAS unsigned*)(lds + (bufoff) + ldsw + 8192), 16, 0, 0); } while (0)
; #define G8_LDA(dst, b, h) do { _Pragma("unroll") for (int m = 0; m < 4; ++m) _Pragma("unroll") for (int k = 0; k < 2; ++k) dst[m][k] = *(const LAS bf16x8*)(lds + G8_SA(b, h) + aoff + m * 2048 + k * 1024); } while (0)
; #define G8_LDB(dst, b, h) do { _Pragma("unroll") for (int n = 0; n < 2; ++n) _Pragma("unroll") for (int k = 0; k < 2; ++k) dst[n][k] = *(const LAS bf16x8*)(lds + G8_SB(b, h) + boff + n * 2048 + k * 1024); } while (0)
; #define G8_MMA(ai, bj, At, Bt) do { __builtin_amdgcn_s_setprio(1); _Pragma("unroll") for (int m = 0; m < 4; ++m) _Pragma("unroll") for (int n = 0; n < 2; ++n) _Pragma("unroll") for (int k = 0; k < 2; ++k) \
;         acc[ai][bj][m][n] = __builtin_amdgcn_mfma_f32_16x16x32_bf16(Bt[n][k], At[m][k], acc[ai][bj][m][n], 0, 0, 0); __builtin_amdgcn_s_setprio(0); } while (0)
; #define G8_WAIT_V(n) asm volatile("s_waitcnt vmcnt(" #n ")" ::: "memory")
; #define G8_WAIT_L(n) asm volatile("s_waitcnt lgkmcnt(" #n ")" ::: "memory")
; #define G8_BAR __builtin_amdgcn_s_barrier()
; #define G8_SCHED __builtin_amdgcn_sched_barrier(0)
; template <class Epi, class Sched, bool GATHER, bool ALIGN_EPI, bool PFB = false>
; __device__ __forceinline__ void gemm_phase(LAS unsigned char* lds, const int lda, const int K, const Sched& S, const Epi& E) {
;     ...
;             G8_WAIT_V(8); G8_WAIT_L(0); G8_BAR; G8_MMA(1, 0, At, B0); G8_MMA(1, 1, At, B1); G8_BAR; G8_SCHED;
;             G8_LDB(B0, 1, 0); G8_LDB(B1, 1, 1); G8_SCHED; G8_LDA(At, 1, 0); G8_STAGE(G8_SA(0, 1), a2, x10, x11);
;             G8_WAIT_V(8); G8_WAIT_L(0); G8_BAR; G8_MMA(0, 0, At, B0); G8_MMA(0, 1, At, B1); G8_BAR; G8_SCHED;
	s_setprio 1
	s_waitcnt lgkmcnt(0)
	v_mfma_f32_16x16x32_bf16 v[62:65], v[148:151], v[188:191], v[62:65]
	v_mfma_f32_16x16x32_bf16 v[58:61], v[162:165], v[188:191], v[58:61]
	v_mfma_f32_16x16x32_bf16 v[54:57], v[148:151], v[196:199], v[54:57]
	v_mfma_f32_16x16x32_bf16 v[46:49], v[162:165], v[196:199], v[46:49]
	v_mfma_f32_16x16x32_bf16 v[38:41], v[148:151], v[204:207], v[38:41]
	v_mfma_f32_16x16x32_bf16 v[30:33], v[162:165], v[204:207], v[30:33]
	v_mfma_f32_16x16x32_bf16 v[22:25], v[148:151], v[212:215], v[22:25]
	v_mfma_f32_16x16x32_bf16 v[14:17], v[162:165], v[212:215], v[14:17]
	v_mfma_f32_16x16x32_bf16 v[62:65], v[158:161], v[192:195], v[62:65]
	v_mfma_f32_16x16x32_bf16 v[58:61], v[166:169], v[192:195], v[58:61]
	v_mfma_f32_16x16x32_bf16 v[54:57], v[158:161], v[200:203], v[54:57]
	v_mfma_f32_16x16x32_bf16 v[46:49], v[166:169], v[200:203], v[46:49]
	v_mfma_f32_16x16x32_bf16 v[38:41], v[158:161], v[208:211], v[38:41]
	v_mfma_f32_16x16x32_bf16 v[30:33], v[166:169], v[208:211], v[30:33]
	v_mfma_f32_16x16x32_bf16 v[22:25], v[158:161], v[216:219], v[22:25]
	v_mfma_f32_16x16x32_bf16 v[14:17], v[166:169], v[216:219], v[14:17]
	v_mfma_f32_16x16x32_bf16 v[50:53], v[170:173], v[188:191], v[50:53]
	v_mfma_f32_16x16x32_bf16 v[42:45], v[178:181], v[188:191], v[42:45]
	v_mfma_f32_16x16x32_bf16 v[34:37], v[170:173], v[196:199], v[34:37]
	v_mfma_f32_16x16x32_bf16 v[26:29], v[178:181], v[196:199], v[26:29]
	v_mfma_f32_16x16x32_bf16 v[18:21], v[170:173], v[204:207], v[18:21]
	v_mfma_f32_16x16x32_bf16 v[10:13], v[178:181], v[204:207], v[10:13]
	v_mfma_f32_16x16x32_bf16 v[6:9], v[170:173], v[212:215], v[6:9]
	v_mfma_f32_16x16x32_bf16 v[2:5], v[178:181], v[212:215], v[2:5]
	v_mfma_f32_16x16x32_bf16 v[50:53], v[174:177], v[192:195], v[50:53]
	v_mfma_f32_16x16x32_bf16 v[42:45], v[184:187], v[192:195], v[42:45]
	v_mfma_f32_16x16x32_bf16 v[34:37], v[174:177], v[200:203], v[34:37]
	v_mfma_f32_16x16x32_bf16 v[26:29], v[184:187], v[200:203], v[26:29]
	v_mfma_f32_16x16x32_bf16 v[18:21], v[174:177], v[208:211], v[18:21]
	v_mfma_f32_16x16x32_bf16 v[10:13], v[184:187], v[208:211], v[10:13]
	v_mfma_f32_16x16x32_bf16 v[6:9], v[174:177], v[216:219], v[6:9]
	v_mfma_f32_16x16x32_bf16 v[2:5], v[184:187], v[216:219], v[2:5]
	s_setprio 0
	s_barrier
	ds_read_b128 v[148:151], v156
	ds_read_b128 v[158:161], v156 offset:1024
	ds_read_b128 v[162:165], v156 offset:2048
	ds_read_b128 v[166:169], v156 offset:3072
	ds_read_b128 v[170:173], v157
	ds_read_b128 v[174:177], v157 offset:1024
	ds_read_b128 v[178:181], v157 offset:2048
	ds_read_b128 v[184:187], v157 offset:3072
	s_mov_b32 m0, s37
	v_lshl_add_u64 v[224:225], s[30:31], 0, v[138:139]
	ds_read_b128 v[188:191], v155 offset:32768
	ds_read_b128 v[192:195], v155 offset:33792
	ds_read_b128 v[196:199], v155 offset:34816
	ds_read_b128 v[200:203], v155 offset:35840
	ds_read_b128 v[204:207], v155 offset:36864
	ds_read_b128 v[208:211], v155 offset:37888
	ds_read_b128 v[212:215], v155 offset:38912
	ds_read_b128 v[216:219], v155 offset:39936
	global_load_lds_dwordx4 v[224:225], off
	v_lshl_add_u64 v[224:225], s[30:31], 0, v[142:143]
	s_mov_b32 m0, s38
	s_nop 0
	global_load_lds_dwordx4 v[224:225], off
	s_waitcnt vmcnt(8)
	s_waitcnt lgkmcnt(0)
	s_barrier
	s_setprio 1
	s_waitcnt lgkmcnt(0)
	v_mfma_f32_16x16x32_bf16 v[126:129], v[148:151], v[188:191], v[126:129]
	v_mfma_f32_16x16x32_bf16 v[122:125], v[162:165], v[188:191], v[122:125]
	v_mfma_f32_16x16x32_bf16 v[118:121], v[148:151], v[196:199], v[118:121]
	v_mfma_f32_16x16x32_bf16 v[110:113], v[162:165], v[196:199], v[110:113]
	v_mfma_f32_16x16x32_bf16 v[102:105], v[148:151], v[204:207], v[102:105]
	v_mfma_f32_16x16x32_bf16 v[94:97], v[162:165], v[204:207], v[94:97]
	v_mfma_f32_16x16x32_bf16 v[86:89], v[148:151], v[212:215], v[86:89]
	v_mfma_f32_16x16x32_bf16 v[78:81], v[162:165], v[212:215], v[78:81]
	v_mfma_f32_16x16x32_bf16 v[126:129], v[158:161], v[192:195], v[126:129]
	v_mfma_f32_16x16x32_bf16 v[122:125], v[166:169], v[192:195], v[122:125]
	v_mfma_f32_16x16x32_bf16 v[118:121], v[158:161], v[200:203], v[118:121]
	v_mfma_f32_16x16x32_bf16 v[110:113], v[166:169], v[200:203], v[110:113]
	v_mfma_f32_16x16x32_bf16 v[102:105], v[158:161], v[208:211], v[102:105]
	v_mfma_f32_16x16x32_bf16 v[94:97], v[166:169], v[208:211], v[94:97]
	v_mfma_f32_16x16x32_bf16 v[86:89], v[158:161], v[216:219], v[86:89]
	v_mfma_f32_16x16x32_bf16 v[78:81], v[166:169], v[216:219], v[78:81]
	v_mfma_f32_16x16x32_bf16 v[114:117], v[170:173], v[188:191], v[114:117]
	v_mfma_f32_16x16x32_bf16 v[106:109], v[178:181], v[188:191], v[106:109]
	v_mfma_f32_16x16x32_bf16 v[98:101], v[170:173], v[196:199], v[98:101]
	v_mfma_f32_16x16x32_bf16 v[90:93], v[178:181], v[196:199], v[90:93]
	v_mfma_f32_16x16x32_bf16 v[82:85], v[170:173], v[204:207], v[82:85]
	v_mfma_f32_16x16x32_bf16 v[74:77], v[178:181], v[204:207], v[74:77]
	v_mfma_f32_16x16x32_bf16 v[70:73], v[170:173], v[212:215], v[70:73]
	v_mfma_f32_16x16x32_bf16 v[66:69], v[178:181], v[212:215], v[66:69]
	v_mfma_f32_16x16x32_bf16 v[114:117], v[174:177], v[192:195], v[114:117]
	v_mfma_f32_16x16x32_bf16 v[106:109], v[184:187], v[192:195], v[106:109]
	v_mfma_f32_16x16x32_bf16 v[98:101], v[174:177], v[200:203], v[98:101]
	v_mfma_f32_16x16x32_bf16 v[90:93], v[184:187], v[200:203], v[90:93]
	v_mfma_f32_16x16x32_bf16 v[82:85], v[174:177], v[208:211], v[82:85]
	v_mfma_f32_16x16x32_bf16 v[74:77], v[184:187], v[208:211], v[74:77]
	v_mfma_f32_16x16x32_bf16 v[70:73], v[174:177], v[216:219], v[70:73]
	v_mfma_f32_16x16x32_bf16 v[66:69], v[184:187], v[216:219], v[66:69]
	s_setprio 0
	s_barrier
; #define G8_STAGE(bufoff, gbase, v0, v1) do { \
;         __builtin_amdgcn_global_load_lds((const unsigned*)((const char*)(gbase) + (v0)), (LAS unsigned*)(lds + (bufoff) + ldsw), 16, 0, 0); \
;         __builtin_amdgcn_global_load_lds((const unsigned*)((const char*)(gbase) + (v1)), (LAS unsigned*)(lds + (bufoff) + ldsw + 8192), 16, 0, 0); } while (0)
; #define G8_LDA(dst, b, h) do { _Pragma("unroll") for (int m = 0; m < 4; ++m) _Pragma("unroll") for (int k = 0; k < 2; ++k) dst[m][k] = *(const LAS bf16x8*)(lds + G8_SA(b, h) + aoff + m * 2048 + k * 1024); } while (0)
; #define G8_MMA(ai, bj, At, Bt) do { __builtin_amdgcn_s_setprio(1); _Pragma("unroll") for (int m = 0; m < 4; ++m) _Pragma("unroll") for (int n = 0; n < 2; ++n) _Pragma("unroll") for (int k = 0; k < 2; ++k) \
;         acc[ai][bj][m][n] = __builtin_amdgcn_mfma_f32_16x16x32_bf16(Bt[n][k], At[m][k], acc[ai][bj][m][n], 0, 0, 0); __builtin_amdgcn_s_setprio(0); } while (0)
; #define G8_WAIT_V(n) asm volatile("s_waitcnt vmcnt(" #n ")" ::: "memory")
; #define G8_WAIT_L(n) asm volatile("s_waitcnt lgkmcnt(" #n ")" ::: "memory")
; #define G8_BAR __builtin_amdgcn_s_barrier()
; #define G8_SCHED __builtin_amdgcn_sched_barrier(0)
; template <class Epi, class Sched, bool GATHER, bool ALIGN_EPI, bool PFB = false>
; __device__ __forceinline__ void gemm_phase(LAS unsigned char* lds, const int lda, const int K, const Sched& S, const Epi& E) {
;     ...
;             G8_LDA(At, 1, 1); G8_STAGE(G8_SB(1, 0), b3, voffB[0], voffB[1]); G8_STAGE(G8_SB(1, 1), b3 + hstepB, voffB[0], voffB[1]); G8_STAGE(G8_SA(1, 0), a3, x00, x01);
;             G8_WAIT_V(8); G8_WAIT_L(0); G8_BAR; G8_MMA(1, 0, At, B0); G8_MMA(1, 1, At, B1); G8_BAR; G8_SCHED;
;         }
	s_add_u32 s20, s28, 0x8000
	s_addc_u32 s21, s29, 0
	s_mov_b32 m0, s56
	v_lshl_add_u64 v[224:225], s[20:21], 0, v[134:135]
	ds_read_b128 v[188:191], v155 offset:49152
	ds_read_b128 v[192:195], v155 offset:50176
	ds_read_b128 v[196:199], v155 offset:51200
	ds_read_b128 v[200:203], v155 offset:52224
	ds_read_b128 v[204:207], v155 offset:53248
	ds_read_b128 v[208:211], v155 offset:54272
	ds_read_b128 v[212:215], v155 offset:55296
	ds_read_b128 v[216:219], v155 offset:56320
	global_load_lds_dwordx4 v[224:225], off
	v_lshl_add_u64 v[224:225], s[20:21], 0, v[132:133]
	s_add_u32 s20, s28, 0xc000
	s_mov_b32 m0, s57
	s_addc_u32 s21, s29, 0
	global_load_lds_dwordx4 v[224:225], off
	v_lshl_add_u64 v[224:225], s[20:21], 0, v[134:135]
	s_mov_b32 m0, s60
	v_lshl_add_u64 v[220:221], v[220:221], 0, s[8:9]
	global_load_lds_dwordx4 v[224:225], off
	v_lshl_add_u64 v[224:225], s[20:21], 0, v[132:133]
	s_add_i32 m0, s60, 0x2000
	s_nop 0
	global_load_lds_dwordx4 v[224:225], off
	s_mov_b32 m0, s39
	s_nop 0
	global_load_lds_dwordx4 v[220:221], off
	v_lshl_add_u64 v[220:221], v[222:223], 0, s[8:9]
	s_mov_b32 m0, s44
	s_nop 0
	global_load_lds_dwordx4 v[220:221], off
	s_waitcnt vmcnt(8)
	s_waitcnt lgkmcnt(0)
	s_barrier
	s_setprio 1
	s_waitcnt lgkmcnt(0)
	v_mfma_f32_16x16x32_bf16 v[62:65], v[148:151], v[188:191], v[62:65]
	v_mfma_f32_16x16x32_bf16 v[58:61], v[162:165], v[188:191], v[58:61]
	v_mfma_f32_16x16x32_bf16 v[54:57], v[148:151], v[196:199], v[54:57]
	v_mfma_f32_16x16x32_bf16 v[46:49], v[162:165], v[196:199], v[46:49]
	v_mfma_f32_16x16x32_bf16 v[38:41], v[148:151], v[204:207], v[38:41]
	v_mfma_f32_16x16x32_bf16 v[30:33], v[162:165], v[204:207], v[30:33]
	v_mfma_f32_16x16x32_bf16 v[22:25], v[148:151], v[212:215], v[22:25]
	v_mfma_f32_16x16x32_bf16 v[14:17], v[162:165], v[212:215], v[14:17]
	v_mfma_f32_16x16x32_bf16 v[62:65], v[158:161], v[192:195], v[62:65]
	v_mfma_f32_16x16x32_bf16 v[58:61], v[166:169], v[192:195], v[58:61]
	v_mfma_f32_16x16x32_bf16 v[54:57], v[158:161], v[200:203], v[54:57]
	v_mfma_f32_16x16x32_bf16 v[46:49], v[166:169], v[200:203], v[46:49]
	v_mfma_f32_16x16x32_bf16 v[38:41], v[158:161], v[208:211], v[38:41]
	v_mfma_f32_16x16x32_bf16 v[30:33], v[166:169], v[208:211], v[30:33]
	v_mfma_f32_16x16x32_bf16 v[22:25], v[158:161], v[216:219], v[22:25]
	v_mfma_f32_16x16x32_bf16 v[14:17], v[166:169], v[216:219], v[14:17]
	v_mfma_f32_16x16x32_bf16 v[50:53], v[170:173], v[188:191], v[50:53]
	v_mfma_f32_16x16x32_bf16 v[42:45], v[178:181], v[188:191], v[42:45]
	v_mfma_f32_16x16x32_bf16 v[34:37], v[170:173], v[196:199], v[34:37]
	v_mfma_f32_16x16x32_bf16 v[26:29], v[178:181], v[196:199], v[26:29]
	v_mfma_f32_16x16x32_bf16 v[18:21], v[170:173], v[204:207], v[18:21]
	v_mfma_f32_16x16x32_bf16 v[10:13], v[178:181], v[204:207], v[10:13]
	v_mfma_f32_16x16x32_bf16 v[6:9], v[170:173], v[212:215], v[6:9]
	v_mfma_f32_16x16x32_bf16 v[2:5], v[178:181], v[212:215], v[2:5]
	v_mfma_f32_16x16x32_bf16 v[50:53], v[174:177], v[192:195], v[50:53]
	v_mfma_f32_16x16x32_bf16 v[42:45], v[184:187], v[192:195], v[42:45]
	v_mfma_f32_16x16x32_bf16 v[34:37], v[174:177], v[200:203], v[34:37]
	v_mfma_f32_16x16x32_bf16 v[26:29], v[184:187], v[200:203], v[26:29]
	v_mfma_f32_16x16x32_bf16 v[18:21], v[174:177], v[208:211], v[18:21]
	v_mfma_f32_16x16x32_bf16 v[10:13], v[184:187], v[208:211], v[10:13]
	v_mfma_f32_16x16x32_bf16 v[6:9], v[174:177], v[216:219], v[6:9]
	v_mfma_f32_16x16x32_bf16 v[2:5], v[184:187], v[216:219], v[2:5]
	s_setprio 0
	s_barrier
	s_add_i32 vcc_lo, vcc_lo, 2
	s_add_u32 s0, s0, 0x10000
	s_addc_u32 s91, s91, 0
	s_cmp_gt_u32 vcc_lo, 3
	s_mov_b64 s[20:21], s[26:27]
	s_cbranch_scc0 .LBB0_853
	s_and_b64 vcc, exec, s[10:11]
	s_cbranch_vccz .LBB0_856
	s_barrier

; #define G8_STAGE(bufoff, gbase, v0, v1) do { \
;         __builtin_amdgcn_global_load_lds((const unsigned*)((const char*)(gbase) + (v0)), (LAS unsigned*)(lds + (bufoff) + ldsw), 16, 0, 0); \
;         __builtin_amdgcn_global_load_lds((const unsigned*)((const char*)(gbase) + (v1)), (LAS unsigned*)(lds + (bufoff) + ldsw + 8192), 16, 0, 0); } while (0)
; #define G8_LDA(dst, b, h) do { _Pragma("unroll") for (int m = 0; m < 4; ++m) _Pragma("unroll") for (int k = 0; k < 2; ++k) dst[m][k] = *(const LAS bf16x8*)(lds + G8_SA(b, h) + aoff + m * 2048 + k * 1024); } while (0)
; #define G8_LDB(dst, b, h) do { _Pragma("unroll") for (int n = 0; n < 2; ++n) _Pragma("unroll") for (int k = 0; k < 2; ++k) dst[n][k] = *(const LAS bf16x8*)(lds + G8_SB(b, h) + boff + n * 2048 + k * 1024); } while (0)
; #define G8_MMA(ai, bj, At, Bt) do { __builtin_amdgcn_s_setprio(1); _Pragma("unroll") for (int m = 0; m < 4; ++m) _Pragma("unroll") for (int n = 0; n < 2; ++n) _Pragma("unroll") for (int k = 0; k < 2; ++k) \
;         acc[ai][bj][m][n] = __builtin_amdgcn_mfma_f32_16x16x32_bf16(Bt[n][k], At[m][k], acc[ai][bj][m][n], 0, 0, 0); __builtin_amdgcn_s_setprio(0); } while (0)
; #define G8_WAIT_V(n) asm volatile("s_waitcnt vmcnt(" #n ")" ::: "memory")
; #define G8_WAIT_L(n) asm volatile("s_waitcnt lgkmcnt(" #n ")" ::: "memory")
; #define G8_BAR __builtin_amdgcn_s_barrier()
; #define G8_SCHED __builtin_amdgcn_sched_barrier(0)
; template <class Epi, class Sched, bool GATHER, bool ALIGN_EPI, bool PFB = false>
; __device__ __forceinline__ void gemm_phase(LAS unsigned char* lds, const int lda, const int K, const Sched& S, const Epi& E) {
;     ...
;             G8_LDB(B0, 0, 0); G8_LDB(B1, 0, 1); G8_SCHED; G8_LDA(At, 0, 0); G8_STAGE(G8_SA(1, 1), a1, vA1[0], vA1[1]);
;             G8_WAIT_V(8); if (PFB) asm volatile("" : "+v"(pf_dummy)); G8_WAIT_L(0); G8_BAR; G8_MMA(0, 0, At, B0); G8_MMA(0, 1, At, B1); G8_BAR; G8_SCHED;
;             G8_LDA(At, 0, 1); G8_STAGE(G8_SB(0, 0), b2, voffB[0], voffB[1]); G8_STAGE(G8_SB(0, 1), b2 + hstepB, voffB[0], voffB[1]); G8_STAGE(G8_SA(0, 0), a2, x00, x01);
;             G8_WAIT_V(8); G8_WAIT_L(0); G8_BAR; G8_MMA(1, 0, At, B0); G8_MMA(1, 1, At, B1); G8_BAR; G8_SCHED;
.LBB0_1275:
	ds_read_b128 v[130:133], v191
	ds_read_b128 v[134:137], v191 offset:1024
	ds_read_b128 v[138:141], v191 offset:2048
	ds_read_b128 v[142:145], v191 offset:3072
	ds_read_b128 v[194:197], v192
	ds_read_b128 v[198:201], v192 offset:1024
	ds_read_b128 v[202:205], v192 offset:2048
	ds_read_b128 v[206:209], v192 offset:3072
	s_add_u32 s26, s24, 0x80
	s_addc_u32 s27, s25, 0
	s_cmp_eq_u32 s30, 12
	s_cselect_b32 s29, s19, s27
	s_cselect_b32 s28, s18, s26
	s_cselect_b32 s27, s21, s17
	s_cselect_b32 s26, s20, s15
	v_lshl_add_u64 v[186:187], s[24:25], 0, v[174:175]
	s_add_i32 m0, s37, 0xc000
	ds_read_b128 v[210:213], v193
	ds_read_b128 v[214:217], v193 offset:1024
	ds_read_b128 v[218:221], v193 offset:2048
	ds_read_b128 v[222:225], v193 offset:3072
	ds_read_b128 v[226:229], v193 offset:4096
	ds_read_b128 v[230:233], v193 offset:5120
	ds_read_b128 v[234:237], v193 offset:6144
	ds_read_b128 v[238:241], v193 offset:7168
	global_load_lds_dwordx4 v[186:187], off
	v_lshl_add_u64 v[186:187], s[24:25], 0, v[176:177]
	s_add_i32 m0, s37, 0xe000
	s_nop 0
	global_load_lds_dwordx4 v[186:187], off
	s_waitcnt vmcnt(8)
	s_waitcnt lgkmcnt(0)
	s_barrier
	s_setprio 1
	s_waitcnt lgkmcnt(0)
	v_mfma_f32_16x16x32_bf16 v[126:129], v[130:133], v[210:213], v[126:129]
	v_mfma_f32_16x16x32_bf16 v[122:125], v[138:141], v[210:213], v[122:125]
	v_mfma_f32_16x16x32_bf16 v[118:121], v[130:133], v[218:221], v[118:121]
	v_mfma_f32_16x16x32_bf16 v[110:113], v[138:141], v[218:221], v[110:113]
	v_mfma_f32_16x16x32_bf16 v[102:105], v[130:133], v[226:229], v[102:105]
	v_mfma_f32_16x16x32_bf16 v[94:97], v[138:141], v[226:229], v[94:97]
	v_mfma_f32_16x16x32_bf16 v[86:89], v[130:133], v[234:237], v[86:89]
	v_mfma_f32_16x16x32_bf16 v[78:81], v[138:141], v[234:237], v[78:81]
	v_mfma_f32_16x16x32_bf16 v[126:129], v[134:137], v[214:217], v[126:129]
	v_mfma_f32_16x16x32_bf16 v[122:125], v[142:145], v[214:217], v[122:125]
	v_mfma_f32_16x16x32_bf16 v[118:121], v[134:137], v[222:225], v[118:121]
	v_mfma_f32_16x16x32_bf16 v[110:113], v[142:145], v[222:225], v[110:113]
	v_mfma_f32_16x16x32_bf16 v[102:105], v[134:137], v[230:233], v[102:105]
	v_mfma_f32_16x16x32_bf16 v[94:97], v[142:145], v[230:233], v[94:97]
	v_mfma_f32_16x16x32_bf16 v[86:89], v[134:137], v[238:241], v[86:89]
	v_mfma_f32_16x16x32_bf16 v[78:81], v[142:145], v[238:241], v[78:81]
	v_mfma_f32_16x16x32_bf16 v[114:117], v[194:197], v[210:213], v[114:117]
	v_mfma_f32_16x16x32_bf16 v[106:109], v[202:205], v[210:213], v[106:109]
	v_mfma_f32_16x16x32_bf16 v[98:101], v[194:197], v[218:221], v[98:101]
	v_mfma_f32_16x16x32_bf16 v[90:93], v[202:205], v[218:221], v[90:93]
	v_mfma_f32_16x16x32_bf16 v[82:85], v[194:197], v[226:229], v[82:85]
	v_mfma_f32_16x16x32_bf16 v[74:77], v[202:205], v[226:229], v[74:77]
	v_mfma_f32_16x16x32_bf16 v[70:73], v[194:197], v[234:237], v[70:73]
	v_mfma_f32_16x16x32_bf16 v[66:69], v[202:205], v[234:237], v[66:69]
	v_mfma_f32_16x16x32_bf16 v[114:117], v[198:201], v[214:217], v[114:117]
	v_mfma_f32_16x16x32_bf16 v[106:109], v[206:209], v[214:217], v[106:109]
	v_mfma_f32_16x16x32_bf16 v[98:101], v[198:201], v[222:225], v[98:101]
	v_mfma_f32_16x16x32_bf16 v[90:93], v[206:209], v[222:225], v[90:93]
	v_mfma_f32_16x16x32_bf16 v[82:85], v[198:201], v[230:233], v[82:85]
	v_mfma_f32_16x16x32_bf16 v[74:77], v[206:209], v[230:233], v[74:77]
	v_mfma_f32_16x16x32_bf16 v[70:73], v[198:201], v[238:241], v[70:73]
	v_mfma_f32_16x16x32_bf16 v[66:69], v[206:209], v[238:241], v[66:69]
	s_setprio 0
	s_barrier
	s_add_i32 s31, s47, s35
	v_lshl_add_u64 v[186:187], s[26:27], 0, v[148:149]
	s_mov_b32 m0, s31
	ds_read_b128 v[210:213], v193 offset:16384
	ds_read_b128 v[214:217], v193 offset:17408
	ds_read_b128 v[218:221], v193 offset:18432
	ds_read_b128 v[222:225], v193 offset:19456
	ds_read_b128 v[226:229], v193 offset:20480
	ds_read_b128 v[230:233], v193 offset:21504
	ds_read_b128 v[234:237], v193 offset:22528
	ds_read_b128 v[238:241], v193 offset:23552
	global_load_lds_dwordx4 v[186:187], off
	s_add_i32 m0, s31, 0x2000
	s_add_u32 s50, s26, 0x4000
	v_lshl_add_u64 v[186:187], s[26:27], 0, v[146:147]
	s_addc_u32 s51, s27, 0
	s_add_i32 s31, s48, s35
	global_load_lds_dwordx4 v[186:187], off
	v_lshl_add_u64 v[186:187], s[50:51], 0, v[148:149]
	s_mov_b32 m0, s31
	v_lshl_add_u64 v[242:243], s[28:29], 0, v[154:155]
	global_load_lds_dwordx4 v[186:187], off
	v_lshl_add_u64 v[186:187], s[50:51], 0, v[146:147]
	s_add_i32 m0, s31, 0x2000
	s_nop 0
	global_load_lds_dwordx4 v[186:187], off
	v_lshl_add_u64 v[186:187], s[28:29], 0, v[150:151]
	s_mov_b32 m0, s37
	s_nop 0
	global_load_lds_dwordx4 v[186:187], off
	s_mov_b32 m0, s38
	s_nop 0
	global_load_lds_dwordx4 v[242:243], off
	s_waitcnt vmcnt(8)
	s_waitcnt lgkmcnt(0)
	s_barrier
; #define G8_STAGE(bufoff, gbase, v0, v1) do { \
;         __builtin_amdgcn_global_load_lds((const unsigned*)((const char*)(gbase) + (v0)), (LAS unsigned*)(lds + (bufoff) + ldsw), 16, 0, 0); \
;         __builtin_amdgcn_global_load_lds((const unsigned*)((const char*)(gbase) + (v1)), (LAS unsigned*)(lds + (bufoff) + ldsw + 8192), 16, 0, 0); } while (0)
; #define G8_LDA(dst, b, h) do { _Pragma("unroll") for (int m = 0; m < 4; ++m) _Pragma("unroll") for (int k = 0; k < 2; ++k) dst[m][k] = *(const LAS bf16x8*)(lds + G8_SA(b, h) + aoff + m * 2048 + k * 1024); } while (0)
; #define G8_LDB(dst, b, h) do { _Pragma("unroll") for (int n = 0; n < 2; ++n) _Pragma("unroll") for (int k = 0; k < 2; ++k) dst[n][k] = *(const LAS bf16x8*)(lds + G8_SB(b, h) + boff + n * 2048 + k * 1024); } while (0)
; #define G8_MMA(ai, bj, At, Bt) do { __builtin_amdgcn_s_setprio(1); _Pragma("unroll") for (int m = 0; m < 4; ++m) _Pragma("unroll") for (int n = 0; n < 2; ++n) _Pragma("unroll") for (int k = 0; k < 2; ++k) \
;         acc[ai][bj][m][n] = __builtin_amdgcn_mfma_f32_16x16x32_bf16(Bt[n][k], At[m][k], acc[ai][bj][m][n], 0, 0, 0); __builtin_amdgcn_s_setprio(0); } while (0)
; #define G8_WAIT_V(n) asm volatile("s_waitcnt vmcnt(" #n ")" ::: "memory")
; #define G8_WAIT_L(n) asm volatile("s_waitcnt lgkmcnt(" #n ")" ::: "memory")
; #define G8_BAR __builtin_amdgcn_s_barrier()
; #define G8_SCHED __builtin_amdgcn_sched_barrier(0)
; template <class Epi, class Sched, bool GATHER, bool ALIGN_EPI, bool PFB = false>
; __device__ __forceinline__ void gemm_phase(LAS unsigned char* lds, const int lda, const int K, const Sched& S, const Epi& E) {
;     ...
;             G8_WAIT_V(8); G8_WAIT_L(0); G8_BAR; G8_MMA(1, 0, At, B0); G8_MMA(1, 1, At, B1); G8_BAR; G8_SCHED;
;             G8_LDB(B0, 1, 0); G8_LDB(B1, 1, 1); G8_SCHED; G8_LDA(At, 1, 0); G8_STAGE(G8_SA(0, 1), a2, x10, x11);
;             G8_WAIT_V(8); G8_WAIT_L(0); G8_BAR; G8_MMA(0, 0, At, B0); G8_MMA(0, 1, At, B1); G8_BAR; G8_SCHED;
	s_setprio 1
	s_waitcnt lgkmcnt(0)
	v_mfma_f32_16x16x32_bf16 v[62:65], v[130:133], v[210:213], v[62:65]
	v_mfma_f32_16x16x32_bf16 v[58:61], v[138:141], v[210:213], v[58:61]
	v_mfma_f32_16x16x32_bf16 v[54:57], v[130:133], v[218:221], v[54:57]
	v_mfma_f32_16x16x32_bf16 v[46:49], v[138:141], v[218:221], v[46:49]
	v_mfma_f32_16x16x32_bf16 v[38:41], v[130:133], v[226:229], v[38:41]
	v_mfma_f32_16x16x32_bf16 v[30:33], v[138:141], v[226:229], v[30:33]
	v_mfma_f32_16x16x32_bf16 v[22:25], v[130:133], v[234:237], v[22:25]
	v_mfma_f32_16x16x32_bf16 v[14:17], v[138:141], v[234:237], v[14:17]
	v_mfma_f32_16x16x32_bf16 v[62:65], v[134:137], v[214:217], v[62:65]
	v_mfma_f32_16x16x32_bf16 v[58:61], v[142:145], v[214:217], v[58:61]
	v_mfma_f32_16x16x32_bf16 v[54:57], v[134:137], v[222:225], v[54:57]
	v_mfma_f32_16x16x32_bf16 v[46:49], v[142:145], v[222:225], v[46:49]
	v_mfma_f32_16x16x32_bf16 v[38:41], v[134:137], v[230:233], v[38:41]
	v_mfma_f32_16x16x32_bf16 v[30:33], v[142:145], v[230:233], v[30:33]
	v_mfma_f32_16x16x32_bf16 v[22:25], v[134:137], v[238:241], v[22:25]
	v_mfma_f32_16x16x32_bf16 v[14:17], v[142:145], v[238:241], v[14:17]
	v_mfma_f32_16x16x32_bf16 v[50:53], v[194:197], v[210:213], v[50:53]
	v_mfma_f32_16x16x32_bf16 v[42:45], v[202:205], v[210:213], v[42:45]
	v_mfma_f32_16x16x32_bf16 v[34:37], v[194:197], v[218:221], v[34:37]
	v_mfma_f32_16x16x32_bf16 v[26:29], v[202:205], v[218:221], v[26:29]
	v_mfma_f32_16x16x32_bf16 v[18:21], v[194:197], v[226:229], v[18:21]
	v_mfma_f32_16x16x32_bf16 v[10:13], v[202:205], v[226:229], v[10:13]
	v_mfma_f32_16x16x32_bf16 v[6:9], v[194:197], v[234:237], v[6:9]
	v_mfma_f32_16x16x32_bf16 v[2:5], v[202:205], v[234:237], v[2:5]
	v_mfma_f32_16x16x32_bf16 v[50:53], v[198:201], v[214:217], v[50:53]
	v_mfma_f32_16x16x32_bf16 v[42:45], v[206:209], v[214:217], v[42:45]
	v_mfma_f32_16x16x32_bf16 v[34:37], v[198:201], v[222:225], v[34:37]
	v_mfma_f32_16x16x32_bf16 v[26:29], v[206:209], v[222:225], v[26:29]
	v_mfma_f32_16x16x32_bf16 v[18:21], v[198:201], v[230:233], v[18:21]
	v_mfma_f32_16x16x32_bf16 v[10:13], v[206:209], v[230:233], v[10:13]
	v_mfma_f32_16x16x32_bf16 v[6:9], v[198:201], v[238:241], v[6:9]
	v_mfma_f32_16x16x32_bf16 v[2:5], v[206:209], v[238:241], v[2:5]
	s_setprio 0
	s_barrier
	s_add_i32 s31, 0, 0x18000
	s_add_i32 s33, 0, 0x1c000
	v_add_u32_e32 v142, s31, v189
	v_add_u32_e32 v206, s33, v189
	ds_read_b128 v[130:133], v142
	ds_read_b128 v[134:137], v142 offset:1024
	ds_read_b128 v[138:141], v142 offset:2048
	ds_read_b128 v[142:145], v142 offset:3072
	ds_read_b128 v[194:197], v206
	ds_read_b128 v[198:201], v206 offset:1024
	ds_read_b128 v[202:205], v206 offset:2048
	ds_read_b128 v[206:209], v206 offset:3072
	s_mov_b32 m0, s39
	v_lshl_add_u64 v[244:245], s[28:29], 0, v[152:153]
	ds_read_b128 v[210:213], v193 offset:32768
	ds_read_b128 v[214:217], v193 offset:33792
	ds_read_b128 v[218:221], v193 offset:34816
	ds_read_b128 v[222:225], v193 offset:35840
	ds_read_b128 v[226:229], v193 offset:36864
	ds_read_b128 v[230:233], v193 offset:37888
	ds_read_b128 v[234:237], v193 offset:38912
	ds_read_b128 v[238:241], v193 offset:39936
	global_load_lds_dwordx4 v[244:245], off
	v_lshl_add_u64 v[244:245], s[28:29], 0, v[156:157]
	s_mov_b32 m0, s40
	s_nop 0
	global_load_lds_dwordx4 v[244:245], off
	s_waitcnt vmcnt(8)
	s_waitcnt lgkmcnt(0)
	s_barrier
	s_setprio 1
	s_waitcnt lgkmcnt(0)
	v_mfma_f32_16x16x32_bf16 v[126:129], v[130:133], v[210:213], v[126:129]
	v_mfma_f32_16x16x32_bf16 v[122:125], v[138:141], v[210:213], v[122:125]
	v_mfma_f32_16x16x32_bf16 v[118:121], v[130:133], v[218:221], v[118:121]
	v_mfma_f32_16x16x32_bf16 v[110:113], v[138:141], v[218:221], v[110:113]
	v_mfma_f32_16x16x32_bf16 v[102:105], v[130:133], v[226:229], v[102:105]
	v_mfma_f32_16x16x32_bf16 v[94:97], v[138:141], v[226:229], v[94:97]
	v_mfma_f32_16x16x32_bf16 v[86:89], v[130:133], v[234:237], v[86:89]
	v_mfma_f32_16x16x32_bf16 v[78:81], v[138:141], v[234:237], v[78:81]
	v_mfma_f32_16x16x32_bf16 v[126:129], v[134:137], v[214:217], v[126:129]
	v_mfma_f32_16x16x32_bf16 v[122:125], v[142:145], v[214:217], v[122:125]
	v_mfma_f32_16x16x32_bf16 v[118:121], v[134:137], v[222:225], v[118:121]
	v_mfma_f32_16x16x32_bf16 v[110:113], v[142:145], v[222:225], v[110:113]
	v_mfma_f32_16x16x32_bf16 v[102:105], v[134:137], v[230:233], v[102:105]
	v_mfma_f32_16x16x32_bf16 v[94:97], v[142:145], v[230:233], v[94:97]
	v_mfma_f32_16x16x32_bf16 v[86:89], v[134:137], v[238:241], v[86:89]
	v_mfma_f32_16x16x32_bf16 v[78:81], v[142:145], v[238:241], v[78:81]
	v_mfma_f32_16x16x32_bf16 v[114:117], v[194:197], v[210:213], v[114:117]
	v_mfma_f32_16x16x32_bf16 v[106:109], v[202:205], v[210:213], v[106:109]
	v_mfma_f32_16x16x32_bf16 v[98:101], v[194:197], v[218:221], v[98:101]
	v_mfma_f32_16x16x32_bf16 v[90:93], v[202:205], v[218:221], v[90:93]
	v_mfma_f32_16x16x32_bf16 v[82:85], v[194:197], v[226:229], v[82:85]
	v_mfma_f32_16x16x32_bf16 v[74:77], v[202:205], v[226:229], v[74:77]
	v_mfma_f32_16x16x32_bf16 v[70:73], v[194:197], v[234:237], v[70:73]
	v_mfma_f32_16x16x32_bf16 v[66:69], v[202:205], v[234:237], v[66:69]
	v_mfma_f32_16x16x32_bf16 v[114:117], v[198:201], v[214:217], v[114:117]
	v_mfma_f32_16x16x32_bf16 v[106:109], v[206:209], v[214:217], v[106:109]
	v_mfma_f32_16x16x32_bf16 v[98:101], v[198:201], v[222:225], v[98:101]
	v_mfma_f32_16x16x32_bf16 v[90:93], v[206:209], v[222:225], v[90:93]
	v_mfma_f32_16x16x32_bf16 v[82:85], v[198:201], v[230:233], v[82:85]
	v_mfma_f32_16x16x32_bf16 v[74:77], v[206:209], v[230:233], v[74:77]
	v_mfma_f32_16x16x32_bf16 v[70:73], v[198:201], v[238:241], v[70:73]
	v_mfma_f32_16x16x32_bf16 v[66:69], v[206:209], v[238:241], v[66:69]
	s_setprio 0
	s_barrier
; #define G8_STAGE(bufoff, gbase, v0, v1) do { \
;         __builtin_amdgcn_global_load_lds((const unsigned*)((const char*)(gbase) + (v0)), (LAS unsigned*)(lds + (bufoff) + ldsw), 16, 0, 0); \
;         __builtin_amdgcn_global_load_lds((const unsigned*)((const char*)(gbase) + (v1)), (LAS unsigned*)(lds + (bufoff) + ldsw + 8192), 16, 0, 0); } while (0)
; #define G8_LDA(dst, b, h) do { _Pragma("unroll") for (int m = 0; m < 4; ++m) _Pragma("unroll") for (int k = 0; k < 2; ++k) dst[m][k] = *(const LAS bf16x8*)(lds + G8_SA(b, h) + aoff + m * 2048 + k * 1024); } while (0)
; #define G8_MMA(ai, bj, At, Bt) do { __builtin_amdgcn_s_setprio(1); _Pragma("unroll") for (int m = 0; m < 4; ++m) _Pragma("unroll") for (int n = 0; n < 2; ++n) _Pragma("unroll") for (int k = 0; k < 2; ++k) \
;         acc[ai][bj][m][n] = __builtin_amdgcn_mfma_f32_16x16x32_bf16(Bt[n][k], At[m][k], acc[ai][bj][m][n], 0, 0, 0); __builtin_amdgcn_s_setprio(0); } while (0)
; #define G8_WAIT_V(n) asm volatile("s_waitcnt vmcnt(" #n ")" ::: "memory")
; #define G8_WAIT_L(n) asm volatile("s_waitcnt lgkmcnt(" #n ")" ::: "memory")
; #define G8_BAR __builtin_amdgcn_s_barrier()
; #define G8_SCHED __builtin_amdgcn_sched_barrier(0)
; template <class Epi, class Sched, bool GATHER, bool ALIGN_EPI, bool PFB = false>
; __device__ __forceinline__ void gemm_phase(LAS unsigned char* lds, const int lda, const int K, const Sched& S, const Epi& E) {
;     ...
;             G8_LDA(At, 1, 1); G8_STAGE(G8_SB(1, 0), b3, voffB[0], voffB[1]); G8_STAGE(G8_SB(1, 1), b3 + hstepB, voffB[0], voffB[1]); G8_STAGE(G8_SA(1, 0), a3, x00, x01);
;             G8_WAIT_V(8); G8_WAIT_L(0); G8_BAR; G8_MMA(1, 0, At, B0); G8_MMA(1, 1, At, B1); G8_BAR; G8_SCHED;
;         }
	s_add_u32 s28, s26, 0x8000
	s_addc_u32 s29, s27, 0
	s_add_i32 s31, s31, s35
	v_lshl_add_u64 v[244:245], s[28:29], 0, v[148:149]
	s_mov_b32 m0, s31
	ds_read_b128 v[210:213], v193 offset:49152
	ds_read_b128 v[214:217], v193 offset:50176
	ds_read_b128 v[218:221], v193 offset:51200
	ds_read_b128 v[222:225], v193 offset:52224
	ds_read_b128 v[226:229], v193 offset:53248
	ds_read_b128 v[230:233], v193 offset:54272
	ds_read_b128 v[234:237], v193 offset:55296
	ds_read_b128 v[238:241], v193 offset:56320
	global_load_lds_dwordx4 v[244:245], off
	s_add_i32 m0, s31, 0x2000
	s_add_u32 s26, s26, 0xc000
	v_lshl_add_u64 v[244:245], s[28:29], 0, v[146:147]
	s_addc_u32 s27, s27, 0
	s_add_i32 s28, s33, s35
	global_load_lds_dwordx4 v[244:245], off
	v_lshl_add_u64 v[244:245], s[26:27], 0, v[148:149]
	s_mov_b32 m0, s28
	v_lshl_add_u64 v[186:187], v[186:187], 0, s[8:9]
	global_load_lds_dwordx4 v[244:245], off
	v_lshl_add_u64 v[244:245], s[26:27], 0, v[146:147]
	s_add_i32 m0, s28, 0x2000
	s_nop 0
	global_load_lds_dwordx4 v[244:245], off
	s_mov_b32 m0, s42
	s_nop 0
	global_load_lds_dwordx4 v[186:187], off
	v_lshl_add_u64 v[186:187], v[242:243], 0, s[8:9]
	s_mov_b32 m0, s43
	s_nop 0
	global_load_lds_dwordx4 v[186:187], off
	s_waitcnt vmcnt(8)
	s_waitcnt lgkmcnt(0)
	s_barrier
	s_setprio 1
	s_waitcnt lgkmcnt(0)
	v_mfma_f32_16x16x32_bf16 v[62:65], v[130:133], v[210:213], v[62:65]
	v_mfma_f32_16x16x32_bf16 v[58:61], v[138:141], v[210:213], v[58:61]
	v_mfma_f32_16x16x32_bf16 v[54:57], v[130:133], v[218:221], v[54:57]
	v_mfma_f32_16x16x32_bf16 v[46:49], v[138:141], v[218:221], v[46:49]
	v_mfma_f32_16x16x32_bf16 v[38:41], v[130:133], v[226:229], v[38:41]
	v_mfma_f32_16x16x32_bf16 v[30:33], v[138:141], v[226:229], v[30:33]
	v_mfma_f32_16x16x32_bf16 v[22:25], v[130:133], v[234:237], v[22:25]
	v_mfma_f32_16x16x32_bf16 v[14:17], v[138:141], v[234:237], v[14:17]
	v_mfma_f32_16x16x32_bf16 v[62:65], v[134:137], v[214:217], v[62:65]
	v_mfma_f32_16x16x32_bf16 v[58:61], v[142:145], v[214:217], v[58:61]
	v_mfma_f32_16x16x32_bf16 v[54:57], v[134:137], v[222:225], v[54:57]
	v_mfma_f32_16x16x32_bf16 v[46:49], v[142:145], v[222:225], v[46:49]
	v_mfma_f32_16x16x32_bf16 v[38:41], v[134:137], v[230:233], v[38:41]
	v_mfma_f32_16x16x32_bf16 v[30:33], v[142:145], v[230:233], v[30:33]
	v_mfma_f32_16x16x32_bf16 v[22:25], v[134:137], v[238:241], v[22:25]
	v_mfma_f32_16x16x32_bf16 v[14:17], v[142:145], v[238:241], v[14:17]
	v_mfma_f32_16x16x32_bf16 v[50:53], v[194:197], v[210:213], v[50:53]
	v_mfma_f32_16x16x32_bf16 v[42:45], v[202:205], v[210:213], v[42:45]
	v_mfma_f32_16x16x32_bf16 v[34:37], v[194:197], v[218:221], v[34:37]
	v_mfma_f32_16x16x32_bf16 v[26:29], v[202:205], v[218:221], v[26:29]
	v_mfma_f32_16x16x32_bf16 v[18:21], v[194:197], v[226:229], v[18:21]
	v_mfma_f32_16x16x32_bf16 v[10:13], v[202:205], v[226:229], v[10:13]
	v_mfma_f32_16x16x32_bf16 v[6:9], v[194:197], v[234:237], v[6:9]
	v_mfma_f32_16x16x32_bf16 v[2:5], v[202:205], v[234:237], v[2:5]
	v_mfma_f32_16x16x32_bf16 v[50:53], v[198:201], v[214:217], v[50:53]
	v_mfma_f32_16x16x32_bf16 v[42:45], v[206:209], v[214:217], v[42:45]
	v_mfma_f32_16x16x32_bf16 v[34:37], v[198:201], v[222:225], v[34:37]
	v_mfma_f32_16x16x32_bf16 v[26:29], v[206:209], v[222:225], v[26:29]
	v_mfma_f32_16x16x32_bf16 v[18:21], v[198:201], v[230:233], v[18:21]
	v_mfma_f32_16x16x32_bf16 v[10:13], v[206:209], v[230:233], v[10:13]
	v_mfma_f32_16x16x32_bf16 v[6:9], v[198:201], v[238:241], v[6:9]
	v_mfma_f32_16x16x32_bf16 v[2:5], v[206:209], v[238:241], v[2:5]
	s_setprio 0
	s_barrier
	s_add_i32 s30, s30, 2
	s_add_u32 s15, s15, 0x10000
	s_addc_u32 s17, s17, 0
	s_add_u32 s24, s24, 0x100
	s_addc_u32 s25, s25, 0
	s_cmp_gt_u32 s30, 13
	s_cbranch_scc0 .LBB0_1275
	s_and_b64 vcc, exec, s[10:11]
	s_cbranch_vccz .LBB0_1278
	s_barrier

; #define G8_STAGE(bufoff, gbase, v0, v1) do { \
;         __builtin_amdgcn_global_load_lds((const unsigned*)((const char*)(gbase) + (v0)), (LAS unsigned*)(lds + (bufoff) + ldsw), 16, 0, 0); \
;         __builtin_amdgcn_global_load_lds((const unsigned*)((const char*)(gbase) + (v1)), (LAS unsigned*)(lds + (bufoff) + ldsw + 8192), 16, 0, 0); } while (0)
; #define G8_LDA(dst, b, h) do { _Pragma("unroll") for (int m = 0; m < 4; ++m) _Pragma("unroll") for (int k = 0; k < 2; ++k) dst[m][k] = *(const LAS bf16x8*)(lds + G8_SA(b, h) + aoff + m * 2048 + k * 1024); } while (0)
; #define G8_LDB(dst, b, h) do { _Pragma("unroll") for (int n = 0; n < 2; ++n) _Pragma("unroll") for (int k = 0; k < 2; ++k) dst[n][k] = *(const LAS bf16x8*)(lds + G8_SB(b, h) + boff + n * 2048 + k * 1024); } while (0)
; #define G8_WAIT_V(n) asm volatile("s_waitcnt vmcnt(" #n ")" ::: "memory")
; #define G8_WAIT_L(n) asm volatile("s_waitcnt lgkmcnt(" #n ")" ::: "memory")
; #define G8_BAR __builtin_amdgcn_s_barrier()
; template <class Epi, class Sched, bool GATHER, bool ALIGN_EPI, bool PFB = false>
; __device__ __forceinline__ void gemm_phase(LAS unsigned char* lds, const int lda, const int K, const Sched& S, const Epi& E) {
;     ...
;         for (int t = 0; t < nt; t += 2) {
;             const bool last = (t == nt - 2);
;             const char* a1 = cA + (size_t)(t + 1) * kstep;
;             const char* a2 = last ? nA : cA + (size_t)(t + 2) * kstep; const char* b2 = last ? nB : cB + (size_t)(t + 2) * kstepB;
;             const char* a3 = a2 + kstep; const char* b3 = b2 + kstepB;
;             unsigned x00 = vA0[0], x01 = vA0[1], x10 = vA1[0], x11 = vA1[1];
;             if (GATHER) { x00 = last ? nA0[0] : vA0[0]; x01 = last ? nA0[1] : vA0[1]; x10 = last ? nA1[0] : vA1[0]; x11 = last ? nA1[1] : vA1[1]; }
;             G8_LDB(B0, 0, 0); G8_LDB(B1, 0, 1); G8_SCHED; G8_LDA(At, 0, 0); G8_STAGE(G8_SA(1, 1), a1, vA1[0], vA1[1]);
;             G8_WAIT_V(8); if (PFB) asm volatile("" : "+v"(pf_dummy)); G8_WAIT_L(0); G8_BAR; G8_MMA(0, 0, At, B0); G8_MMA(0, 1, At, B1); G8_BAR; G8_SCHED;
;             G8_LDA(At, 0, 1); G8_STAGE(G8_SB(0, 0), b2, voffB[0], voffB[1]); G8_STAGE(G8_SB(0, 1), b2 + hstepB, voffB[0], voffB[1]); G8_STAGE(G8_SA(0, 0), a2, x00, x01);
;             G8_WAIT_V(8); G8_WAIT_L(0); G8_BAR; G8_MMA(1, 0, At, B0); G8_MMA(1, 1, At, B1); G8_BAR; G8_SCHED;
.LBB0_1504:
	s_add_u32 s22, s78, s0
	s_addc_u32 s23, s79, s1
	s_add_u32 s24, s22, 0x1944e100
	ds_read_b128 v[166:169], v156
	ds_read_b128 v[170:173], v156 offset:1024
	ds_read_b128 v[174:177], v156 offset:2048
	ds_read_b128 v[178:181], v156 offset:3072
	ds_read_b128 v[186:189], v157
	ds_read_b128 v[190:193], v157 offset:1024
	ds_read_b128 v[194:197], v157 offset:2048
	ds_read_b128 v[198:201], v157 offset:3072
	s_addc_u32 s25, s23, 0
	s_cmpk_eq_i32 s0, 0x700
	s_cselect_b64 vcc, -1, 0
	s_and_b64 s[22:23], vcc, exec
	s_cselect_b32 s22, s18, s21
	s_cselect_b32 s27, s59, s25
	s_cselect_b32 s26, s58, s24
	s_cselect_b32 s23, s19, s52
	s_add_u32 s24, s22, 0x8000
	v_cndmask_b32_e32 v142, v99, v144, vcc
	v_cndmask_b32_e32 v101, v100, v161, vcc
	v_cndmask_b32_e32 v234, v98, v162, vcc
	s_addc_u32 s25, s23, 0
	v_lshl_add_u64 v[236:237], v[146:147], 0, s[0:1]
	s_add_i32 m0, s31, 0xc000
	ds_read_b128 v[202:205], v158
	ds_read_b128 v[206:209], v158 offset:1024
	ds_read_b128 v[210:213], v158 offset:2048
	ds_read_b128 v[214:217], v158 offset:3072
	ds_read_b128 v[218:221], v158 offset:4096
	ds_read_b128 v[222:225], v158 offset:5120
	ds_read_b128 v[226:229], v158 offset:6144
	ds_read_b128 v[230:233], v158 offset:7168
	global_load_lds_dwordx4 v[236:237], off
	v_lshl_add_u64 v[236:237], v[108:109], 0, s[0:1]
	s_add_i32 m0, s31, 0xe000
	s_nop 0
	global_load_lds_dwordx4 v[236:237], off
	s_waitcnt vmcnt(8)
	s_waitcnt lgkmcnt(0)
	s_barrier
	s_setprio 1
	s_waitcnt lgkmcnt(0)
	v_mfma_f32_16x16x32_bf16 v[134:137], v[166:169], v[202:205], v[134:137]
	v_mfma_f32_16x16x32_bf16 v[130:133], v[174:177], v[202:205], v[130:133]
	v_mfma_f32_16x16x32_bf16 v[126:129], v[166:169], v[210:213], v[126:129]
	v_mfma_f32_16x16x32_bf16 v[110:113], v[174:177], v[210:213], v[110:113]
	v_mfma_f32_16x16x32_bf16 v[94:97], v[166:169], v[218:221], v[94:97]
	v_mfma_f32_16x16x32_bf16 v[86:89], v[174:177], v[218:221], v[86:89]
	v_mfma_f32_16x16x32_bf16 v[78:81], v[166:169], v[226:229], v[78:81]
	v_mfma_f32_16x16x32_bf16 v[70:73], v[174:177], v[226:229], v[70:73]
	v_mfma_f32_16x16x32_bf16 v[134:137], v[170:173], v[206:209], v[134:137]
	v_mfma_f32_16x16x32_bf16 v[130:133], v[178:181], v[206:209], v[130:133]
	v_mfma_f32_16x16x32_bf16 v[126:129], v[170:173], v[214:217], v[126:129]
	v_mfma_f32_16x16x32_bf16 v[110:113], v[178:181], v[214:217], v[110:113]
	v_mfma_f32_16x16x32_bf16 v[94:97], v[170:173], v[222:225], v[94:97]
	v_mfma_f32_16x16x32_bf16 v[86:89], v[178:181], v[222:225], v[86:89]
	v_mfma_f32_16x16x32_bf16 v[78:81], v[170:173], v[230:233], v[78:81]
	v_mfma_f32_16x16x32_bf16 v[70:73], v[178:181], v[230:233], v[70:73]
	v_mfma_f32_16x16x32_bf16 v[122:125], v[186:189], v[202:205], v[122:125]
	v_mfma_f32_16x16x32_bf16 v[118:121], v[194:197], v[202:205], v[118:121]
	v_mfma_f32_16x16x32_bf16 v[114:117], v[186:189], v[210:213], v[114:117]
	v_mfma_f32_16x16x32_bf16 v[102:105], v[194:197], v[210:213], v[102:105]
	v_mfma_f32_16x16x32_bf16 v[90:93], v[186:189], v[218:221], v[90:93]
	v_mfma_f32_16x16x32_bf16 v[82:85], v[194:197], v[218:221], v[82:85]
	v_mfma_f32_16x16x32_bf16 v[74:77], v[186:189], v[226:229], v[74:77]
	v_mfma_f32_16x16x32_bf16 v[66:69], v[194:197], v[226:229], v[66:69]
	v_mfma_f32_16x16x32_bf16 v[122:125], v[190:193], v[206:209], v[122:125]
	v_mfma_f32_16x16x32_bf16 v[118:121], v[198:201], v[206:209], v[118:121]
	v_mfma_f32_16x16x32_bf16 v[114:117], v[190:193], v[214:217], v[114:117]
	v_mfma_f32_16x16x32_bf16 v[102:105], v[198:201], v[214:217], v[102:105]
	v_mfma_f32_16x16x32_bf16 v[90:93], v[190:193], v[222:225], v[90:93]
	v_mfma_f32_16x16x32_bf16 v[82:85], v[198:201], v[222:225], v[82:85]
	v_mfma_f32_16x16x32_bf16 v[74:77], v[190:193], v[230:233], v[74:77]
	v_mfma_f32_16x16x32_bf16 v[66:69], v[198:201], v[230:233], v[66:69]
	s_setprio 0
	s_barrier
	s_add_i32 s33, s40, s3
	v_lshl_add_u64 v[236:237], s[22:23], 0, v[138:139]
	s_mov_b32 m0, s33
	ds_read_b128 v[202:205], v158 offset:16384
	ds_read_b128 v[206:209], v158 offset:17408
	ds_read_b128 v[210:213], v158 offset:18432
	ds_read_b128 v[214:217], v158 offset:19456
	ds_read_b128 v[218:221], v158 offset:20480
	ds_read_b128 v[222:225], v158 offset:21504
	ds_read_b128 v[226:229], v158 offset:22528
	ds_read_b128 v[230:233], v158 offset:23552
	global_load_lds_dwordx4 v[236:237], off
	s_add_i32 m0, s33, 0x2000
	s_add_u32 s54, s22, 0x4000
	v_lshl_add_u64 v[236:237], s[22:23], 0, v[140:141]
	s_addc_u32 s55, s23, 0
	s_add_i32 s33, s41, s3
	global_load_lds_dwordx4 v[236:237], off
	v_lshl_add_u64 v[236:237], s[54:55], 0, v[138:139]
	s_mov_b32 m0, s33
	v_mov_b32_e32 v235, v143
	global_load_lds_dwordx4 v[236:237], off
	v_lshl_add_u64 v[236:237], s[54:55], 0, v[140:141]
	s_add_i32 m0, s33, 0x2000
	s_nop 0
	global_load_lds_dwordx4 v[236:237], off
	s_mov_b32 m0, s31
	v_lshl_add_u64 v[236:237], s[26:27], 0, v[142:143]
	global_load_lds_dwordx4 v142, s[26:27]
	s_mov_b32 m0, s34
	s_nop 0
	global_load_lds_dwordx4 v234, s[26:27]
	s_waitcnt vmcnt(8)
	s_waitcnt lgkmcnt(0)
	v_lshl_add_u64 v[234:235], s[26:27], 0, v[234:235]
	s_barrier
; #define G8_STAGE(bufoff, gbase, v0, v1) do { \
;         __builtin_amdgcn_global_load_lds((const unsigned*)((const char*)(gbase) + (v0)), (LAS unsigned*)(lds + (bufoff) + ldsw), 16, 0, 0); \
;         __builtin_amdgcn_global_load_lds((const unsigned*)((const char*)(gbase) + (v1)), (LAS unsigned*)(lds + (bufoff) + ldsw + 8192), 16, 0, 0); } while (0)
; #define G8_LDA(dst, b, h) do { _Pragma("unroll") for (int m = 0; m < 4; ++m) _Pragma("unroll") for (int k = 0; k < 2; ++k) dst[m][k] = *(const LAS bf16x8*)(lds + G8_SA(b, h) + aoff + m * 2048 + k * 1024); } while (0)
; #define G8_LDB(dst, b, h) do { _Pragma("unroll") for (int n = 0; n < 2; ++n) _Pragma("unroll") for (int k = 0; k < 2; ++k) dst[n][k] = *(const LAS bf16x8*)(lds + G8_SB(b, h) + boff + n * 2048 + k * 1024); } while (0)
; #define G8_MMA(ai, bj, At, Bt) do { __builtin_amdgcn_s_setprio(1); _Pragma("unroll") for (int m = 0; m < 4; ++m) _Pragma("unroll") for (int n = 0; n < 2; ++n) _Pragma("unroll") for (int k = 0; k < 2; ++k) \
;         acc[ai][bj][m][n] = __builtin_amdgcn_mfma_f32_16x16x32_bf16(Bt[n][k], At[m][k], acc[ai][bj][m][n], 0, 0, 0); __builtin_amdgcn_s_setprio(0); } while (0)
; #define G8_WAIT_V(n) asm volatile("s_waitcnt vmcnt(" #n ")" ::: "memory")
; #define G8_WAIT_L(n) asm volatile("s_waitcnt lgkmcnt(" #n ")" ::: "memory")
; #define G8_BAR __builtin_amdgcn_s_barrier()
; #define G8_SCHED __builtin_amdgcn_sched_barrier(0)
; template <class Epi, class Sched, bool GATHER, bool ALIGN_EPI, bool PFB = false>
; __device__ __forceinline__ void gemm_phase(LAS unsigned char* lds, const int lda, const int K, const Sched& S, const Epi& E) {
;     ...
;             G8_LDA(At, 0, 1); G8_STAGE(G8_SB(0, 0), b2, voffB[0], voffB[1]); G8_STAGE(G8_SB(0, 1), b2 + hstepB, voffB[0], voffB[1]); G8_STAGE(G8_SA(0, 0), a2, x00, x01);
;             G8_WAIT_V(8); G8_WAIT_L(0); G8_BAR; G8_MMA(1, 0, At, B0); G8_MMA(1, 1, At, B1); G8_BAR; G8_SCHED;
;             G8_LDB(B0, 1, 0); G8_LDB(B1, 1, 1); G8_SCHED; G8_LDA(At, 1, 0); G8_STAGE(G8_SA(0, 1), a2, x10, x11);
;             G8_WAIT_V(8); G8_WAIT_L(0); G8_BAR; G8_MMA(0, 0, At, B0); G8_MMA(0, 1, At, B1); G8_BAR; G8_SCHED;
	s_setprio 1
	s_waitcnt lgkmcnt(0)
	v_mfma_f32_16x16x32_bf16 v[62:65], v[166:169], v[202:205], v[62:65]
	v_mfma_f32_16x16x32_bf16 v[54:57], v[174:177], v[202:205], v[54:57]
	v_mfma_f32_16x16x32_bf16 v[46:49], v[166:169], v[210:213], v[46:49]
	v_mfma_f32_16x16x32_bf16 v[38:41], v[174:177], v[210:213], v[38:41]
	v_mfma_f32_16x16x32_bf16 v[30:33], v[166:169], v[218:221], v[30:33]
	v_mfma_f32_16x16x32_bf16 v[22:25], v[174:177], v[218:221], v[22:25]
	v_mfma_f32_16x16x32_bf16 v[14:17], v[166:169], v[226:229], v[14:17]
	v_mfma_f32_16x16x32_bf16 v[6:9], v[174:177], v[226:229], v[6:9]
	v_mfma_f32_16x16x32_bf16 v[62:65], v[170:173], v[206:209], v[62:65]
	v_mfma_f32_16x16x32_bf16 v[54:57], v[178:181], v[206:209], v[54:57]
	v_mfma_f32_16x16x32_bf16 v[46:49], v[170:173], v[214:217], v[46:49]
	v_mfma_f32_16x16x32_bf16 v[38:41], v[178:181], v[214:217], v[38:41]
	v_mfma_f32_16x16x32_bf16 v[30:33], v[170:173], v[222:225], v[30:33]
	v_mfma_f32_16x16x32_bf16 v[22:25], v[178:181], v[222:225], v[22:25]
	v_mfma_f32_16x16x32_bf16 v[14:17], v[170:173], v[230:233], v[14:17]
	v_mfma_f32_16x16x32_bf16 v[6:9], v[178:181], v[230:233], v[6:9]
	v_mfma_f32_16x16x32_bf16 v[58:61], v[186:189], v[202:205], v[58:61]
	v_mfma_f32_16x16x32_bf16 v[50:53], v[194:197], v[202:205], v[50:53]
	v_mfma_f32_16x16x32_bf16 v[42:45], v[186:189], v[210:213], v[42:45]
	v_mfma_f32_16x16x32_bf16 v[34:37], v[194:197], v[210:213], v[34:37]
	v_mfma_f32_16x16x32_bf16 v[26:29], v[186:189], v[218:221], v[26:29]
	v_mfma_f32_16x16x32_bf16 v[18:21], v[194:197], v[218:221], v[18:21]
	v_mfma_f32_16x16x32_bf16 v[10:13], v[186:189], v[226:229], v[10:13]
	v_mfma_f32_16x16x32_bf16 v[2:5], v[194:197], v[226:229], v[2:5]
	v_mfma_f32_16x16x32_bf16 v[58:61], v[190:193], v[206:209], v[58:61]
	v_mfma_f32_16x16x32_bf16 v[50:53], v[198:201], v[206:209], v[50:53]
	v_mfma_f32_16x16x32_bf16 v[42:45], v[190:193], v[214:217], v[42:45]
	v_mfma_f32_16x16x32_bf16 v[34:37], v[198:201], v[214:217], v[34:37]
	v_mfma_f32_16x16x32_bf16 v[26:29], v[190:193], v[222:225], v[26:29]
	v_mfma_f32_16x16x32_bf16 v[18:21], v[198:201], v[222:225], v[18:21]
	v_mfma_f32_16x16x32_bf16 v[10:13], v[190:193], v[230:233], v[10:13]
	v_mfma_f32_16x16x32_bf16 v[2:5], v[198:201], v[230:233], v[2:5]
	s_setprio 0
	s_barrier
	s_add_i32 s33, 0, 0x18000
	v_add_u32_e32 v107, s33, v153
	s_add_i32 s54, 0, 0x1c000
	ds_read_b128 v[166:169], v107
	ds_read_b128 v[170:173], v107 offset:1024
	ds_read_b128 v[174:177], v107 offset:2048
	ds_read_b128 v[178:181], v107 offset:3072
	v_add_u32_e32 v107, s54, v153
	ds_read_b128 v[186:189], v107
	ds_read_b128 v[190:193], v107 offset:1024
	ds_read_b128 v[194:197], v107 offset:2048
	ds_read_b128 v[198:201], v107 offset:3072
	s_mov_b32 m0, s35
	ds_read_b128 v[202:205], v158 offset:32768
	ds_read_b128 v[206:209], v158 offset:33792
	ds_read_b128 v[210:213], v158 offset:34816
	ds_read_b128 v[214:217], v158 offset:35840
	ds_read_b128 v[218:221], v158 offset:36864
	ds_read_b128 v[222:225], v158 offset:37888
	ds_read_b128 v[226:229], v158 offset:38912
	ds_read_b128 v[230:233], v158 offset:39936
	v_cndmask_b32_e32 v107, v106, v163, vcc
	global_load_lds_dwordx4 v101, s[26:27]
	s_mov_b32 m0, s36
	s_nop 0
	global_load_lds_dwordx4 v107, s[26:27]
	s_waitcnt vmcnt(8)
	s_waitcnt lgkmcnt(0)
	s_barrier
	s_setprio 1
	s_waitcnt lgkmcnt(0)
	v_mfma_f32_16x16x32_bf16 v[134:137], v[166:169], v[202:205], v[134:137]
	v_mfma_f32_16x16x32_bf16 v[130:133], v[174:177], v[202:205], v[130:133]
	v_mfma_f32_16x16x32_bf16 v[126:129], v[166:169], v[210:213], v[126:129]
	v_mfma_f32_16x16x32_bf16 v[110:113], v[174:177], v[210:213], v[110:113]
	v_mfma_f32_16x16x32_bf16 v[94:97], v[166:169], v[218:221], v[94:97]
	v_mfma_f32_16x16x32_bf16 v[86:89], v[174:177], v[218:221], v[86:89]
	v_mfma_f32_16x16x32_bf16 v[78:81], v[166:169], v[226:229], v[78:81]
	v_mfma_f32_16x16x32_bf16 v[70:73], v[174:177], v[226:229], v[70:73]
	v_mfma_f32_16x16x32_bf16 v[134:137], v[170:173], v[206:209], v[134:137]
	v_mfma_f32_16x16x32_bf16 v[130:133], v[178:181], v[206:209], v[130:133]
	v_mfma_f32_16x16x32_bf16 v[126:129], v[170:173], v[214:217], v[126:129]
	v_mfma_f32_16x16x32_bf16 v[110:113], v[178:181], v[214:217], v[110:113]
	v_mfma_f32_16x16x32_bf16 v[94:97], v[170:173], v[222:225], v[94:97]
	v_mfma_f32_16x16x32_bf16 v[86:89], v[178:181], v[222:225], v[86:89]
	v_mfma_f32_16x16x32_bf16 v[78:81], v[170:173], v[230:233], v[78:81]
	v_mfma_f32_16x16x32_bf16 v[70:73], v[178:181], v[230:233], v[70:73]
	v_mfma_f32_16x16x32_bf16 v[122:125], v[186:189], v[202:205], v[122:125]
	v_mfma_f32_16x16x32_bf16 v[118:121], v[194:197], v[202:205], v[118:121]
	v_mfma_f32_16x16x32_bf16 v[114:117], v[186:189], v[210:213], v[114:117]
	v_mfma_f32_16x16x32_bf16 v[102:105], v[194:197], v[210:213], v[102:105]
	v_mfma_f32_16x16x32_bf16 v[90:93], v[186:189], v[218:221], v[90:93]
	v_mfma_f32_16x16x32_bf16 v[82:85], v[194:197], v[218:221], v[82:85]
	v_mfma_f32_16x16x32_bf16 v[74:77], v[186:189], v[226:229], v[74:77]
	v_mfma_f32_16x16x32_bf16 v[66:69], v[194:197], v[226:229], v[66:69]
	v_mfma_f32_16x16x32_bf16 v[122:125], v[190:193], v[206:209], v[122:125]
	v_mfma_f32_16x16x32_bf16 v[118:121], v[198:201], v[206:209], v[118:121]
	v_mfma_f32_16x16x32_bf16 v[114:117], v[190:193], v[214:217], v[114:117]
	v_mfma_f32_16x16x32_bf16 v[102:105], v[198:201], v[214:217], v[102:105]
	v_mfma_f32_16x16x32_bf16 v[90:93], v[190:193], v[222:225], v[90:93]
	v_mfma_f32_16x16x32_bf16 v[82:85], v[198:201], v[222:225], v[82:85]
	v_mfma_f32_16x16x32_bf16 v[74:77], v[190:193], v[230:233], v[74:77]
	v_mfma_f32_16x16x32_bf16 v[66:69], v[198:201], v[230:233], v[66:69]
	s_setprio 0
	s_barrier
; #define G8_STAGE(bufoff, gbase, v0, v1) do { \
;         __builtin_amdgcn_global_load_lds((const unsigned*)((const char*)(gbase) + (v0)), (LAS unsigned*)(lds + (bufoff) + ldsw), 16, 0, 0); \
;         __builtin_amdgcn_global_load_lds((const unsigned*)((const char*)(gbase) + (v1)), (LAS unsigned*)(lds + (bufoff) + ldsw + 8192), 16, 0, 0); } while (0)
; #define G8_LDA(dst, b, h) do { _Pragma("unroll") for (int m = 0; m < 4; ++m) _Pragma("unroll") for (int k = 0; k < 2; ++k) dst[m][k] = *(const LAS bf16x8*)(lds + G8_SA(b, h) + aoff + m * 2048 + k * 1024); } while (0)
; #define G8_MMA(ai, bj, At, Bt) do { __builtin_amdgcn_s_setprio(1); _Pragma("unroll") for (int m = 0; m < 4; ++m) _Pragma("unroll") for (int n = 0; n < 2; ++n) _Pragma("unroll") for (int k = 0; k < 2; ++k) \
;         acc[ai][bj][m][n] = __builtin_amdgcn_mfma_f32_16x16x32_bf16(Bt[n][k], At[m][k], acc[ai][bj][m][n], 0, 0, 0); __builtin_amdgcn_s_setprio(0); } while (0)
; #define G8_WAIT_V(n) asm volatile("s_waitcnt vmcnt(" #n ")" ::: "memory")
; #define G8_WAIT_L(n) asm volatile("s_waitcnt lgkmcnt(" #n ")" ::: "memory")
; #define G8_BAR __builtin_amdgcn_s_barrier()
; #define G8_SCHED __builtin_amdgcn_sched_barrier(0)
; template <class Epi, class Sched, bool GATHER, bool ALIGN_EPI, bool PFB = false>
; __device__ __forceinline__ void gemm_phase(LAS unsigned char* lds, const int lda, const int K, const Sched& S, const Epi& E) {
;     ...
;             G8_LDA(At, 1, 1); G8_STAGE(G8_SB(1, 0), b3, voffB[0], voffB[1]); G8_STAGE(G8_SB(1, 1), b3 + hstepB, voffB[0], voffB[1]); G8_STAGE(G8_SA(1, 0), a3, x00, x01);
;             G8_WAIT_V(8); G8_WAIT_L(0); G8_BAR; G8_MMA(1, 0, At, B0); G8_MMA(1, 1, At, B1); G8_BAR; G8_SCHED;
;         }
	s_add_i32 s26, s33, s3
	v_lshl_add_u64 v[238:239], s[24:25], 0, v[138:139]
	s_mov_b32 m0, s26
	ds_read_b128 v[202:205], v158 offset:49152
	ds_read_b128 v[206:209], v158 offset:50176
	ds_read_b128 v[210:213], v158 offset:51200
	ds_read_b128 v[214:217], v158 offset:52224
	ds_read_b128 v[218:221], v158 offset:53248
	ds_read_b128 v[222:225], v158 offset:54272
	ds_read_b128 v[226:229], v158 offset:55296
	ds_read_b128 v[230:233], v158 offset:56320
	global_load_lds_dwordx4 v[238:239], off
	s_add_i32 m0, s26, 0x2000
	s_add_u32 s22, s22, 0xc000
	v_lshl_add_u64 v[238:239], s[24:25], 0, v[140:141]
	s_addc_u32 s23, s23, 0
	s_add_i32 s24, s54, s3
	global_load_lds_dwordx4 v[238:239], off
	v_lshl_add_u64 v[238:239], s[22:23], 0, v[138:139]
	s_mov_b32 m0, s24
	v_lshl_add_u64 v[236:237], v[236:237], 0, s[14:15]
	global_load_lds_dwordx4 v[238:239], off
	v_lshl_add_u64 v[238:239], s[22:23], 0, v[140:141]
	s_add_i32 m0, s24, 0x2000
	v_lshl_add_u64 v[234:235], v[234:235], 0, s[14:15]
	global_load_lds_dwordx4 v[238:239], off
	s_mov_b32 m0, s37
	s_nop 0
	global_load_lds_dwordx4 v[236:237], off
	s_mov_b32 m0, s38
	s_nop 0
	global_load_lds_dwordx4 v[234:235], off
	s_waitcnt vmcnt(8)
	s_waitcnt lgkmcnt(0)
	s_barrier
	s_setprio 1
	s_waitcnt lgkmcnt(0)
	v_mfma_f32_16x16x32_bf16 v[62:65], v[166:169], v[202:205], v[62:65]
	v_mfma_f32_16x16x32_bf16 v[54:57], v[174:177], v[202:205], v[54:57]
	v_mfma_f32_16x16x32_bf16 v[46:49], v[166:169], v[210:213], v[46:49]
	v_mfma_f32_16x16x32_bf16 v[38:41], v[174:177], v[210:213], v[38:41]
	v_mfma_f32_16x16x32_bf16 v[30:33], v[166:169], v[218:221], v[30:33]
	v_mfma_f32_16x16x32_bf16 v[22:25], v[174:177], v[218:221], v[22:25]
	v_mfma_f32_16x16x32_bf16 v[14:17], v[166:169], v[226:229], v[14:17]
	v_mfma_f32_16x16x32_bf16 v[6:9], v[174:177], v[226:229], v[6:9]
	v_mfma_f32_16x16x32_bf16 v[62:65], v[170:173], v[206:209], v[62:65]
	v_mfma_f32_16x16x32_bf16 v[54:57], v[178:181], v[206:209], v[54:57]
	v_mfma_f32_16x16x32_bf16 v[46:49], v[170:173], v[214:217], v[46:49]
	v_mfma_f32_16x16x32_bf16 v[38:41], v[178:181], v[214:217], v[38:41]
	v_mfma_f32_16x16x32_bf16 v[30:33], v[170:173], v[222:225], v[30:33]
	v_mfma_f32_16x16x32_bf16 v[22:25], v[178:181], v[222:225], v[22:25]
	v_mfma_f32_16x16x32_bf16 v[14:17], v[170:173], v[230:233], v[14:17]
	v_mfma_f32_16x16x32_bf16 v[6:9], v[178:181], v[230:233], v[6:9]
	v_mfma_f32_16x16x32_bf16 v[58:61], v[186:189], v[202:205], v[58:61]
	v_mfma_f32_16x16x32_bf16 v[50:53], v[194:197], v[202:205], v[50:53]
	v_mfma_f32_16x16x32_bf16 v[42:45], v[186:189], v[210:213], v[42:45]
	v_mfma_f32_16x16x32_bf16 v[34:37], v[194:197], v[210:213], v[34:37]
	v_mfma_f32_16x16x32_bf16 v[26:29], v[186:189], v[218:221], v[26:29]
	v_mfma_f32_16x16x32_bf16 v[18:21], v[194:197], v[218:221], v[18:21]
	v_mfma_f32_16x16x32_bf16 v[10:13], v[186:189], v[226:229], v[10:13]
	v_mfma_f32_16x16x32_bf16 v[2:5], v[194:197], v[226:229], v[2:5]
	v_mfma_f32_16x16x32_bf16 v[58:61], v[190:193], v[206:209], v[58:61]
	v_mfma_f32_16x16x32_bf16 v[50:53], v[198:201], v[206:209], v[50:53]
	v_mfma_f32_16x16x32_bf16 v[42:45], v[190:193], v[214:217], v[42:45]
	v_mfma_f32_16x16x32_bf16 v[34:37], v[198:201], v[214:217], v[34:37]
	v_mfma_f32_16x16x32_bf16 v[26:29], v[190:193], v[222:225], v[26:29]
	v_mfma_f32_16x16x32_bf16 v[18:21], v[198:201], v[222:225], v[18:21]
	v_mfma_f32_16x16x32_bf16 v[10:13], v[190:193], v[230:233], v[10:13]
	v_mfma_f32_16x16x32_bf16 v[2:5], v[198:201], v[230:233], v[2:5]
	s_setprio 0
	s_barrier
	s_add_i32 s53, s53, 2
	s_add_u32 s21, s21, 0x10000
	s_addc_u32 s52, s52, 0
	s_add_u32 s0, s0, 0x100
	s_addc_u32 s1, s1, 0
	s_cmp_gt_u32 s53, 13
	s_cbranch_scc0 .LBB0_1504
	s_and_b64 vcc, exec, s[10:11]
	s_cbranch_vccz .LBB0_1507
	s_barrier

; #define G8_STAGE(bufoff, gbase, v0, v1) do { \
;         __builtin_amdgcn_global_load_lds((const unsigned*)((const char*)(gbase) + (v0)), (LAS unsigned*)(lds + (bufoff) + ldsw), 16, 0, 0); \
;         __builtin_amdgcn_global_load_lds((const unsigned*)((const char*)(gbase) + (v1)), (LAS unsigned*)(lds + (bufoff) + ldsw + 8192), 16, 0, 0); } while (0)
; #define G8_LDA(dst, b, h) do { _Pragma("unroll") for (int m = 0; m < 4; ++m) _Pragma("unroll") for (int k = 0; k < 2; ++k) dst[m][k] = *(const LAS bf16x8*)(lds + G8_SA(b, h) + aoff + m * 2048 + k * 1024); } while (0)
; #define G8_LDB(dst, b, h) do { _Pragma("unroll") for (int n = 0; n < 2; ++n) _Pragma("unroll") for (int k = 0; k < 2; ++k) dst[n][k] = *(const LAS bf16x8*)(lds + G8_SB(b, h) + boff + n * 2048 + k * 1024); } while (0)
; #define G8_WAIT_V(n) asm volatile("s_waitcnt vmcnt(" #n ")" ::: "memory")
; #define G8_WAIT_L(n) asm volatile("s_waitcnt lgkmcnt(" #n ")" ::: "memory")
; #define G8_BAR __builtin_amdgcn_s_barrier()
; template <class Epi, class Sched, bool GATHER, bool ALIGN_EPI, bool PFB = false>
; __device__ __forceinline__ void gemm_phase(LAS unsigned char* lds, const int lda, const int K, const Sched& S, const Epi& E) {
;     ...
;         for (int t = 0; t < nt; t += 2) {
;             const bool last = (t == nt - 2);
;             const char* a1 = cA + (size_t)(t + 1) * kstep;
;             const char* a2 = last ? nA : cA + (size_t)(t + 2) * kstep; const char* b2 = last ? nB : cB + (size_t)(t + 2) * kstepB;
;             const char* a3 = a2 + kstep; const char* b3 = b2 + kstepB;
;             unsigned x00 = vA0[0], x01 = vA0[1], x10 = vA1[0], x11 = vA1[1];
;             if (GATHER) { x00 = last ? nA0[0] : vA0[0]; x01 = last ? nA0[1] : vA0[1]; x10 = last ? nA1[0] : vA1[0]; x11 = last ? nA1[1] : vA1[1]; }
;             G8_LDB(B0, 0, 0); G8_LDB(B1, 0, 1); G8_SCHED; G8_LDA(At, 0, 0); G8_STAGE(G8_SA(1, 1), a1, vA1[0], vA1[1]);
;             G8_WAIT_V(8); if (PFB) asm volatile("" : "+v"(pf_dummy)); G8_WAIT_L(0); G8_BAR; G8_MMA(0, 0, At, B0); G8_MMA(0, 1, At, B1); G8_BAR; G8_SCHED;
;             G8_LDA(At, 0, 1); G8_STAGE(G8_SB(0, 0), b2, voffB[0], voffB[1]); G8_STAGE(G8_SB(0, 1), b2 + hstepB, voffB[0], voffB[1]); G8_STAGE(G8_SA(0, 0), a2, x00, x01);
;             G8_WAIT_V(8); G8_WAIT_L(0); G8_BAR; G8_MMA(1, 0, At, B0); G8_MMA(1, 1, At, B1); G8_BAR; G8_SCHED;
.LBB0_1586:
	s_waitcnt vmcnt(0)
	ds_read_b128 v[130:133], v203
	ds_read_b128 v[134:137], v203 offset:1024
	ds_read_b128 v[138:141], v203 offset:2048
	ds_read_b128 v[142:145], v203 offset:3072
	ds_read_b128 v[166:169], v204
	ds_read_b128 v[176:179], v204 offset:1024
	ds_read_b128 v[194:197], v204 offset:2048
	ds_read_b128 v[206:209], v204 offset:3072
	s_add_u32 s20, s18, 0x80
	s_addc_u32 s21, s19, 0
	s_cmp_eq_u32 s49, 12
	s_cselect_b32 s23, s13, s21
	s_cselect_b32 s22, s12, s20
	s_cselect_b32 s21, s15, s48
	s_cselect_b32 s20, s14, s17
	v_lshl_add_u64 v[170:171], s[18:19], 0, v[160:161]
	s_add_i32 m0, s28, 0xc000
	ds_read_b128 v[210:213], v205
	ds_read_b128 v[214:217], v205 offset:1024
	ds_read_b128 v[218:221], v205 offset:2048
	ds_read_b128 v[222:225], v205 offset:3072
	ds_read_b128 v[226:229], v205 offset:4096
	ds_read_b128 v[230:233], v205 offset:5120
	ds_read_b128 v[234:237], v205 offset:6144
	ds_read_b128 v[238:241], v205 offset:7168
	global_load_lds_dwordx4 v[170:171], off
	v_lshl_add_u64 v[170:171], s[18:19], 0, v[162:163]
	s_add_i32 m0, s28, 0xe000
	s_nop 0
	global_load_lds_dwordx4 v[170:171], off
	s_waitcnt vmcnt(8)
	s_waitcnt lgkmcnt(0)
	s_barrier
	s_setprio 1
	s_waitcnt lgkmcnt(0)
	v_mfma_f32_16x16x32_bf16 v[126:129], v[130:133], v[210:213], v[126:129]
	v_mfma_f32_16x16x32_bf16 v[122:125], v[138:141], v[210:213], v[122:125]
	v_mfma_f32_16x16x32_bf16 v[110:113], v[130:133], v[218:221], v[110:113]
	v_mfma_f32_16x16x32_bf16 v[106:109], v[138:141], v[218:221], v[106:109]
	v_mfma_f32_16x16x32_bf16 v[94:97], v[130:133], v[226:229], v[94:97]
	v_mfma_f32_16x16x32_bf16 v[90:93], v[138:141], v[226:229], v[90:93]
	v_mfma_f32_16x16x32_bf16 v[78:81], v[130:133], v[234:237], v[78:81]
	v_mfma_f32_16x16x32_bf16 v[74:77], v[138:141], v[234:237], v[74:77]
	v_mfma_f32_16x16x32_bf16 v[126:129], v[134:137], v[214:217], v[126:129]
	v_mfma_f32_16x16x32_bf16 v[122:125], v[142:145], v[214:217], v[122:125]
	v_mfma_f32_16x16x32_bf16 v[110:113], v[134:137], v[222:225], v[110:113]
	v_mfma_f32_16x16x32_bf16 v[106:109], v[142:145], v[222:225], v[106:109]
	v_mfma_f32_16x16x32_bf16 v[94:97], v[134:137], v[230:233], v[94:97]
	v_mfma_f32_16x16x32_bf16 v[90:93], v[142:145], v[230:233], v[90:93]
	v_mfma_f32_16x16x32_bf16 v[78:81], v[134:137], v[238:241], v[78:81]
	v_mfma_f32_16x16x32_bf16 v[74:77], v[142:145], v[238:241], v[74:77]
	v_mfma_f32_16x16x32_bf16 v[118:121], v[166:169], v[210:213], v[118:121]
	v_mfma_f32_16x16x32_bf16 v[114:117], v[194:197], v[210:213], v[114:117]
	v_mfma_f32_16x16x32_bf16 v[102:105], v[166:169], v[218:221], v[102:105]
	v_mfma_f32_16x16x32_bf16 v[98:101], v[194:197], v[218:221], v[98:101]
	v_mfma_f32_16x16x32_bf16 v[86:89], v[166:169], v[226:229], v[86:89]
	v_mfma_f32_16x16x32_bf16 v[82:85], v[194:197], v[226:229], v[82:85]
	v_mfma_f32_16x16x32_bf16 v[70:73], v[166:169], v[234:237], v[70:73]
	v_mfma_f32_16x16x32_bf16 v[66:69], v[194:197], v[234:237], v[66:69]
	v_mfma_f32_16x16x32_bf16 v[118:121], v[176:179], v[214:217], v[118:121]
	v_mfma_f32_16x16x32_bf16 v[114:117], v[206:209], v[214:217], v[114:117]
	v_mfma_f32_16x16x32_bf16 v[102:105], v[176:179], v[222:225], v[102:105]
	v_mfma_f32_16x16x32_bf16 v[98:101], v[206:209], v[222:225], v[98:101]
	v_mfma_f32_16x16x32_bf16 v[86:89], v[176:179], v[230:233], v[86:89]
	v_mfma_f32_16x16x32_bf16 v[82:85], v[206:209], v[230:233], v[82:85]
	v_mfma_f32_16x16x32_bf16 v[70:73], v[176:179], v[238:241], v[70:73]
	v_mfma_f32_16x16x32_bf16 v[66:69], v[206:209], v[238:241], v[66:69]
	s_setprio 0
	s_barrier
	s_add_i32 s33, s41, s27
	v_lshl_add_u64 v[170:171], s[20:21], 0, v[146:147]
	s_mov_b32 m0, s33
	ds_read_b128 v[210:213], v205 offset:16384
	ds_read_b128 v[214:217], v205 offset:17408
	ds_read_b128 v[218:221], v205 offset:18432
	ds_read_b128 v[222:225], v205 offset:19456
	ds_read_b128 v[226:229], v205 offset:20480
	ds_read_b128 v[230:233], v205 offset:21504
	ds_read_b128 v[234:237], v205 offset:22528
	ds_read_b128 v[238:241], v205 offset:23552
	global_load_lds_dwordx4 v[170:171], off
	s_add_i32 m0, s33, 0x2000
	s_add_u32 s50, s20, 0x4000
	v_lshl_add_u64 v[170:171], s[20:21], 0, v[148:149]
	s_addc_u32 s51, s21, 0
	s_add_i32 s33, s42, s27
	global_load_lds_dwordx4 v[170:171], off
	v_lshl_add_u64 v[170:171], s[50:51], 0, v[146:147]
	s_mov_b32 m0, s33
	v_lshl_add_u64 v[186:187], s[22:23], 0, v[154:155]
	global_load_lds_dwordx4 v[170:171], off
	v_lshl_add_u64 v[170:171], s[50:51], 0, v[148:149]
	s_add_i32 m0, s33, 0x2000
	s_nop 0
	global_load_lds_dwordx4 v[170:171], off
	v_lshl_add_u64 v[170:171], s[22:23], 0, v[150:151]
	s_mov_b32 m0, s28
	s_nop 0
	global_load_lds_dwordx4 v[170:171], off
	s_mov_b32 m0, s29
	s_nop 0
	global_load_lds_dwordx4 v[186:187], off
	s_waitcnt vmcnt(8)
	s_waitcnt lgkmcnt(0)
	s_barrier
; #define G8_STAGE(bufoff, gbase, v0, v1) do { \
;         __builtin_amdgcn_global_load_lds((const unsigned*)((const char*)(gbase) + (v0)), (LAS unsigned*)(lds + (bufoff) + ldsw), 16, 0, 0); \
;         __builtin_amdgcn_global_load_lds((const unsigned*)((const char*)(gbase) + (v1)), (LAS unsigned*)(lds + (bufoff) + ldsw + 8192), 16, 0, 0); } while (0)
; #define G8_LDA(dst, b, h) do { _Pragma("unroll") for (int m = 0; m < 4; ++m) _Pragma("unroll") for (int k = 0; k < 2; ++k) dst[m][k] = *(const LAS bf16x8*)(lds + G8_SA(b, h) + aoff + m * 2048 + k * 1024); } while (0)
; #define G8_LDB(dst, b, h) do { _Pragma("unroll") for (int n = 0; n < 2; ++n) _Pragma("unroll") for (int k = 0; k < 2; ++k) dst[n][k] = *(const LAS bf16x8*)(lds + G8_SB(b, h) + boff + n * 2048 + k * 1024); } while (0)
; #define G8_MMA(ai, bj, At, Bt) do { __builtin_amdgcn_s_setprio(1); _Pragma("unroll") for (int m = 0; m < 4; ++m) _Pragma("unroll") for (int n = 0; n < 2; ++n) _Pragma("unroll") for (int k = 0; k < 2; ++k) \
;         acc[ai][bj][m][n] = __builtin_amdgcn_mfma_f32_16x16x32_bf16(Bt[n][k], At[m][k], acc[ai][bj][m][n], 0, 0, 0); __builtin_amdgcn_s_setprio(0); } while (0)
; #define G8_WAIT_V(n) asm volatile("s_waitcnt vmcnt(" #n ")" ::: "memory")
; #define G8_WAIT_L(n) asm volatile("s_waitcnt lgkmcnt(" #n ")" ::: "memory")
; #define G8_BAR __builtin_amdgcn_s_barrier()
; #define G8_SCHED __builtin_amdgcn_sched_barrier(0)
; template <class Epi, class Sched, bool GATHER, bool ALIGN_EPI, bool PFB = false>
; __device__ __forceinline__ void gemm_phase(LAS unsigned char* lds, const int lda, const int K, const Sched& S, const Epi& E) {
;     ...
;             G8_LDA(At, 0, 1); G8_STAGE(G8_SB(0, 0), b2, voffB[0], voffB[1]); G8_STAGE(G8_SB(0, 1), b2 + hstepB, voffB[0], voffB[1]); G8_STAGE(G8_SA(0, 0), a2, x00, x01);
;             G8_WAIT_V(8); G8_WAIT_L(0); G8_BAR; G8_MMA(1, 0, At, B0); G8_MMA(1, 1, At, B1); G8_BAR; G8_SCHED;
;             G8_LDB(B0, 1, 0); G8_LDB(B1, 1, 1); G8_SCHED; G8_LDA(At, 1, 0); G8_STAGE(G8_SA(0, 1), a2, x10, x11);
;             G8_WAIT_V(8); G8_WAIT_L(0); G8_BAR; G8_MMA(0, 0, At, B0); G8_MMA(0, 1, At, B1); G8_BAR; G8_SCHED;
	s_setprio 1
	s_waitcnt lgkmcnt(0)
	v_mfma_f32_16x16x32_bf16 v[62:65], v[130:133], v[210:213], v[62:65]
	v_mfma_f32_16x16x32_bf16 v[58:61], v[138:141], v[210:213], v[58:61]
	v_mfma_f32_16x16x32_bf16 v[46:49], v[130:133], v[218:221], v[46:49]
	v_mfma_f32_16x16x32_bf16 v[42:45], v[138:141], v[218:221], v[42:45]
	v_mfma_f32_16x16x32_bf16 v[30:33], v[130:133], v[226:229], v[30:33]
	v_mfma_f32_16x16x32_bf16 v[26:29], v[138:141], v[226:229], v[26:29]
	v_mfma_f32_16x16x32_bf16 v[14:17], v[130:133], v[234:237], v[14:17]
	v_mfma_f32_16x16x32_bf16 v[10:13], v[138:141], v[234:237], v[10:13]
	v_mfma_f32_16x16x32_bf16 v[62:65], v[134:137], v[214:217], v[62:65]
	v_mfma_f32_16x16x32_bf16 v[58:61], v[142:145], v[214:217], v[58:61]
	v_mfma_f32_16x16x32_bf16 v[46:49], v[134:137], v[222:225], v[46:49]
	v_mfma_f32_16x16x32_bf16 v[42:45], v[142:145], v[222:225], v[42:45]
	v_mfma_f32_16x16x32_bf16 v[30:33], v[134:137], v[230:233], v[30:33]
	v_mfma_f32_16x16x32_bf16 v[26:29], v[142:145], v[230:233], v[26:29]
	v_mfma_f32_16x16x32_bf16 v[14:17], v[134:137], v[238:241], v[14:17]
	v_mfma_f32_16x16x32_bf16 v[10:13], v[142:145], v[238:241], v[10:13]
	v_mfma_f32_16x16x32_bf16 v[54:57], v[166:169], v[210:213], v[54:57]
	v_mfma_f32_16x16x32_bf16 v[50:53], v[194:197], v[210:213], v[50:53]
	v_mfma_f32_16x16x32_bf16 v[38:41], v[166:169], v[218:221], v[38:41]
	v_mfma_f32_16x16x32_bf16 v[34:37], v[194:197], v[218:221], v[34:37]
	v_mfma_f32_16x16x32_bf16 v[22:25], v[166:169], v[226:229], v[22:25]
	v_mfma_f32_16x16x32_bf16 v[18:21], v[194:197], v[226:229], v[18:21]
	v_mfma_f32_16x16x32_bf16 v[6:9], v[166:169], v[234:237], v[6:9]
	v_mfma_f32_16x16x32_bf16 v[2:5], v[194:197], v[234:237], v[2:5]
	v_mfma_f32_16x16x32_bf16 v[54:57], v[176:179], v[214:217], v[54:57]
	v_mfma_f32_16x16x32_bf16 v[50:53], v[206:209], v[214:217], v[50:53]
	v_mfma_f32_16x16x32_bf16 v[38:41], v[176:179], v[222:225], v[38:41]
	v_mfma_f32_16x16x32_bf16 v[34:37], v[206:209], v[222:225], v[34:37]
	v_mfma_f32_16x16x32_bf16 v[22:25], v[176:179], v[230:233], v[22:25]
	v_mfma_f32_16x16x32_bf16 v[18:21], v[206:209], v[230:233], v[18:21]
	v_mfma_f32_16x16x32_bf16 v[6:9], v[176:179], v[238:241], v[6:9]
	v_mfma_f32_16x16x32_bf16 v[2:5], v[206:209], v[238:241], v[2:5]
	s_setprio 0
	s_barrier
	s_add_i32 s33, 0, 0x18000
	s_add_i32 s50, 0, 0x1c000
	v_add_u32_e32 v142, s33, v189
	v_add_u32_e32 v158, s50, v189
	ds_read_b128 v[130:133], v142
	ds_read_b128 v[134:137], v142 offset:1024
	ds_read_b128 v[138:141], v142 offset:2048
	ds_read_b128 v[142:145], v142 offset:3072
	ds_read_b128 v[166:169], v158
	ds_read_b128 v[176:179], v158 offset:1024
	ds_read_b128 v[194:197], v158 offset:2048
	ds_read_b128 v[206:209], v158 offset:3072
	s_mov_b32 m0, s30
	v_lshl_add_u64 v[190:191], s[22:23], 0, v[152:153]
	ds_read_b128 v[210:213], v205 offset:32768
	ds_read_b128 v[214:217], v205 offset:33792
	ds_read_b128 v[218:221], v205 offset:34816
	ds_read_b128 v[222:225], v205 offset:35840
	ds_read_b128 v[226:229], v205 offset:36864
	ds_read_b128 v[230:233], v205 offset:37888
	ds_read_b128 v[234:237], v205 offset:38912
	ds_read_b128 v[238:241], v205 offset:39936
	global_load_lds_dwordx4 v[190:191], off
	v_lshl_add_u64 v[190:191], s[22:23], 0, v[156:157]
	s_mov_b32 m0, s31
	s_nop 0
	global_load_lds_dwordx4 v[190:191], off
	s_waitcnt vmcnt(8)
	s_waitcnt lgkmcnt(0)
	s_barrier
	s_setprio 1
	s_waitcnt lgkmcnt(0)
	v_mfma_f32_16x16x32_bf16 v[126:129], v[130:133], v[210:213], v[126:129]
	v_mfma_f32_16x16x32_bf16 v[122:125], v[138:141], v[210:213], v[122:125]
	v_mfma_f32_16x16x32_bf16 v[110:113], v[130:133], v[218:221], v[110:113]
	v_mfma_f32_16x16x32_bf16 v[106:109], v[138:141], v[218:221], v[106:109]
	v_mfma_f32_16x16x32_bf16 v[94:97], v[130:133], v[226:229], v[94:97]
	v_mfma_f32_16x16x32_bf16 v[90:93], v[138:141], v[226:229], v[90:93]
	v_mfma_f32_16x16x32_bf16 v[78:81], v[130:133], v[234:237], v[78:81]
	v_mfma_f32_16x16x32_bf16 v[74:77], v[138:141], v[234:237], v[74:77]
	v_mfma_f32_16x16x32_bf16 v[126:129], v[134:137], v[214:217], v[126:129]
	v_mfma_f32_16x16x32_bf16 v[122:125], v[142:145], v[214:217], v[122:125]
	v_mfma_f32_16x16x32_bf16 v[110:113], v[134:137], v[222:225], v[110:113]
	v_mfma_f32_16x16x32_bf16 v[106:109], v[142:145], v[222:225], v[106:109]
	v_mfma_f32_16x16x32_bf16 v[94:97], v[134:137], v[230:233], v[94:97]
	v_mfma_f32_16x16x32_bf16 v[90:93], v[142:145], v[230:233], v[90:93]
	v_mfma_f32_16x16x32_bf16 v[78:81], v[134:137], v[238:241], v[78:81]
	v_mfma_f32_16x16x32_bf16 v[74:77], v[142:145], v[238:241], v[74:77]
	v_mfma_f32_16x16x32_bf16 v[118:121], v[166:169], v[210:213], v[118:121]
	v_mfma_f32_16x16x32_bf16 v[114:117], v[194:197], v[210:213], v[114:117]
	v_mfma_f32_16x16x32_bf16 v[102:105], v[166:169], v[218:221], v[102:105]
	v_mfma_f32_16x16x32_bf16 v[98:101], v[194:197], v[218:221], v[98:101]
	v_mfma_f32_16x16x32_bf16 v[86:89], v[166:169], v[226:229], v[86:89]
	v_mfma_f32_16x16x32_bf16 v[82:85], v[194:197], v[226:229], v[82:85]
	v_mfma_f32_16x16x32_bf16 v[70:73], v[166:169], v[234:237], v[70:73]
	v_mfma_f32_16x16x32_bf16 v[66:69], v[194:197], v[234:237], v[66:69]
	v_mfma_f32_16x16x32_bf16 v[118:121], v[176:179], v[214:217], v[118:121]
	v_mfma_f32_16x16x32_bf16 v[114:117], v[206:209], v[214:217], v[114:117]
	v_mfma_f32_16x16x32_bf16 v[102:105], v[176:179], v[222:225], v[102:105]
	v_mfma_f32_16x16x32_bf16 v[98:101], v[206:209], v[222:225], v[98:101]
	v_mfma_f32_16x16x32_bf16 v[86:89], v[176:179], v[230:233], v[86:89]
	v_mfma_f32_16x16x32_bf16 v[82:85], v[206:209], v[230:233], v[82:85]
	v_mfma_f32_16x16x32_bf16 v[70:73], v[176:179], v[238:241], v[70:73]
	v_mfma_f32_16x16x32_bf16 v[66:69], v[206:209], v[238:241], v[66:69]
	s_setprio 0
	s_barrier
; #define G8_STAGE(bufoff, gbase, v0, v1) do { \
;         __builtin_amdgcn_global_load_lds((const unsigned*)((const char*)(gbase) + (v0)), (LAS unsigned*)(lds + (bufoff) + ldsw), 16, 0, 0); \
;         __builtin_amdgcn_global_load_lds((const unsigned*)((const char*)(gbase) + (v1)), (LAS unsigned*)(lds + (bufoff) + ldsw + 8192), 16, 0, 0); } while (0)
; #define G8_LDA(dst, b, h) do { _Pragma("unroll") for (int m = 0; m < 4; ++m) _Pragma("unroll") for (int k = 0; k < 2; ++k) dst[m][k] = *(const LAS bf16x8*)(lds + G8_SA(b, h) + aoff + m * 2048 + k * 1024); } while (0)
; #define G8_MMA(ai, bj, At, Bt) do { __builtin_amdgcn_s_setprio(1); _Pragma("unroll") for (int m = 0; m < 4; ++m) _Pragma("unroll") for (int n = 0; n < 2; ++n) _Pragma("unroll") for (int k = 0; k < 2; ++k) \
;         acc[ai][bj][m][n] = __builtin_amdgcn_mfma_f32_16x16x32_bf16(Bt[n][k], At[m][k], acc[ai][bj][m][n], 0, 0, 0); __builtin_amdgcn_s_setprio(0); } while (0)
; #define G8_WAIT_V(n) asm volatile("s_waitcnt vmcnt(" #n ")" ::: "memory")
; #define G8_WAIT_L(n) asm volatile("s_waitcnt lgkmcnt(" #n ")" ::: "memory")
; #define G8_BAR __builtin_amdgcn_s_barrier()
; #define G8_SCHED __builtin_amdgcn_sched_barrier(0)
; template <class Epi, class Sched, bool GATHER, bool ALIGN_EPI, bool PFB = false>
; __device__ __forceinline__ void gemm_phase(LAS unsigned char* lds, const int lda, const int K, const Sched& S, const Epi& E) {
;     ...
;             G8_LDA(At, 1, 1); G8_STAGE(G8_SB(1, 0), b3, voffB[0], voffB[1]); G8_STAGE(G8_SB(1, 1), b3 + hstepB, voffB[0], voffB[1]); G8_STAGE(G8_SA(1, 0), a3, x00, x01);
;             G8_WAIT_V(8); G8_WAIT_L(0); G8_BAR; G8_MMA(1, 0, At, B0); G8_MMA(1, 1, At, B1); G8_BAR; G8_SCHED;
;         }
	s_add_u32 s22, s20, 0x8000
	s_addc_u32 s23, s21, 0
	s_add_i32 s33, s33, s27
	v_lshl_add_u64 v[190:191], s[22:23], 0, v[146:147]
	s_mov_b32 m0, s33
	ds_read_b128 v[210:213], v205 offset:49152
	ds_read_b128 v[214:217], v205 offset:50176
	ds_read_b128 v[218:221], v205 offset:51200
	ds_read_b128 v[222:225], v205 offset:52224
	ds_read_b128 v[226:229], v205 offset:53248
	ds_read_b128 v[230:233], v205 offset:54272
	ds_read_b128 v[234:237], v205 offset:55296
	ds_read_b128 v[238:241], v205 offset:56320
	global_load_lds_dwordx4 v[190:191], off
	s_add_i32 m0, s33, 0x2000
	s_add_u32 s20, s20, 0xc000
	v_lshl_add_u64 v[190:191], s[22:23], 0, v[148:149]
	s_addc_u32 s21, s21, 0
	s_add_i32 s22, s50, s27
	global_load_lds_dwordx4 v[190:191], off
	v_lshl_add_u64 v[190:191], s[20:21], 0, v[146:147]
	s_mov_b32 m0, s22
	v_lshl_add_u64 v[170:171], v[170:171], 0, s[6:7]
	global_load_lds_dwordx4 v[190:191], off
	v_lshl_add_u64 v[190:191], s[20:21], 0, v[148:149]
	s_add_i32 m0, s22, 0x2000
	s_nop 0
	global_load_lds_dwordx4 v[190:191], off
	s_mov_b32 m0, s35
	s_nop 0
	global_load_lds_dwordx4 v[170:171], off
	v_lshl_add_u64 v[170:171], v[186:187], 0, s[6:7]
	s_mov_b32 m0, s36
	s_nop 0
	global_load_lds_dwordx4 v[170:171], off
	s_waitcnt vmcnt(8)
	s_waitcnt lgkmcnt(0)
	s_barrier
	s_setprio 1
	s_waitcnt lgkmcnt(0)
	v_mfma_f32_16x16x32_bf16 v[62:65], v[130:133], v[210:213], v[62:65]
	v_mfma_f32_16x16x32_bf16 v[58:61], v[138:141], v[210:213], v[58:61]
	v_mfma_f32_16x16x32_bf16 v[46:49], v[130:133], v[218:221], v[46:49]
	v_mfma_f32_16x16x32_bf16 v[42:45], v[138:141], v[218:221], v[42:45]
	v_mfma_f32_16x16x32_bf16 v[30:33], v[130:133], v[226:229], v[30:33]
	v_mfma_f32_16x16x32_bf16 v[26:29], v[138:141], v[226:229], v[26:29]
	v_mfma_f32_16x16x32_bf16 v[14:17], v[130:133], v[234:237], v[14:17]
	v_mfma_f32_16x16x32_bf16 v[10:13], v[138:141], v[234:237], v[10:13]
	v_mfma_f32_16x16x32_bf16 v[62:65], v[134:137], v[214:217], v[62:65]
	v_mfma_f32_16x16x32_bf16 v[58:61], v[142:145], v[214:217], v[58:61]
	v_mfma_f32_16x16x32_bf16 v[46:49], v[134:137], v[222:225], v[46:49]
	v_mfma_f32_16x16x32_bf16 v[42:45], v[142:145], v[222:225], v[42:45]
	v_mfma_f32_16x16x32_bf16 v[30:33], v[134:137], v[230:233], v[30:33]
	v_mfma_f32_16x16x32_bf16 v[26:29], v[142:145], v[230:233], v[26:29]
	v_mfma_f32_16x16x32_bf16 v[14:17], v[134:137], v[238:241], v[14:17]
	v_mfma_f32_16x16x32_bf16 v[10:13], v[142:145], v[238:241], v[10:13]
	v_mfma_f32_16x16x32_bf16 v[54:57], v[166:169], v[210:213], v[54:57]
	v_mfma_f32_16x16x32_bf16 v[50:53], v[194:197], v[210:213], v[50:53]
	v_mfma_f32_16x16x32_bf16 v[38:41], v[166:169], v[218:221], v[38:41]
	v_mfma_f32_16x16x32_bf16 v[34:37], v[194:197], v[218:221], v[34:37]
	v_mfma_f32_16x16x32_bf16 v[22:25], v[166:169], v[226:229], v[22:25]
	v_mfma_f32_16x16x32_bf16 v[18:21], v[194:197], v[226:229], v[18:21]
	v_mfma_f32_16x16x32_bf16 v[6:9], v[166:169], v[234:237], v[6:9]
	v_mfma_f32_16x16x32_bf16 v[2:5], v[194:197], v[234:237], v[2:5]
	v_mfma_f32_16x16x32_bf16 v[54:57], v[176:179], v[214:217], v[54:57]
	v_mfma_f32_16x16x32_bf16 v[50:53], v[206:209], v[214:217], v[50:53]
	v_mfma_f32_16x16x32_bf16 v[38:41], v[176:179], v[222:225], v[38:41]
	v_mfma_f32_16x16x32_bf16 v[34:37], v[206:209], v[222:225], v[34:37]
	v_mfma_f32_16x16x32_bf16 v[22:25], v[176:179], v[230:233], v[22:25]
	v_mfma_f32_16x16x32_bf16 v[18:21], v[206:209], v[230:233], v[18:21]
	v_mfma_f32_16x16x32_bf16 v[6:9], v[176:179], v[238:241], v[6:9]
	v_mfma_f32_16x16x32_bf16 v[2:5], v[206:209], v[238:241], v[2:5]
	s_setprio 0
	s_barrier
	s_add_i32 s49, s49, 2
	s_add_u32 s17, s17, 0x10000
	s_addc_u32 s48, s48, 0
	s_add_u32 s18, s18, 0x100
	s_addc_u32 s19, s19, 0
	s_cmp_gt_u32 s49, 13
	s_cbranch_scc0 .LBB0_1586
	s_and_b64 vcc, exec, s[8:9]
	s_cbranch_vccz .LBB0_1589
	s_barrier

; #define G8_STAGE(bufoff, gbase, v0, v1) do { \
;         __builtin_amdgcn_global_load_lds((const unsigned*)((const char*)(gbase) + (v0)), (LAS unsigned*)(lds + (bufoff) + ldsw), 16, 0, 0); \
;         __builtin_amdgcn_global_load_lds((const unsigned*)((const char*)(gbase) + (v1)), (LAS unsigned*)(lds + (bufoff) + ldsw + 8192), 16, 0, 0); } while (0)
; #define G8_LDA(dst, b, h) do { _Pragma("unroll") for (int m = 0; m < 4; ++m) _Pragma("unroll") for (int k = 0; k < 2; ++k) dst[m][k] = *(const LAS bf16x8*)(lds + G8_SA(b, h) + aoff + m * 2048 + k * 1024); } while (0)
; #define G8_LDB(dst, b, h) do { _Pragma("unroll") for (int n = 0; n < 2; ++n) _Pragma("unroll") for (int k = 0; k < 2; ++k) dst[n][k] = *(const LAS bf16x8*)(lds + G8_SB(b, h) + boff + n * 2048 + k * 1024); } while (0)
; #define G8_WAIT_V(n) asm volatile("s_waitcnt vmcnt(" #n ")" ::: "memory")
; #define G8_WAIT_L(n) asm volatile("s_waitcnt lgkmcnt(" #n ")" ::: "memory")
; #define G8_BAR __builtin_amdgcn_s_barrier()
; template <class Epi, class Sched, bool GATHER, bool ALIGN_EPI, bool PFB = false>
; __device__ __forceinline__ void gemm_phase(LAS unsigned char* lds, const int lda, const int K, const Sched& S, const Epi& E) {
;     ...
;         for (int t = 0; t < nt; t += 2) {
;             const bool last = (t == nt - 2);
;             const char* a1 = cA + (size_t)(t + 1) * kstep;
;             const char* a2 = last ? nA : cA + (size_t)(t + 2) * kstep; const char* b2 = last ? nB : cB + (size_t)(t + 2) * kstepB;
;             const char* a3 = a2 + kstep; const char* b3 = b2 + kstepB;
;             unsigned x00 = vA0[0], x01 = vA0[1], x10 = vA1[0], x11 = vA1[1];
;             if (GATHER) { x00 = last ? nA0[0] : vA0[0]; x01 = last ? nA0[1] : vA0[1]; x10 = last ? nA1[0] : vA1[0]; x11 = last ? nA1[1] : vA1[1]; }
;             G8_LDB(B0, 0, 0); G8_LDB(B1, 0, 1); G8_SCHED; G8_LDA(At, 0, 0); G8_STAGE(G8_SA(1, 1), a1, vA1[0], vA1[1]);
;             G8_WAIT_V(8); if (PFB) asm volatile("" : "+v"(pf_dummy)); G8_WAIT_L(0); G8_BAR; G8_MMA(0, 0, At, B0); G8_MMA(0, 1, At, B1); G8_BAR; G8_SCHED;
;             G8_LDA(At, 0, 1); G8_STAGE(G8_SB(0, 0), b2, voffB[0], voffB[1]); G8_STAGE(G8_SB(0, 1), b2 + hstepB, voffB[0], voffB[1]); G8_STAGE(G8_SA(0, 0), a2, x00, x01);
;             G8_WAIT_V(8); G8_WAIT_L(0); G8_BAR; G8_MMA(1, 0, At, B0); G8_MMA(1, 1, At, B1); G8_BAR; G8_SCHED;
.LBB0_1756:
	v_add_u32_e32 v142, s52, v220
	v_add_u32_e32 v180, s53, v220
	ds_read_b128 v[130:133], v142
	ds_read_b128 v[134:137], v142 offset:1024
	ds_read_b128 v[138:141], v142 offset:2048
	ds_read_b128 v[142:145], v142 offset:3072
	ds_read_b128 v[146:149], v180
	ds_read_b128 v[150:153], v180 offset:1024
	ds_read_b128 v[186:189], v180 offset:2048
	ds_read_b128 v[190:193], v180 offset:3072
	s_add_u32 s12, s0, 0x80
	s_addc_u32 s13, s1, 0
	s_cmp_eq_u32 s29, 12
	s_cselect_b32 s15, s35, s13
	s_cselect_b32 s14, s34, s12
	s_cselect_b32 s13, s37, s17
	s_cselect_b32 s12, s36, s16
	v_lshl_add_u64 v[180:181], s[0:1], 0, v[174:175]
	s_add_i32 m0, s42, 0xc000
	ds_read_b128 v[194:197], v239
	ds_read_b128 v[198:201], v239 offset:1024
	ds_read_b128 v[202:205], v239 offset:2048
	ds_read_b128 v[206:209], v239 offset:3072
	ds_read_b128 v[210:213], v239 offset:4096
	ds_read_b128 v[214:217], v239 offset:5120
	ds_read_b128 v[242:245], v239 offset:6144
	ds_read_b128 v[246:249], v239 offset:7168
	global_load_lds_dwordx4 v[180:181], off
	v_lshl_add_u64 v[180:181], s[0:1], 0, v[176:177]
	s_add_i32 m0, s42, 0xe000
	s_nop 0
	global_load_lds_dwordx4 v[180:181], off
	s_waitcnt vmcnt(8)
	s_waitcnt lgkmcnt(0)
	s_barrier
	s_setprio 1
	s_waitcnt lgkmcnt(0)
	v_mfma_f32_16x16x32_bf16 v[126:129], v[130:133], v[194:197], v[126:129]
	v_mfma_f32_16x16x32_bf16 v[122:125], v[138:141], v[194:197], v[122:125]
	v_mfma_f32_16x16x32_bf16 v[110:113], v[130:133], v[202:205], v[110:113]
	v_mfma_f32_16x16x32_bf16 v[106:109], v[138:141], v[202:205], v[106:109]
	v_mfma_f32_16x16x32_bf16 v[94:97], v[130:133], v[210:213], v[94:97]
	v_mfma_f32_16x16x32_bf16 v[90:93], v[138:141], v[210:213], v[90:93]
	v_mfma_f32_16x16x32_bf16 v[78:81], v[130:133], v[242:245], v[78:81]
	v_mfma_f32_16x16x32_bf16 v[74:77], v[138:141], v[242:245], v[74:77]
	v_mfma_f32_16x16x32_bf16 v[126:129], v[134:137], v[198:201], v[126:129]
	v_mfma_f32_16x16x32_bf16 v[122:125], v[142:145], v[198:201], v[122:125]
	v_mfma_f32_16x16x32_bf16 v[110:113], v[134:137], v[206:209], v[110:113]
	v_mfma_f32_16x16x32_bf16 v[106:109], v[142:145], v[206:209], v[106:109]
	v_mfma_f32_16x16x32_bf16 v[94:97], v[134:137], v[214:217], v[94:97]
	v_mfma_f32_16x16x32_bf16 v[90:93], v[142:145], v[214:217], v[90:93]
	v_mfma_f32_16x16x32_bf16 v[78:81], v[134:137], v[246:249], v[78:81]
	v_mfma_f32_16x16x32_bf16 v[74:77], v[142:145], v[246:249], v[74:77]
	v_mfma_f32_16x16x32_bf16 v[118:121], v[146:149], v[194:197], v[118:121]
	v_mfma_f32_16x16x32_bf16 v[114:117], v[186:189], v[194:197], v[114:117]
	v_mfma_f32_16x16x32_bf16 v[102:105], v[146:149], v[202:205], v[102:105]
	v_mfma_f32_16x16x32_bf16 v[98:101], v[186:189], v[202:205], v[98:101]
	v_mfma_f32_16x16x32_bf16 v[86:89], v[146:149], v[210:213], v[86:89]
	v_mfma_f32_16x16x32_bf16 v[82:85], v[186:189], v[210:213], v[82:85]
	v_mfma_f32_16x16x32_bf16 v[70:73], v[146:149], v[242:245], v[70:73]
	v_mfma_f32_16x16x32_bf16 v[66:69], v[186:189], v[242:245], v[66:69]
	v_mfma_f32_16x16x32_bf16 v[118:121], v[150:153], v[198:201], v[118:121]
	v_mfma_f32_16x16x32_bf16 v[114:117], v[190:193], v[198:201], v[114:117]
	v_mfma_f32_16x16x32_bf16 v[102:105], v[150:153], v[206:209], v[102:105]
	v_mfma_f32_16x16x32_bf16 v[98:101], v[190:193], v[206:209], v[98:101]
	v_mfma_f32_16x16x32_bf16 v[86:89], v[150:153], v[214:217], v[86:89]
	v_mfma_f32_16x16x32_bf16 v[82:85], v[190:193], v[214:217], v[82:85]
	v_mfma_f32_16x16x32_bf16 v[70:73], v[150:153], v[246:249], v[70:73]
	v_mfma_f32_16x16x32_bf16 v[66:69], v[190:193], v[246:249], v[66:69]
	s_setprio 0
	s_barrier
	s_add_i32 s31, s52, s39
	v_lshl_add_u64 v[180:181], s[12:13], 0, v[154:155]
	s_mov_b32 m0, s31
	ds_read_b128 v[194:197], v239 offset:16384
	ds_read_b128 v[198:201], v239 offset:17408
	ds_read_b128 v[202:205], v239 offset:18432
	ds_read_b128 v[206:209], v239 offset:19456
	ds_read_b128 v[210:213], v239 offset:20480
	ds_read_b128 v[214:217], v239 offset:21504
	ds_read_b128 v[242:245], v239 offset:22528
	ds_read_b128 v[246:249], v239 offset:23552
	global_load_lds_dwordx4 v[180:181], off
	s_add_i32 m0, s31, 0x2000
	s_add_u32 s40, s12, 0x4000
	v_lshl_add_u64 v[180:181], s[12:13], 0, v[156:157]
	s_addc_u32 s41, s13, 0
	s_add_i32 s31, s53, s39
	global_load_lds_dwordx4 v[180:181], off
	v_lshl_add_u64 v[180:181], s[40:41], 0, v[154:155]
	s_mov_b32 m0, s31
	v_lshl_add_u64 v[250:251], s[14:15], 0, v[162:163]
	global_load_lds_dwordx4 v[180:181], off
	v_lshl_add_u64 v[180:181], s[40:41], 0, v[156:157]
	s_add_i32 m0, s31, 0x2000
	s_nop 0
	global_load_lds_dwordx4 v[180:181], off
	v_lshl_add_u64 v[180:181], s[14:15], 0, v[158:159]
	s_mov_b32 m0, s42
	s_nop 0
	global_load_lds_dwordx4 v[180:181], off
	s_mov_b32 m0, s43
	s_nop 0
	global_load_lds_dwordx4 v[250:251], off
	s_waitcnt vmcnt(8)
	s_waitcnt lgkmcnt(0)
	s_barrier
; #define G8_STAGE(bufoff, gbase, v0, v1) do { \
;         __builtin_amdgcn_global_load_lds((const unsigned*)((const char*)(gbase) + (v0)), (LAS unsigned*)(lds + (bufoff) + ldsw), 16, 0, 0); \
;         __builtin_amdgcn_global_load_lds((const unsigned*)((const char*)(gbase) + (v1)), (LAS unsigned*)(lds + (bufoff) + ldsw + 8192), 16, 0, 0); } while (0)
; #define G8_LDA(dst, b, h) do { _Pragma("unroll") for (int m = 0; m < 4; ++m) _Pragma("unroll") for (int k = 0; k < 2; ++k) dst[m][k] = *(const LAS bf16x8*)(lds + G8_SA(b, h) + aoff + m * 2048 + k * 1024); } while (0)
; #define G8_LDB(dst, b, h) do { _Pragma("unroll") for (int n = 0; n < 2; ++n) _Pragma("unroll") for (int k = 0; k < 2; ++k) dst[n][k] = *(const LAS bf16x8*)(lds + G8_SB(b, h) + boff + n * 2048 + k * 1024); } while (0)
; #define G8_MMA(ai, bj, At, Bt) do { __builtin_amdgcn_s_setprio(1); _Pragma("unroll") for (int m = 0; m < 4; ++m) _Pragma("unroll") for (int n = 0; n < 2; ++n) _Pragma("unroll") for (int k = 0; k < 2; ++k) \
;         acc[ai][bj][m][n] = __builtin_amdgcn_mfma_f32_16x16x32_bf16(Bt[n][k], At[m][k], acc[ai][bj][m][n], 0, 0, 0); __builtin_amdgcn_s_setprio(0); } while (0)
; #define G8_WAIT_V(n) asm volatile("s_waitcnt vmcnt(" #n ")" ::: "memory")
; #define G8_WAIT_L(n) asm volatile("s_waitcnt lgkmcnt(" #n ")" ::: "memory")
; #define G8_BAR __builtin_amdgcn_s_barrier()
; #define G8_SCHED __builtin_amdgcn_sched_barrier(0)
; template <class Epi, class Sched, bool GATHER, bool ALIGN_EPI, bool PFB = false>
; __device__ __forceinline__ void gemm_phase(LAS unsigned char* lds, const int lda, const int K, const Sched& S, const Epi& E) {
;     ...
;             G8_LDA(At, 0, 1); G8_STAGE(G8_SB(0, 0), b2, voffB[0], voffB[1]); G8_STAGE(G8_SB(0, 1), b2 + hstepB, voffB[0], voffB[1]); G8_STAGE(G8_SA(0, 0), a2, x00, x01);
;             G8_WAIT_V(8); G8_WAIT_L(0); G8_BAR; G8_MMA(1, 0, At, B0); G8_MMA(1, 1, At, B1); G8_BAR; G8_SCHED;
;             G8_LDB(B0, 1, 0); G8_LDB(B1, 1, 1); G8_SCHED; G8_LDA(At, 1, 0); G8_STAGE(G8_SA(0, 1), a2, x10, x11);
;             G8_WAIT_V(8); G8_WAIT_L(0); G8_BAR; G8_MMA(0, 0, At, B0); G8_MMA(0, 1, At, B1); G8_BAR; G8_SCHED;
	s_setprio 1
	s_waitcnt lgkmcnt(0)
	v_mfma_f32_16x16x32_bf16 v[62:65], v[130:133], v[194:197], v[62:65]
	v_mfma_f32_16x16x32_bf16 v[58:61], v[138:141], v[194:197], v[58:61]
	v_mfma_f32_16x16x32_bf16 v[46:49], v[130:133], v[202:205], v[46:49]
	v_mfma_f32_16x16x32_bf16 v[42:45], v[138:141], v[202:205], v[42:45]
	v_mfma_f32_16x16x32_bf16 v[30:33], v[130:133], v[210:213], v[30:33]
	v_mfma_f32_16x16x32_bf16 v[26:29], v[138:141], v[210:213], v[26:29]
	v_mfma_f32_16x16x32_bf16 v[14:17], v[130:133], v[242:245], v[14:17]
	v_mfma_f32_16x16x32_bf16 v[10:13], v[138:141], v[242:245], v[10:13]
	v_mfma_f32_16x16x32_bf16 v[62:65], v[134:137], v[198:201], v[62:65]
	v_mfma_f32_16x16x32_bf16 v[58:61], v[142:145], v[198:201], v[58:61]
	v_mfma_f32_16x16x32_bf16 v[46:49], v[134:137], v[206:209], v[46:49]
	v_mfma_f32_16x16x32_bf16 v[42:45], v[142:145], v[206:209], v[42:45]
	v_mfma_f32_16x16x32_bf16 v[30:33], v[134:137], v[214:217], v[30:33]
	v_mfma_f32_16x16x32_bf16 v[26:29], v[142:145], v[214:217], v[26:29]
	v_mfma_f32_16x16x32_bf16 v[14:17], v[134:137], v[246:249], v[14:17]
	v_mfma_f32_16x16x32_bf16 v[10:13], v[142:145], v[246:249], v[10:13]
	v_mfma_f32_16x16x32_bf16 v[54:57], v[146:149], v[194:197], v[54:57]
	v_mfma_f32_16x16x32_bf16 v[50:53], v[186:189], v[194:197], v[50:53]
	v_mfma_f32_16x16x32_bf16 v[38:41], v[146:149], v[202:205], v[38:41]
	v_mfma_f32_16x16x32_bf16 v[34:37], v[186:189], v[202:205], v[34:37]
	v_mfma_f32_16x16x32_bf16 v[22:25], v[146:149], v[210:213], v[22:25]
	v_mfma_f32_16x16x32_bf16 v[18:21], v[186:189], v[210:213], v[18:21]
	v_mfma_f32_16x16x32_bf16 v[6:9], v[146:149], v[242:245], v[6:9]
	v_mfma_f32_16x16x32_bf16 v[2:5], v[186:189], v[242:245], v[2:5]
	v_mfma_f32_16x16x32_bf16 v[54:57], v[150:153], v[198:201], v[54:57]
	v_mfma_f32_16x16x32_bf16 v[50:53], v[190:193], v[198:201], v[50:53]
	v_mfma_f32_16x16x32_bf16 v[38:41], v[150:153], v[206:209], v[38:41]
	v_mfma_f32_16x16x32_bf16 v[34:37], v[190:193], v[206:209], v[34:37]
	v_mfma_f32_16x16x32_bf16 v[22:25], v[150:153], v[214:217], v[22:25]
	v_mfma_f32_16x16x32_bf16 v[18:21], v[190:193], v[214:217], v[18:21]
	v_mfma_f32_16x16x32_bf16 v[6:9], v[150:153], v[246:249], v[6:9]
	v_mfma_f32_16x16x32_bf16 v[2:5], v[190:193], v[246:249], v[2:5]
	s_setprio 0
	s_barrier
	s_add_i32 s31, 0, 0x18000
	s_add_i32 s33, 0, 0x1c000
	v_add_u32_e32 v142, s31, v220
	v_add_u32_e32 v190, s33, v220
	ds_read_b128 v[130:133], v142
	ds_read_b128 v[134:137], v142 offset:1024
	ds_read_b128 v[138:141], v142 offset:2048
	ds_read_b128 v[142:145], v142 offset:3072
	ds_read_b128 v[146:149], v190
	ds_read_b128 v[150:153], v190 offset:1024
	ds_read_b128 v[186:189], v190 offset:2048
	ds_read_b128 v[190:193], v190 offset:3072
	s_mov_b32 m0, s44
	v_lshl_add_u64 v[252:253], s[14:15], 0, v[160:161]
	ds_read_b128 v[194:197], v239 offset:32768
	ds_read_b128 v[198:201], v239 offset:33792
	ds_read_b128 v[202:205], v239 offset:34816
	ds_read_b128 v[206:209], v239 offset:35840
	ds_read_b128 v[210:213], v239 offset:36864
	ds_read_b128 v[214:217], v239 offset:37888
	ds_read_b128 v[242:245], v239 offset:38912
	ds_read_b128 v[246:249], v239 offset:39936
	global_load_lds_dwordx4 v[252:253], off
	v_lshl_add_u64 v[252:253], s[14:15], 0, v[164:165]
	s_mov_b32 m0, s45
	s_nop 0
	global_load_lds_dwordx4 v[252:253], off
	s_waitcnt vmcnt(8)
	s_waitcnt lgkmcnt(0)
	s_barrier
	s_setprio 1
	s_waitcnt lgkmcnt(0)
	v_mfma_f32_16x16x32_bf16 v[126:129], v[130:133], v[194:197], v[126:129]
	v_mfma_f32_16x16x32_bf16 v[122:125], v[138:141], v[194:197], v[122:125]
	v_mfma_f32_16x16x32_bf16 v[110:113], v[130:133], v[202:205], v[110:113]
	v_mfma_f32_16x16x32_bf16 v[106:109], v[138:141], v[202:205], v[106:109]
	v_mfma_f32_16x16x32_bf16 v[94:97], v[130:133], v[210:213], v[94:97]
	v_mfma_f32_16x16x32_bf16 v[90:93], v[138:141], v[210:213], v[90:93]
	v_mfma_f32_16x16x32_bf16 v[78:81], v[130:133], v[242:245], v[78:81]
	v_mfma_f32_16x16x32_bf16 v[74:77], v[138:141], v[242:245], v[74:77]
	v_mfma_f32_16x16x32_bf16 v[126:129], v[134:137], v[198:201], v[126:129]
	v_mfma_f32_16x16x32_bf16 v[122:125], v[142:145], v[198:201], v[122:125]
	v_mfma_f32_16x16x32_bf16 v[110:113], v[134:137], v[206:209], v[110:113]
	v_mfma_f32_16x16x32_bf16 v[106:109], v[142:145], v[206:209], v[106:109]
	v_mfma_f32_16x16x32_bf16 v[94:97], v[134:137], v[214:217], v[94:97]
	v_mfma_f32_16x16x32_bf16 v[90:93], v[142:145], v[214:217], v[90:93]
	v_mfma_f32_16x16x32_bf16 v[78:81], v[134:137], v[246:249], v[78:81]
	v_mfma_f32_16x16x32_bf16 v[74:77], v[142:145], v[246:249], v[74:77]
	v_mfma_f32_16x16x32_bf16 v[118:121], v[146:149], v[194:197], v[118:121]
	v_mfma_f32_16x16x32_bf16 v[114:117], v[186:189], v[194:197], v[114:117]
	v_mfma_f32_16x16x32_bf16 v[102:105], v[146:149], v[202:205], v[102:105]
	v_mfma_f32_16x16x32_bf16 v[98:101], v[186:189], v[202:205], v[98:101]
	v_mfma_f32_16x16x32_bf16 v[86:89], v[146:149], v[210:213], v[86:89]
	v_mfma_f32_16x16x32_bf16 v[82:85], v[186:189], v[210:213], v[82:85]
	v_mfma_f32_16x16x32_bf16 v[70:73], v[146:149], v[242:245], v[70:73]
	v_mfma_f32_16x16x32_bf16 v[66:69], v[186:189], v[242:245], v[66:69]
	v_mfma_f32_16x16x32_bf16 v[118:121], v[150:153], v[198:201], v[118:121]
	v_mfma_f32_16x16x32_bf16 v[114:117], v[190:193], v[198:201], v[114:117]
	v_mfma_f32_16x16x32_bf16 v[102:105], v[150:153], v[206:209], v[102:105]
	v_mfma_f32_16x16x32_bf16 v[98:101], v[190:193], v[206:209], v[98:101]
	v_mfma_f32_16x16x32_bf16 v[86:89], v[150:153], v[214:217], v[86:89]
	v_mfma_f32_16x16x32_bf16 v[82:85], v[190:193], v[214:217], v[82:85]
	v_mfma_f32_16x16x32_bf16 v[70:73], v[150:153], v[246:249], v[70:73]
	v_mfma_f32_16x16x32_bf16 v[66:69], v[190:193], v[246:249], v[66:69]
	s_setprio 0
	s_barrier
; #define G8_STAGE(bufoff, gbase, v0, v1) do { \
;         __builtin_amdgcn_global_load_lds((const unsigned*)((const char*)(gbase) + (v0)), (LAS unsigned*)(lds + (bufoff) + ldsw), 16, 0, 0); \
;         __builtin_amdgcn_global_load_lds((const unsigned*)((const char*)(gbase) + (v1)), (LAS unsigned*)(lds + (bufoff) + ldsw + 8192), 16, 0, 0); } while (0)
; #define G8_LDA(dst, b, h) do { _Pragma("unroll") for (int m = 0; m < 4; ++m) _Pragma("unroll") for (int k = 0; k < 2; ++k) dst[m][k] = *(const LAS bf16x8*)(lds + G8_SA(b, h) + aoff + m * 2048 + k * 1024); } while (0)
; #define G8_MMA(ai, bj, At, Bt) do { __builtin_amdgcn_s_setprio(1); _Pragma("unroll") for (int m = 0; m < 4; ++m) _Pragma("unroll") for (int n = 0; n < 2; ++n) _Pragma("unroll") for (int k = 0; k < 2; ++k) \
;         acc[ai][bj][m][n] = __builtin_amdgcn_mfma_f32_16x16x32_bf16(Bt[n][k], At[m][k], acc[ai][bj][m][n], 0, 0, 0); __builtin_amdgcn_s_setprio(0); } while (0)
; #define G8_WAIT_V(n) asm volatile("s_waitcnt vmcnt(" #n ")" ::: "memory")
; #define G8_WAIT_L(n) asm volatile("s_waitcnt lgkmcnt(" #n ")" ::: "memory")
; #define G8_BAR __builtin_amdgcn_s_barrier()
; #define G8_SCHED __builtin_amdgcn_sched_barrier(0)
; template <class Epi, class Sched, bool GATHER, bool ALIGN_EPI, bool PFB = false>
; __device__ __forceinline__ void gemm_phase(LAS unsigned char* lds, const int lda, const int K, const Sched& S, const Epi& E) {
;     ...
;             G8_LDA(At, 1, 1); G8_STAGE(G8_SB(1, 0), b3, voffB[0], voffB[1]); G8_STAGE(G8_SB(1, 1), b3 + hstepB, voffB[0], voffB[1]); G8_STAGE(G8_SA(1, 0), a3, x00, x01);
;             G8_WAIT_V(8); G8_WAIT_L(0); G8_BAR; G8_MMA(1, 0, At, B0); G8_MMA(1, 1, At, B1); G8_BAR; G8_SCHED;
;         }
	s_add_u32 s14, s12, 0x8000
	s_addc_u32 s15, s13, 0
	s_add_i32 s31, s31, s39
	v_lshl_add_u64 v[252:253], s[14:15], 0, v[154:155]
	s_mov_b32 m0, s31
	ds_read_b128 v[194:197], v239 offset:49152
	ds_read_b128 v[198:201], v239 offset:50176
	ds_read_b128 v[202:205], v239 offset:51200
	ds_read_b128 v[206:209], v239 offset:52224
	ds_read_b128 v[210:213], v239 offset:53248
	ds_read_b128 v[214:217], v239 offset:54272
	ds_read_b128 v[242:245], v239 offset:55296
	ds_read_b128 v[246:249], v239 offset:56320
	global_load_lds_dwordx4 v[252:253], off
	s_add_i32 m0, s31, 0x2000
	s_add_u32 s12, s12, 0xc000
	v_lshl_add_u64 v[252:253], s[14:15], 0, v[156:157]
	s_addc_u32 s13, s13, 0
	s_add_i32 s14, s33, s39
	global_load_lds_dwordx4 v[252:253], off
	v_lshl_add_u64 v[252:253], s[12:13], 0, v[154:155]
	s_mov_b32 m0, s14
	v_lshl_add_u64 v[180:181], v[180:181], 0, s[22:23]
	global_load_lds_dwordx4 v[252:253], off
	v_lshl_add_u64 v[252:253], s[12:13], 0, v[156:157]
	s_add_i32 m0, s14, 0x2000
	s_nop 0
	global_load_lds_dwordx4 v[252:253], off
	s_mov_b32 m0, s47
	s_nop 0
	global_load_lds_dwordx4 v[180:181], off
	v_lshl_add_u64 v[180:181], v[250:251], 0, s[22:23]
	s_mov_b32 m0, s48
	s_nop 0
	global_load_lds_dwordx4 v[180:181], off
	s_waitcnt vmcnt(8)
	s_waitcnt lgkmcnt(0)
	s_barrier
	s_setprio 1
	s_waitcnt lgkmcnt(0)
	v_mfma_f32_16x16x32_bf16 v[62:65], v[130:133], v[194:197], v[62:65]
	v_mfma_f32_16x16x32_bf16 v[58:61], v[138:141], v[194:197], v[58:61]
	v_mfma_f32_16x16x32_bf16 v[46:49], v[130:133], v[202:205], v[46:49]
	v_mfma_f32_16x16x32_bf16 v[42:45], v[138:141], v[202:205], v[42:45]
	v_mfma_f32_16x16x32_bf16 v[30:33], v[130:133], v[210:213], v[30:33]
	v_mfma_f32_16x16x32_bf16 v[26:29], v[138:141], v[210:213], v[26:29]
	v_mfma_f32_16x16x32_bf16 v[14:17], v[130:133], v[242:245], v[14:17]
	v_mfma_f32_16x16x32_bf16 v[10:13], v[138:141], v[242:245], v[10:13]
	v_mfma_f32_16x16x32_bf16 v[62:65], v[134:137], v[198:201], v[62:65]
	v_mfma_f32_16x16x32_bf16 v[58:61], v[142:145], v[198:201], v[58:61]
	v_mfma_f32_16x16x32_bf16 v[46:49], v[134:137], v[206:209], v[46:49]
	v_mfma_f32_16x16x32_bf16 v[42:45], v[142:145], v[206:209], v[42:45]
	v_mfma_f32_16x16x32_bf16 v[30:33], v[134:137], v[214:217], v[30:33]
	v_mfma_f32_16x16x32_bf16 v[26:29], v[142:145], v[214:217], v[26:29]
	v_mfma_f32_16x16x32_bf16 v[14:17], v[134:137], v[246:249], v[14:17]
	v_mfma_f32_16x16x32_bf16 v[10:13], v[142:145], v[246:249], v[10:13]
	v_mfma_f32_16x16x32_bf16 v[54:57], v[146:149], v[194:197], v[54:57]
	v_mfma_f32_16x16x32_bf16 v[50:53], v[186:189], v[194:197], v[50:53]
	v_mfma_f32_16x16x32_bf16 v[38:41], v[146:149], v[202:205], v[38:41]
	v_mfma_f32_16x16x32_bf16 v[34:37], v[186:189], v[202:205], v[34:37]
	v_mfma_f32_16x16x32_bf16 v[22:25], v[146:149], v[210:213], v[22:25]
	v_mfma_f32_16x16x32_bf16 v[18:21], v[186:189], v[210:213], v[18:21]
	v_mfma_f32_16x16x32_bf16 v[6:9], v[146:149], v[242:245], v[6:9]
	v_mfma_f32_16x16x32_bf16 v[2:5], v[186:189], v[242:245], v[2:5]
	v_mfma_f32_16x16x32_bf16 v[54:57], v[150:153], v[198:201], v[54:57]
	v_mfma_f32_16x16x32_bf16 v[50:53], v[190:193], v[198:201], v[50:53]
	v_mfma_f32_16x16x32_bf16 v[38:41], v[150:153], v[206:209], v[38:41]
	v_mfma_f32_16x16x32_bf16 v[34:37], v[190:193], v[206:209], v[34:37]
	v_mfma_f32_16x16x32_bf16 v[22:25], v[150:153], v[214:217], v[22:25]
	v_mfma_f32_16x16x32_bf16 v[18:21], v[190:193], v[214:217], v[18:21]
	v_mfma_f32_16x16x32_bf16 v[6:9], v[150:153], v[246:249], v[6:9]
	v_mfma_f32_16x16x32_bf16 v[2:5], v[190:193], v[246:249], v[2:5]
	s_setprio 0
	s_barrier
	s_add_i32 s29, s29, 2
	s_add_u32 s16, s16, 0x10000
	s_addc_u32 s17, s17, 0
	s_add_u32 s0, s0, 0x100
	s_addc_u32 s1, s1, 0
	s_cmp_gt_u32 s29, 13
	s_cbranch_scc0 .LBB0_1756
	s_and_b64 vcc, exec, s[24:25]
	s_cbranch_vccz .LBB0_1759
	s_barrier

; #define G8_STAGE(bufoff, gbase, v0, v1) do { \
;         __builtin_amdgcn_global_load_lds((const unsigned*)((const char*)(gbase) + (v0)), (LAS unsigned*)(lds + (bufoff) + ldsw), 16, 0, 0); \
;         __builtin_amdgcn_global_load_lds((const unsigned*)((const char*)(gbase) + (v1)), (LAS unsigned*)(lds + (bufoff) + ldsw + 8192), 16, 0, 0); } while (0)
; #define G8_LDA(dst, b, h) do { _Pragma("unroll") for (int m = 0; m < 4; ++m) _Pragma("unroll") for (int k = 0; k < 2; ++k) dst[m][k] = *(const LAS bf16x8*)(lds + G8_SA(b, h) + aoff + m * 2048 + k * 1024); } while (0)
; #define G8_LDB(dst, b, h) do { _Pragma("unroll") for (int n = 0; n < 2; ++n) _Pragma("unroll") for (int k = 0; k < 2; ++k) dst[n][k] = *(const LAS bf16x8*)(lds + G8_SB(b, h) + boff + n * 2048 + k * 1024); } while (0)
; #define G8_WAIT_V(n) asm volatile("s_waitcnt vmcnt(" #n ")" ::: "memory")
; #define G8_WAIT_L(n) asm volatile("s_waitcnt lgkmcnt(" #n ")" ::: "memory")
; #define G8_BAR __builtin_amdgcn_s_barrier()
; template <class Epi, class Sched, bool GATHER, bool ALIGN_EPI, bool PFB = false>
; __device__ __forceinline__ void gemm_phase(LAS unsigned char* lds, const int lda, const int K, const Sched& S, const Epi& E) {
;     ...
;         for (int t = 0; t < nt; t += 2) {
;             const bool last = (t == nt - 2);
;             const char* a1 = cA + (size_t)(t + 1) * kstep;
;             const char* a2 = last ? nA : cA + (size_t)(t + 2) * kstep; const char* b2 = last ? nB : cB + (size_t)(t + 2) * kstepB;
;             const char* a3 = a2 + kstep; const char* b3 = b2 + kstepB;
;             unsigned x00 = vA0[0], x01 = vA0[1], x10 = vA1[0], x11 = vA1[1];
;             if (GATHER) { x00 = last ? nA0[0] : vA0[0]; x01 = last ? nA0[1] : vA0[1]; x10 = last ? nA1[0] : vA1[0]; x11 = last ? nA1[1] : vA1[1]; }
;             G8_LDB(B0, 0, 0); G8_LDB(B1, 0, 1); G8_SCHED; G8_LDA(At, 0, 0); G8_STAGE(G8_SA(1, 1), a1, vA1[0], vA1[1]);
;             G8_WAIT_V(8); if (PFB) asm volatile("" : "+v"(pf_dummy)); G8_WAIT_L(0); G8_BAR; G8_MMA(0, 0, At, B0); G8_MMA(0, 1, At, B1); G8_BAR; G8_SCHED;
;             G8_LDA(At, 0, 1); G8_STAGE(G8_SB(0, 0), b2, voffB[0], voffB[1]); G8_STAGE(G8_SB(0, 1), b2 + hstepB, voffB[0], voffB[1]); G8_STAGE(G8_SA(0, 0), a2, x00, x01);
;             G8_WAIT_V(8); G8_WAIT_L(0); G8_BAR; G8_MMA(1, 0, At, B0); G8_MMA(1, 1, At, B1); G8_BAR; G8_SCHED;
.LBB0_2139:
	ds_read_b128 v[122:125], v191
	ds_read_b128 v[126:129], v191 offset:1024
	ds_read_b128 v[138:141], v191 offset:2048
	ds_read_b128 v[142:145], v191 offset:3072
	ds_read_b128 v[194:197], v192
	ds_read_b128 v[198:201], v192 offset:1024
	ds_read_b128 v[202:205], v192 offset:2048
	ds_read_b128 v[206:209], v192 offset:3072
	s_add_u32 s26, s24, 0x80
	s_addc_u32 s27, s25, 0
	s_cmp_eq_u32 s23, 12
	s_cselect_b32 s29, s19, s27
	s_cselect_b32 s28, s18, s26
	s_cselect_b32 s27, s21, s17
	s_cselect_b32 s26, s20, s15
	v_lshl_add_u64 v[186:187], s[24:25], 0, v[174:175]
	s_add_i32 m0, s35, 0xc000
	ds_read_b128 v[210:213], v193
	ds_read_b128 v[214:217], v193 offset:1024
	ds_read_b128 v[218:221], v193 offset:2048
	ds_read_b128 v[222:225], v193 offset:3072
	ds_read_b128 v[226:229], v193 offset:4096
	ds_read_b128 v[230:233], v193 offset:5120
	ds_read_b128 v[234:237], v193 offset:6144
	ds_read_b128 v[238:241], v193 offset:7168
	global_load_lds_dwordx4 v[186:187], off
	v_lshl_add_u64 v[186:187], s[24:25], 0, v[176:177]
	s_add_i32 m0, s35, 0xe000
	s_nop 0
	global_load_lds_dwordx4 v[186:187], off
	s_waitcnt vmcnt(8)
	s_waitcnt lgkmcnt(0)
	s_barrier
	s_setprio 1
	s_waitcnt lgkmcnt(0)
	v_mfma_f32_16x16x32_bf16 v[134:137], v[122:125], v[210:213], v[134:137]
	v_mfma_f32_16x16x32_bf16 v[130:133], v[138:141], v[210:213], v[130:133]
	v_mfma_f32_16x16x32_bf16 v[118:121], v[122:125], v[218:221], v[118:121]
	v_mfma_f32_16x16x32_bf16 v[106:109], v[138:141], v[218:221], v[106:109]
	v_mfma_f32_16x16x32_bf16 v[102:105], v[122:125], v[226:229], v[102:105]
	v_mfma_f32_16x16x32_bf16 v[90:93], v[138:141], v[226:229], v[90:93]
	v_mfma_f32_16x16x32_bf16 v[86:89], v[122:125], v[234:237], v[86:89]
	v_mfma_f32_16x16x32_bf16 v[74:77], v[138:141], v[234:237], v[74:77]
	v_mfma_f32_16x16x32_bf16 v[134:137], v[126:129], v[214:217], v[134:137]
	v_mfma_f32_16x16x32_bf16 v[130:133], v[142:145], v[214:217], v[130:133]
	v_mfma_f32_16x16x32_bf16 v[118:121], v[126:129], v[222:225], v[118:121]
	v_mfma_f32_16x16x32_bf16 v[106:109], v[142:145], v[222:225], v[106:109]
	v_mfma_f32_16x16x32_bf16 v[102:105], v[126:129], v[230:233], v[102:105]
	v_mfma_f32_16x16x32_bf16 v[90:93], v[142:145], v[230:233], v[90:93]
	v_mfma_f32_16x16x32_bf16 v[86:89], v[126:129], v[238:241], v[86:89]
	v_mfma_f32_16x16x32_bf16 v[74:77], v[142:145], v[238:241], v[74:77]
	v_mfma_f32_16x16x32_bf16 v[114:117], v[194:197], v[210:213], v[114:117]
	v_mfma_f32_16x16x32_bf16 v[110:113], v[202:205], v[210:213], v[110:113]
	v_mfma_f32_16x16x32_bf16 v[98:101], v[194:197], v[218:221], v[98:101]
	v_mfma_f32_16x16x32_bf16 v[94:97], v[202:205], v[218:221], v[94:97]
	v_mfma_f32_16x16x32_bf16 v[82:85], v[194:197], v[226:229], v[82:85]
	v_mfma_f32_16x16x32_bf16 v[78:81], v[202:205], v[226:229], v[78:81]
	v_mfma_f32_16x16x32_bf16 v[70:73], v[194:197], v[234:237], v[70:73]
	v_mfma_f32_16x16x32_bf16 v[66:69], v[202:205], v[234:237], v[66:69]
	v_mfma_f32_16x16x32_bf16 v[114:117], v[198:201], v[214:217], v[114:117]
	v_mfma_f32_16x16x32_bf16 v[110:113], v[206:209], v[214:217], v[110:113]
	v_mfma_f32_16x16x32_bf16 v[98:101], v[198:201], v[222:225], v[98:101]
	v_mfma_f32_16x16x32_bf16 v[94:97], v[206:209], v[222:225], v[94:97]
	v_mfma_f32_16x16x32_bf16 v[82:85], v[198:201], v[230:233], v[82:85]
	v_mfma_f32_16x16x32_bf16 v[78:81], v[206:209], v[230:233], v[78:81]
	v_mfma_f32_16x16x32_bf16 v[70:73], v[198:201], v[238:241], v[70:73]
	v_mfma_f32_16x16x32_bf16 v[66:69], v[206:209], v[238:241], v[66:69]
	s_setprio 0
	s_barrier
	s_add_i32 s33, s45, s34
	v_lshl_add_u64 v[186:187], s[26:27], 0, v[146:147]
	s_mov_b32 m0, s33
	ds_read_b128 v[210:213], v193 offset:16384
	ds_read_b128 v[214:217], v193 offset:17408
	ds_read_b128 v[218:221], v193 offset:18432
	ds_read_b128 v[222:225], v193 offset:19456
	ds_read_b128 v[226:229], v193 offset:20480
	ds_read_b128 v[230:233], v193 offset:21504
	ds_read_b128 v[234:237], v193 offset:22528
	ds_read_b128 v[238:241], v193 offset:23552
	global_load_lds_dwordx4 v[186:187], off
	s_add_i32 m0, s33, 0x2000
	s_add_u32 s50, s26, 0x4000
	v_lshl_add_u64 v[186:187], s[26:27], 0, v[148:149]
	s_addc_u32 s51, s27, 0
	s_add_i32 s33, s46, s34
	global_load_lds_dwordx4 v[186:187], off
	v_lshl_add_u64 v[186:187], s[50:51], 0, v[146:147]
	s_mov_b32 m0, s33
	v_lshl_add_u64 v[242:243], s[28:29], 0, v[154:155]
	global_load_lds_dwordx4 v[186:187], off
	v_lshl_add_u64 v[186:187], s[50:51], 0, v[148:149]
	s_add_i32 m0, s33, 0x2000
	s_nop 0
	global_load_lds_dwordx4 v[186:187], off
	v_lshl_add_u64 v[186:187], s[28:29], 0, v[150:151]
	s_mov_b32 m0, s35
	s_nop 0
	global_load_lds_dwordx4 v[186:187], off
	s_mov_b32 m0, s36
	s_nop 0
	global_load_lds_dwordx4 v[242:243], off
	s_waitcnt vmcnt(8)
	s_waitcnt lgkmcnt(0)
	s_barrier
; #define G8_STAGE(bufoff, gbase, v0, v1) do { \
;         __builtin_amdgcn_global_load_lds((const unsigned*)((const char*)(gbase) + (v0)), (LAS unsigned*)(lds + (bufoff) + ldsw), 16, 0, 0); \
;         __builtin_amdgcn_global_load_lds((const unsigned*)((const char*)(gbase) + (v1)), (LAS unsigned*)(lds + (bufoff) + ldsw + 8192), 16, 0, 0); } while (0)
; #define G8_LDA(dst, b, h) do { _Pragma("unroll") for (int m = 0; m < 4; ++m) _Pragma("unroll") for (int k = 0; k < 2; ++k) dst[m][k] = *(const LAS bf16x8*)(lds + G8_SA(b, h) + aoff + m * 2048 + k * 1024); } while (0)
; #define G8_LDB(dst, b, h) do { _Pragma("unroll") for (int n = 0; n < 2; ++n) _Pragma("unroll") for (int k = 0; k < 2; ++k) dst[n][k] = *(const LAS bf16x8*)(lds + G8_SB(b, h) + boff + n * 2048 + k * 1024); } while (0)
; #define G8_MMA(ai, bj, At, Bt) do { __builtin_amdgcn_s_setprio(1); _Pragma("unroll") for (int m = 0; m < 4; ++m) _Pragma("unroll") for (int n = 0; n < 2; ++n) _Pragma("unroll") for (int k = 0; k < 2; ++k) \
;         acc[ai][bj][m][n] = __builtin_amdgcn_mfma_f32_16x16x32_bf16(Bt[n][k], At[m][k], acc[ai][bj][m][n], 0, 0, 0); __builtin_amdgcn_s_setprio(0); } while (0)
; #define G8_WAIT_V(n) asm volatile("s_waitcnt vmcnt(" #n ")" ::: "memory")
; #define G8_WAIT_L(n) asm volatile("s_waitcnt lgkmcnt(" #n ")" ::: "memory")
; #define G8_BAR __builtin_amdgcn_s_barrier()
; #define G8_SCHED __builtin_amdgcn_sched_barrier(0)
; template <class Epi, class Sched, bool GATHER, bool ALIGN_EPI, bool PFB = false>
; __device__ __forceinline__ void gemm_phase(LAS unsigned char* lds, const int lda, const int K, const Sched& S, const Epi& E) {
;     ...
;             G8_LDA(At, 0, 1); G8_STAGE(G8_SB(0, 0), b2, voffB[0], voffB[1]); G8_STAGE(G8_SB(0, 1), b2 + hstepB, voffB[0], voffB[1]); G8_STAGE(G8_SA(0, 0), a2, x00, x01);
;             G8_WAIT_V(8); G8_WAIT_L(0); G8_BAR; G8_MMA(1, 0, At, B0); G8_MMA(1, 1, At, B1); G8_BAR; G8_SCHED;
;             G8_LDB(B0, 1, 0); G8_LDB(B1, 1, 1); G8_SCHED; G8_LDA(At, 1, 0); G8_STAGE(G8_SA(0, 1), a2, x10, x11);
;             G8_WAIT_V(8); G8_WAIT_L(0); G8_BAR; G8_MMA(0, 0, At, B0); G8_MMA(0, 1, At, B1); G8_BAR; G8_SCHED;
	s_setprio 1
	s_waitcnt lgkmcnt(0)
	v_mfma_f32_16x16x32_bf16 v[62:65], v[122:125], v[210:213], v[62:65]
	v_mfma_f32_16x16x32_bf16 v[58:61], v[138:141], v[210:213], v[58:61]
	v_mfma_f32_16x16x32_bf16 v[54:57], v[122:125], v[218:221], v[54:57]
	v_mfma_f32_16x16x32_bf16 v[42:45], v[138:141], v[218:221], v[42:45]
	v_mfma_f32_16x16x32_bf16 v[38:41], v[122:125], v[226:229], v[38:41]
	v_mfma_f32_16x16x32_bf16 v[26:29], v[138:141], v[226:229], v[26:29]
	v_mfma_f32_16x16x32_bf16 v[22:25], v[122:125], v[234:237], v[22:25]
	v_mfma_f32_16x16x32_bf16 v[10:13], v[138:141], v[234:237], v[10:13]
	v_mfma_f32_16x16x32_bf16 v[62:65], v[126:129], v[214:217], v[62:65]
	v_mfma_f32_16x16x32_bf16 v[58:61], v[142:145], v[214:217], v[58:61]
	v_mfma_f32_16x16x32_bf16 v[54:57], v[126:129], v[222:225], v[54:57]
	v_mfma_f32_16x16x32_bf16 v[42:45], v[142:145], v[222:225], v[42:45]
	v_mfma_f32_16x16x32_bf16 v[38:41], v[126:129], v[230:233], v[38:41]
	v_mfma_f32_16x16x32_bf16 v[26:29], v[142:145], v[230:233], v[26:29]
	v_mfma_f32_16x16x32_bf16 v[22:25], v[126:129], v[238:241], v[22:25]
	v_mfma_f32_16x16x32_bf16 v[10:13], v[142:145], v[238:241], v[10:13]
	v_mfma_f32_16x16x32_bf16 v[50:53], v[194:197], v[210:213], v[50:53]
	v_mfma_f32_16x16x32_bf16 v[46:49], v[202:205], v[210:213], v[46:49]
	v_mfma_f32_16x16x32_bf16 v[34:37], v[194:197], v[218:221], v[34:37]
	v_mfma_f32_16x16x32_bf16 v[30:33], v[202:205], v[218:221], v[30:33]
	v_mfma_f32_16x16x32_bf16 v[18:21], v[194:197], v[226:229], v[18:21]
	v_mfma_f32_16x16x32_bf16 v[14:17], v[202:205], v[226:229], v[14:17]
	v_mfma_f32_16x16x32_bf16 v[6:9], v[194:197], v[234:237], v[6:9]
	v_mfma_f32_16x16x32_bf16 v[2:5], v[202:205], v[234:237], v[2:5]
	v_mfma_f32_16x16x32_bf16 v[50:53], v[198:201], v[214:217], v[50:53]
	v_mfma_f32_16x16x32_bf16 v[46:49], v[206:209], v[214:217], v[46:49]
	v_mfma_f32_16x16x32_bf16 v[34:37], v[198:201], v[222:225], v[34:37]
	v_mfma_f32_16x16x32_bf16 v[30:33], v[206:209], v[222:225], v[30:33]
	v_mfma_f32_16x16x32_bf16 v[18:21], v[198:201], v[230:233], v[18:21]
	v_mfma_f32_16x16x32_bf16 v[14:17], v[206:209], v[230:233], v[14:17]
	v_mfma_f32_16x16x32_bf16 v[6:9], v[198:201], v[238:241], v[6:9]
	v_mfma_f32_16x16x32_bf16 v[2:5], v[206:209], v[238:241], v[2:5]
	s_setprio 0
	s_barrier
	s_add_i32 s33, 0, 0x18000
	s_add_i32 s49, 0, 0x1c000
	v_add_u32_e32 v142, s33, v189
	v_add_u32_e32 v206, s49, v189
	ds_read_b128 v[122:125], v142
	ds_read_b128 v[126:129], v142 offset:1024
	ds_read_b128 v[138:141], v142 offset:2048
	ds_read_b128 v[142:145], v142 offset:3072
	ds_read_b128 v[194:197], v206
	ds_read_b128 v[198:201], v206 offset:1024
	ds_read_b128 v[202:205], v206 offset:2048
	ds_read_b128 v[206:209], v206 offset:3072
	s_mov_b32 m0, s37
	v_lshl_add_u64 v[244:245], s[28:29], 0, v[152:153]
	ds_read_b128 v[210:213], v193 offset:32768
	ds_read_b128 v[214:217], v193 offset:33792
	ds_read_b128 v[218:221], v193 offset:34816
	ds_read_b128 v[222:225], v193 offset:35840
	ds_read_b128 v[226:229], v193 offset:36864
	ds_read_b128 v[230:233], v193 offset:37888
	ds_read_b128 v[234:237], v193 offset:38912
	ds_read_b128 v[238:241], v193 offset:39936
	global_load_lds_dwordx4 v[244:245], off
	v_lshl_add_u64 v[244:245], s[28:29], 0, v[156:157]
	s_mov_b32 m0, s38
	s_nop 0
	global_load_lds_dwordx4 v[244:245], off
	s_waitcnt vmcnt(8)
	s_waitcnt lgkmcnt(0)
	s_barrier
	s_setprio 1
	s_waitcnt lgkmcnt(0)
	v_mfma_f32_16x16x32_bf16 v[134:137], v[122:125], v[210:213], v[134:137]
	v_mfma_f32_16x16x32_bf16 v[130:133], v[138:141], v[210:213], v[130:133]
	v_mfma_f32_16x16x32_bf16 v[118:121], v[122:125], v[218:221], v[118:121]
	v_mfma_f32_16x16x32_bf16 v[106:109], v[138:141], v[218:221], v[106:109]
	v_mfma_f32_16x16x32_bf16 v[102:105], v[122:125], v[226:229], v[102:105]
	v_mfma_f32_16x16x32_bf16 v[90:93], v[138:141], v[226:229], v[90:93]
	v_mfma_f32_16x16x32_bf16 v[86:89], v[122:125], v[234:237], v[86:89]
	v_mfma_f32_16x16x32_bf16 v[74:77], v[138:141], v[234:237], v[74:77]
	v_mfma_f32_16x16x32_bf16 v[134:137], v[126:129], v[214:217], v[134:137]
	v_mfma_f32_16x16x32_bf16 v[130:133], v[142:145], v[214:217], v[130:133]
	v_mfma_f32_16x16x32_bf16 v[118:121], v[126:129], v[222:225], v[118:121]
	v_mfma_f32_16x16x32_bf16 v[106:109], v[142:145], v[222:225], v[106:109]
	v_mfma_f32_16x16x32_bf16 v[102:105], v[126:129], v[230:233], v[102:105]
	v_mfma_f32_16x16x32_bf16 v[90:93], v[142:145], v[230:233], v[90:93]
	v_mfma_f32_16x16x32_bf16 v[86:89], v[126:129], v[238:241], v[86:89]
	v_mfma_f32_16x16x32_bf16 v[74:77], v[142:145], v[238:241], v[74:77]
	v_mfma_f32_16x16x32_bf16 v[114:117], v[194:197], v[210:213], v[114:117]
	v_mfma_f32_16x16x32_bf16 v[110:113], v[202:205], v[210:213], v[110:113]
	v_mfma_f32_16x16x32_bf16 v[98:101], v[194:197], v[218:221], v[98:101]
	v_mfma_f32_16x16x32_bf16 v[94:97], v[202:205], v[218:221], v[94:97]
	v_mfma_f32_16x16x32_bf16 v[82:85], v[194:197], v[226:229], v[82:85]
	v_mfma_f32_16x16x32_bf16 v[78:81], v[202:205], v[226:229], v[78:81]
	v_mfma_f32_16x16x32_bf16 v[70:73], v[194:197], v[234:237], v[70:73]
	v_mfma_f32_16x16x32_bf16 v[66:69], v[202:205], v[234:237], v[66:69]
	v_mfma_f32_16x16x32_bf16 v[114:117], v[198:201], v[214:217], v[114:117]
	v_mfma_f32_16x16x32_bf16 v[110:113], v[206:209], v[214:217], v[110:113]
	v_mfma_f32_16x16x32_bf16 v[98:101], v[198:201], v[222:225], v[98:101]
	v_mfma_f32_16x16x32_bf16 v[94:97], v[206:209], v[222:225], v[94:97]
	v_mfma_f32_16x16x32_bf16 v[82:85], v[198:201], v[230:233], v[82:85]
	v_mfma_f32_16x16x32_bf16 v[78:81], v[206:209], v[230:233], v[78:81]
	v_mfma_f32_16x16x32_bf16 v[70:73], v[198:201], v[238:241], v[70:73]
	v_mfma_f32_16x16x32_bf16 v[66:69], v[206:209], v[238:241], v[66:69]
	s_setprio 0
	s_barrier
; #define G8_STAGE(bufoff, gbase, v0, v1) do { \
;         __builtin_amdgcn_global_load_lds((const unsigned*)((const char*)(gbase) + (v0)), (LAS unsigned*)(lds + (bufoff) + ldsw), 16, 0, 0); \
;         __builtin_amdgcn_global_load_lds((const unsigned*)((const char*)(gbase) + (v1)), (LAS unsigned*)(lds + (bufoff) + ldsw + 8192), 16, 0, 0); } while (0)
; #define G8_LDA(dst, b, h) do { _Pragma("unroll") for (int m = 0; m < 4; ++m) _Pragma("unroll") for (int k = 0; k < 2; ++k) dst[m][k] = *(const LAS bf16x8*)(lds + G8_SA(b, h) + aoff + m * 2048 + k * 1024); } while (0)
; #define G8_MMA(ai, bj, At, Bt) do { __builtin_amdgcn_s_setprio(1); _Pragma("unroll") for (int m = 0; m < 4; ++m) _Pragma("unroll") for (int n = 0; n < 2; ++n) _Pragma("unroll") for (int k = 0; k < 2; ++k) \
;         acc[ai][bj][m][n] = __builtin_amdgcn_mfma_f32_16x16x32_bf16(Bt[n][k], At[m][k], acc[ai][bj][m][n], 0, 0, 0); __builtin_amdgcn_s_setprio(0); } while (0)
; #define G8_WAIT_V(n) asm volatile("s_waitcnt vmcnt(" #n ")" ::: "memory")
; #define G8_WAIT_L(n) asm volatile("s_waitcnt lgkmcnt(" #n ")" ::: "memory")
; #define G8_BAR __builtin_amdgcn_s_barrier()
; #define G8_SCHED __builtin_amdgcn_sched_barrier(0)
; template <class Epi, class Sched, bool GATHER, bool ALIGN_EPI, bool PFB = false>
; __device__ __forceinline__ void gemm_phase(LAS unsigned char* lds, const int lda, const int K, const Sched& S, const Epi& E) {
;     ...
;             G8_LDA(At, 1, 1); G8_STAGE(G8_SB(1, 0), b3, voffB[0], voffB[1]); G8_STAGE(G8_SB(1, 1), b3 + hstepB, voffB[0], voffB[1]); G8_STAGE(G8_SA(1, 0), a3, x00, x01);
;             G8_WAIT_V(8); G8_WAIT_L(0); G8_BAR; G8_MMA(1, 0, At, B0); G8_MMA(1, 1, At, B1); G8_BAR; G8_SCHED;
;         }
	s_add_u32 s28, s26, 0x8000
	s_addc_u32 s29, s27, 0
	s_add_i32 s33, s33, s34
	v_lshl_add_u64 v[244:245], s[28:29], 0, v[146:147]
	s_mov_b32 m0, s33
	ds_read_b128 v[210:213], v193 offset:49152
	ds_read_b128 v[214:217], v193 offset:50176
	ds_read_b128 v[218:221], v193 offset:51200
	ds_read_b128 v[222:225], v193 offset:52224
	ds_read_b128 v[226:229], v193 offset:53248
	ds_read_b128 v[230:233], v193 offset:54272
	ds_read_b128 v[234:237], v193 offset:55296
	ds_read_b128 v[238:241], v193 offset:56320
	global_load_lds_dwordx4 v[244:245], off
	s_add_i32 m0, s33, 0x2000
	s_add_u32 s26, s26, 0xc000
	v_lshl_add_u64 v[244:245], s[28:29], 0, v[148:149]
	s_addc_u32 s27, s27, 0
	s_add_i32 s28, s49, s34
	global_load_lds_dwordx4 v[244:245], off
	v_lshl_add_u64 v[244:245], s[26:27], 0, v[146:147]
	s_mov_b32 m0, s28
	v_lshl_add_u64 v[186:187], v[186:187], 0, s[8:9]
	global_load_lds_dwordx4 v[244:245], off
	v_lshl_add_u64 v[244:245], s[26:27], 0, v[148:149]
	s_add_i32 m0, s28, 0x2000
	s_nop 0
	global_load_lds_dwordx4 v[244:245], off
	s_mov_b32 m0, s40
	s_nop 0
	global_load_lds_dwordx4 v[186:187], off
	v_lshl_add_u64 v[186:187], v[242:243], 0, s[8:9]
	s_mov_b32 m0, s41
	s_nop 0
	global_load_lds_dwordx4 v[186:187], off
	s_waitcnt vmcnt(8)
	s_waitcnt lgkmcnt(0)
	s_barrier
	s_setprio 1
	s_waitcnt lgkmcnt(0)
	v_mfma_f32_16x16x32_bf16 v[62:65], v[122:125], v[210:213], v[62:65]
	v_mfma_f32_16x16x32_bf16 v[58:61], v[138:141], v[210:213], v[58:61]
	v_mfma_f32_16x16x32_bf16 v[54:57], v[122:125], v[218:221], v[54:57]
	v_mfma_f32_16x16x32_bf16 v[42:45], v[138:141], v[218:221], v[42:45]
	v_mfma_f32_16x16x32_bf16 v[38:41], v[122:125], v[226:229], v[38:41]
	v_mfma_f32_16x16x32_bf16 v[26:29], v[138:141], v[226:229], v[26:29]
	v_mfma_f32_16x16x32_bf16 v[22:25], v[122:125], v[234:237], v[22:25]
	v_mfma_f32_16x16x32_bf16 v[10:13], v[138:141], v[234:237], v[10:13]
	v_mfma_f32_16x16x32_bf16 v[62:65], v[126:129], v[214:217], v[62:65]
	v_mfma_f32_16x16x32_bf16 v[58:61], v[142:145], v[214:217], v[58:61]
	v_mfma_f32_16x16x32_bf16 v[54:57], v[126:129], v[222:225], v[54:57]
	v_mfma_f32_16x16x32_bf16 v[42:45], v[142:145], v[222:225], v[42:45]
	v_mfma_f32_16x16x32_bf16 v[38:41], v[126:129], v[230:233], v[38:41]
	v_mfma_f32_16x16x32_bf16 v[26:29], v[142:145], v[230:233], v[26:29]
	v_mfma_f32_16x16x32_bf16 v[22:25], v[126:129], v[238:241], v[22:25]
	v_mfma_f32_16x16x32_bf16 v[10:13], v[142:145], v[238:241], v[10:13]
	v_mfma_f32_16x16x32_bf16 v[50:53], v[194:197], v[210:213], v[50:53]
	v_mfma_f32_16x16x32_bf16 v[46:49], v[202:205], v[210:213], v[46:49]
	v_mfma_f32_16x16x32_bf16 v[34:37], v[194:197], v[218:221], v[34:37]
	v_mfma_f32_16x16x32_bf16 v[30:33], v[202:205], v[218:221], v[30:33]
	v_mfma_f32_16x16x32_bf16 v[18:21], v[194:197], v[226:229], v[18:21]
	v_mfma_f32_16x16x32_bf16 v[14:17], v[202:205], v[226:229], v[14:17]
	v_mfma_f32_16x16x32_bf16 v[6:9], v[194:197], v[234:237], v[6:9]
	v_mfma_f32_16x16x32_bf16 v[2:5], v[202:205], v[234:237], v[2:5]
	v_mfma_f32_16x16x32_bf16 v[50:53], v[198:201], v[214:217], v[50:53]
	v_mfma_f32_16x16x32_bf16 v[46:49], v[206:209], v[214:217], v[46:49]
	v_mfma_f32_16x16x32_bf16 v[34:37], v[198:201], v[222:225], v[34:37]
	v_mfma_f32_16x16x32_bf16 v[30:33], v[206:209], v[222:225], v[30:33]
	v_mfma_f32_16x16x32_bf16 v[18:21], v[198:201], v[230:233], v[18:21]
	v_mfma_f32_16x16x32_bf16 v[14:17], v[206:209], v[230:233], v[14:17]
	v_mfma_f32_16x16x32_bf16 v[6:9], v[198:201], v[238:241], v[6:9]
	v_mfma_f32_16x16x32_bf16 v[2:5], v[206:209], v[238:241], v[2:5]
	s_setprio 0
	s_barrier
	s_add_i32 s23, s23, 2
	s_add_u32 s15, s15, 0x10000
	s_addc_u32 s17, s17, 0
	s_add_u32 s24, s24, 0x100
	s_addc_u32 s25, s25, 0
	s_cmp_gt_u32 s23, 13
	s_cbranch_scc0 .LBB0_2139
	s_and_b64 vcc, exec, s[10:11]
	s_cbranch_vccz .LBB0_2142
	s_barrier

; #define G8_STAGE(bufoff, gbase, v0, v1) do { \
;         __builtin_amdgcn_global_load_lds((const unsigned*)((const char*)(gbase) + (v0)), (LAS unsigned*)(lds + (bufoff) + ldsw), 16, 0, 0); \
;         __builtin_amdgcn_global_load_lds((const unsigned*)((const char*)(gbase) + (v1)), (LAS unsigned*)(lds + (bufoff) + ldsw + 8192), 16, 0, 0); } while (0)
; #define G8_LDA(dst, b, h) do { _Pragma("unroll") for (int m = 0; m < 4; ++m) _Pragma("unroll") for (int k = 0; k < 2; ++k) dst[m][k] = *(const LAS bf16x8*)(lds + G8_SA(b, h) + aoff + m * 2048 + k * 1024); } while (0)
; #define G8_LDB(dst, b, h) do { _Pragma("unroll") for (int n = 0; n < 2; ++n) _Pragma("unroll") for (int k = 0; k < 2; ++k) dst[n][k] = *(const LAS bf16x8*)(lds + G8_SB(b, h) + boff + n * 2048 + k * 1024); } while (0)
; #define G8_WAIT_V(n) asm volatile("s_waitcnt vmcnt(" #n ")" ::: "memory")
; #define G8_WAIT_L(n) asm volatile("s_waitcnt lgkmcnt(" #n ")" ::: "memory")
; #define G8_BAR __builtin_amdgcn_s_barrier()
; template <class Epi, class Sched, bool GATHER, bool ALIGN_EPI, bool PFB = false>
; __device__ __forceinline__ void gemm_phase(LAS unsigned char* lds, const int lda, const int K, const Sched& S, const Epi& E) {
;     ...
;         for (int t = 0; t < nt; t += 2) {
;             const bool last = (t == nt - 2);
;             const char* a1 = cA + (size_t)(t + 1) * kstep;
;             const char* a2 = last ? nA : cA + (size_t)(t + 2) * kstep; const char* b2 = last ? nB : cB + (size_t)(t + 2) * kstepB;
;             const char* a3 = a2 + kstep; const char* b3 = b2 + kstepB;
;             unsigned x00 = vA0[0], x01 = vA0[1], x10 = vA1[0], x11 = vA1[1];
;             if (GATHER) { x00 = last ? nA0[0] : vA0[0]; x01 = last ? nA0[1] : vA0[1]; x10 = last ? nA1[0] : vA1[0]; x11 = last ? nA1[1] : vA1[1]; }
;             G8_LDB(B0, 0, 0); G8_LDB(B1, 0, 1); G8_SCHED; G8_LDA(At, 0, 0); G8_STAGE(G8_SA(1, 1), a1, vA1[0], vA1[1]);
;             G8_WAIT_V(8); if (PFB) asm volatile("" : "+v"(pf_dummy)); G8_WAIT_L(0); G8_BAR; G8_MMA(0, 0, At, B0); G8_MMA(0, 1, At, B1); G8_BAR; G8_SCHED;
;             G8_LDA(At, 0, 1); G8_STAGE(G8_SB(0, 0), b2, voffB[0], voffB[1]); G8_STAGE(G8_SB(0, 1), b2 + hstepB, voffB[0], voffB[1]); G8_STAGE(G8_SA(0, 0), a2, x00, x01);
;             G8_WAIT_V(8); G8_WAIT_L(0); G8_BAR; G8_MMA(1, 0, At, B0); G8_MMA(1, 1, At, B1); G8_BAR; G8_SCHED;
.LBB0_2366:
	s_add_u32 s26, s78, s0
	s_addc_u32 s27, s79, s1
	s_add_u32 s28, s26, 0x1944e100
	ds_read_b128 v[168:171], v160
	ds_read_b128 v[172:175], v160 offset:1024
	ds_read_b128 v[176:179], v160 offset:2048
	ds_read_b128 v[186:189], v160 offset:3072
	ds_read_b128 v[190:193], v161
	ds_read_b128 v[194:197], v161 offset:1024
	ds_read_b128 v[198:201], v161 offset:2048
	ds_read_b128 v[202:205], v161 offset:3072
	s_addc_u32 s29, s27, 0
	s_cmpk_eq_i32 s0, 0x700
	s_cselect_b64 vcc, -1, 0
	s_and_b64 s[26:27], vcc, exec
	s_cselect_b32 s26, s22, s25
	s_cselect_b32 s31, s59, s29
	s_cselect_b32 s30, s58, s28
	s_cselect_b32 s27, s23, s61
	s_add_u32 s28, s26, 0x8000
	v_cndmask_b32_e32 v142, v99, v144, vcc
	v_cndmask_b32_e32 v101, v100, v165, vcc
	v_cndmask_b32_e32 v150, v98, v166, vcc
	s_addc_u32 s29, s27, 0
	v_lshl_add_u64 v[180:181], v[146:147], 0, s[0:1]
	s_add_i32 m0, s37, 0xc000
	ds_read_b128 v[206:209], v162
	ds_read_b128 v[210:213], v162 offset:1024
	ds_read_b128 v[214:217], v162 offset:2048
	ds_read_b128 v[218:221], v162 offset:3072
	ds_read_b128 v[222:225], v162 offset:4096
	ds_read_b128 v[226:229], v162 offset:5120
	ds_read_b128 v[230:233], v162 offset:6144
	ds_read_b128 v[234:237], v162 offset:7168
	global_load_lds_dwordx4 v[180:181], off
	v_lshl_add_u64 v[180:181], v[112:113], 0, s[0:1]
	s_add_i32 m0, s37, 0xe000
	s_nop 0
	global_load_lds_dwordx4 v[180:181], off
	s_waitcnt vmcnt(8)
	s_waitcnt lgkmcnt(0)
	s_barrier
	s_setprio 1
	s_waitcnt lgkmcnt(0)
	v_mfma_f32_16x16x32_bf16 v[134:137], v[168:171], v[206:209], v[134:137]
	v_mfma_f32_16x16x32_bf16 v[130:133], v[176:179], v[206:209], v[130:133]
	v_mfma_f32_16x16x32_bf16 v[122:125], v[168:171], v[214:217], v[122:125]
	v_mfma_f32_16x16x32_bf16 v[106:109], v[176:179], v[214:217], v[106:109]
	v_mfma_f32_16x16x32_bf16 v[94:97], v[168:171], v[222:225], v[94:97]
	v_mfma_f32_16x16x32_bf16 v[86:89], v[176:179], v[222:225], v[86:89]
	v_mfma_f32_16x16x32_bf16 v[78:81], v[168:171], v[230:233], v[78:81]
	v_mfma_f32_16x16x32_bf16 v[70:73], v[176:179], v[230:233], v[70:73]
	v_mfma_f32_16x16x32_bf16 v[134:137], v[172:175], v[210:213], v[134:137]
	v_mfma_f32_16x16x32_bf16 v[130:133], v[186:189], v[210:213], v[130:133]
	v_mfma_f32_16x16x32_bf16 v[122:125], v[172:175], v[218:221], v[122:125]
	v_mfma_f32_16x16x32_bf16 v[106:109], v[186:189], v[218:221], v[106:109]
	v_mfma_f32_16x16x32_bf16 v[94:97], v[172:175], v[226:229], v[94:97]
	v_mfma_f32_16x16x32_bf16 v[86:89], v[186:189], v[226:229], v[86:89]
	v_mfma_f32_16x16x32_bf16 v[78:81], v[172:175], v[234:237], v[78:81]
	v_mfma_f32_16x16x32_bf16 v[70:73], v[186:189], v[234:237], v[70:73]
	v_mfma_f32_16x16x32_bf16 v[118:121], v[190:193], v[206:209], v[118:121]
	v_mfma_f32_16x16x32_bf16 v[126:129], v[198:201], v[206:209], v[126:129]
	v_mfma_f32_16x16x32_bf16 v[114:117], v[190:193], v[214:217], v[114:117]
	v_mfma_f32_16x16x32_bf16 v[102:105], v[198:201], v[214:217], v[102:105]
	v_mfma_f32_16x16x32_bf16 v[90:93], v[190:193], v[222:225], v[90:93]
	v_mfma_f32_16x16x32_bf16 v[82:85], v[198:201], v[222:225], v[82:85]
	v_mfma_f32_16x16x32_bf16 v[74:77], v[190:193], v[230:233], v[74:77]
	v_mfma_f32_16x16x32_bf16 v[66:69], v[198:201], v[230:233], v[66:69]
	v_mfma_f32_16x16x32_bf16 v[118:121], v[194:197], v[210:213], v[118:121]
	v_mfma_f32_16x16x32_bf16 v[126:129], v[202:205], v[210:213], v[126:129]
	v_mfma_f32_16x16x32_bf16 v[114:117], v[194:197], v[218:221], v[114:117]
	v_mfma_f32_16x16x32_bf16 v[102:105], v[202:205], v[218:221], v[102:105]
	v_mfma_f32_16x16x32_bf16 v[90:93], v[194:197], v[226:229], v[90:93]
	v_mfma_f32_16x16x32_bf16 v[82:85], v[202:205], v[226:229], v[82:85]
	v_mfma_f32_16x16x32_bf16 v[74:77], v[194:197], v[234:237], v[74:77]
	v_mfma_f32_16x16x32_bf16 v[66:69], v[202:205], v[234:237], v[66:69]
	s_setprio 0
	s_barrier
	s_add_i32 s33, s47, s3
	v_lshl_add_u64 v[180:181], s[26:27], 0, v[138:139]
	s_mov_b32 m0, s33
	ds_read_b128 v[206:209], v162 offset:16384
	ds_read_b128 v[210:213], v162 offset:17408
	ds_read_b128 v[214:217], v162 offset:18432
	ds_read_b128 v[218:221], v162 offset:19456
	ds_read_b128 v[222:225], v162 offset:20480
	ds_read_b128 v[226:229], v162 offset:21504
	ds_read_b128 v[230:233], v162 offset:22528
	ds_read_b128 v[234:237], v162 offset:23552
	global_load_lds_dwordx4 v[180:181], off
	s_add_i32 m0, s33, 0x2000
	s_add_u32 s64, s26, 0x4000
	v_lshl_add_u64 v[180:181], s[26:27], 0, v[140:141]
	s_addc_u32 s65, s27, 0
	s_add_i32 s33, s48, s3
	global_load_lds_dwordx4 v[180:181], off
	v_lshl_add_u64 v[180:181], s[64:65], 0, v[138:139]
	s_mov_b32 m0, s33
	v_mov_b32_e32 v151, v143
	global_load_lds_dwordx4 v[180:181], off
	v_lshl_add_u64 v[180:181], s[64:65], 0, v[140:141]
	s_add_i32 m0, s33, 0x2000
	s_nop 0
	global_load_lds_dwordx4 v[180:181], off
	s_mov_b32 m0, s37
	v_lshl_add_u64 v[180:181], s[30:31], 0, v[142:143]
	global_load_lds_dwordx4 v142, s[30:31]
	s_mov_b32 m0, s38
	s_nop 0
	global_load_lds_dwordx4 v150, s[30:31]
	s_waitcnt vmcnt(8)
	s_waitcnt lgkmcnt(0)
	v_lshl_add_u64 v[150:151], s[30:31], 0, v[150:151]
	s_barrier
; #define G8_STAGE(bufoff, gbase, v0, v1) do { \
;         __builtin_amdgcn_global_load_lds((const unsigned*)((const char*)(gbase) + (v0)), (LAS unsigned*)(lds + (bufoff) + ldsw), 16, 0, 0); \
;         __builtin_amdgcn_global_load_lds((const unsigned*)((const char*)(gbase) + (v1)), (LAS unsigned*)(lds + (bufoff) + ldsw + 8192), 16, 0, 0); } while (0)
; #define G8_LDA(dst, b, h) do { _Pragma("unroll") for (int m = 0; m < 4; ++m) _Pragma("unroll") for (int k = 0; k < 2; ++k) dst[m][k] = *(const LAS bf16x8*)(lds + G8_SA(b, h) + aoff + m * 2048 + k * 1024); } while (0)
; #define G8_LDB(dst, b, h) do { _Pragma("unroll") for (int n = 0; n < 2; ++n) _Pragma("unroll") for (int k = 0; k < 2; ++k) dst[n][k] = *(const LAS bf16x8*)(lds + G8_SB(b, h) + boff + n * 2048 + k * 1024); } while (0)
; #define G8_MMA(ai, bj, At, Bt) do { __builtin_amdgcn_s_setprio(1); _Pragma("unroll") for (int m = 0; m < 4; ++m) _Pragma("unroll") for (int n = 0; n < 2; ++n) _Pragma("unroll") for (int k = 0; k < 2; ++k) \
;         acc[ai][bj][m][n] = __builtin_amdgcn_mfma_f32_16x16x32_bf16(Bt[n][k], At[m][k], acc[ai][bj][m][n], 0, 0, 0); __builtin_amdgcn_s_setprio(0); } while (0)
; #define G8_WAIT_V(n) asm volatile("s_waitcnt vmcnt(" #n ")" ::: "memory")
; #define G8_WAIT_L(n) asm volatile("s_waitcnt lgkmcnt(" #n ")" ::: "memory")
; #define G8_BAR __builtin_amdgcn_s_barrier()
; #define G8_SCHED __builtin_amdgcn_sched_barrier(0)
; template <class Epi, class Sched, bool GATHER, bool ALIGN_EPI, bool PFB = false>
; __device__ __forceinline__ void gemm_phase(LAS unsigned char* lds, const int lda, const int K, const Sched& S, const Epi& E) {
;     ...
;             G8_LDA(At, 0, 1); G8_STAGE(G8_SB(0, 0), b2, voffB[0], voffB[1]); G8_STAGE(G8_SB(0, 1), b2 + hstepB, voffB[0], voffB[1]); G8_STAGE(G8_SA(0, 0), a2, x00, x01);
;             G8_WAIT_V(8); G8_WAIT_L(0); G8_BAR; G8_MMA(1, 0, At, B0); G8_MMA(1, 1, At, B1); G8_BAR; G8_SCHED;
;             G8_LDB(B0, 1, 0); G8_LDB(B1, 1, 1); G8_SCHED; G8_LDA(At, 1, 0); G8_STAGE(G8_SA(0, 1), a2, x10, x11);
;             G8_WAIT_V(8); G8_WAIT_L(0); G8_BAR; G8_MMA(0, 0, At, B0); G8_MMA(0, 1, At, B1); G8_BAR; G8_SCHED;
	s_setprio 1
	s_waitcnt lgkmcnt(0)
	v_mfma_f32_16x16x32_bf16 v[62:65], v[168:171], v[206:209], v[62:65]
	v_mfma_f32_16x16x32_bf16 v[54:57], v[176:179], v[206:209], v[54:57]
	v_mfma_f32_16x16x32_bf16 v[46:49], v[168:171], v[214:217], v[46:49]
	v_mfma_f32_16x16x32_bf16 v[38:41], v[176:179], v[214:217], v[38:41]
	v_mfma_f32_16x16x32_bf16 v[30:33], v[168:171], v[222:225], v[30:33]
	v_mfma_f32_16x16x32_bf16 v[22:25], v[176:179], v[222:225], v[22:25]
	v_mfma_f32_16x16x32_bf16 v[14:17], v[168:171], v[230:233], v[14:17]
	v_mfma_f32_16x16x32_bf16 v[6:9], v[176:179], v[230:233], v[6:9]
	v_mfma_f32_16x16x32_bf16 v[62:65], v[172:175], v[210:213], v[62:65]
	v_mfma_f32_16x16x32_bf16 v[54:57], v[186:189], v[210:213], v[54:57]
	v_mfma_f32_16x16x32_bf16 v[46:49], v[172:175], v[218:221], v[46:49]
	v_mfma_f32_16x16x32_bf16 v[38:41], v[186:189], v[218:221], v[38:41]
	v_mfma_f32_16x16x32_bf16 v[30:33], v[172:175], v[226:229], v[30:33]
	v_mfma_f32_16x16x32_bf16 v[22:25], v[186:189], v[226:229], v[22:25]
	v_mfma_f32_16x16x32_bf16 v[14:17], v[172:175], v[234:237], v[14:17]
	v_mfma_f32_16x16x32_bf16 v[6:9], v[186:189], v[234:237], v[6:9]
	v_mfma_f32_16x16x32_bf16 v[58:61], v[190:193], v[206:209], v[58:61]
	v_mfma_f32_16x16x32_bf16 v[50:53], v[198:201], v[206:209], v[50:53]
	v_mfma_f32_16x16x32_bf16 v[42:45], v[190:193], v[214:217], v[42:45]
	v_mfma_f32_16x16x32_bf16 v[34:37], v[198:201], v[214:217], v[34:37]
	v_mfma_f32_16x16x32_bf16 v[26:29], v[190:193], v[222:225], v[26:29]
	v_mfma_f32_16x16x32_bf16 v[18:21], v[198:201], v[222:225], v[18:21]
	v_mfma_f32_16x16x32_bf16 v[10:13], v[190:193], v[230:233], v[10:13]
	v_mfma_f32_16x16x32_bf16 v[2:5], v[198:201], v[230:233], v[2:5]
	v_mfma_f32_16x16x32_bf16 v[58:61], v[194:197], v[210:213], v[58:61]
	v_mfma_f32_16x16x32_bf16 v[50:53], v[202:205], v[210:213], v[50:53]
	v_mfma_f32_16x16x32_bf16 v[42:45], v[194:197], v[218:221], v[42:45]
	v_mfma_f32_16x16x32_bf16 v[34:37], v[202:205], v[218:221], v[34:37]
	v_mfma_f32_16x16x32_bf16 v[26:29], v[194:197], v[226:229], v[26:29]
	v_mfma_f32_16x16x32_bf16 v[18:21], v[202:205], v[226:229], v[18:21]
	v_mfma_f32_16x16x32_bf16 v[10:13], v[194:197], v[234:237], v[10:13]
	v_mfma_f32_16x16x32_bf16 v[2:5], v[202:205], v[234:237], v[2:5]
	s_setprio 0
	s_barrier
	s_add_i32 s33, 0, 0x18000
	v_add_u32_e32 v111, s33, v157
	s_add_i32 s64, 0, 0x1c000
	ds_read_b128 v[168:171], v111
	ds_read_b128 v[172:175], v111 offset:1024
	ds_read_b128 v[176:179], v111 offset:2048
	ds_read_b128 v[186:189], v111 offset:3072
	v_add_u32_e32 v111, s64, v157
	ds_read_b128 v[190:193], v111
	ds_read_b128 v[194:197], v111 offset:1024
	ds_read_b128 v[198:201], v111 offset:2048
	ds_read_b128 v[202:205], v111 offset:3072
	s_mov_b32 m0, s39
	ds_read_b128 v[206:209], v162 offset:32768
	ds_read_b128 v[210:213], v162 offset:33792
	ds_read_b128 v[214:217], v162 offset:34816
	ds_read_b128 v[218:221], v162 offset:35840
	ds_read_b128 v[222:225], v162 offset:36864
	ds_read_b128 v[226:229], v162 offset:37888
	ds_read_b128 v[230:233], v162 offset:38912
	ds_read_b128 v[234:237], v162 offset:39936
	v_cndmask_b32_e32 v111, v110, v167, vcc
	global_load_lds_dwordx4 v101, s[30:31]
	s_mov_b32 m0, s40
	s_nop 0
	global_load_lds_dwordx4 v111, s[30:31]
	s_waitcnt vmcnt(8)
	s_waitcnt lgkmcnt(0)
	s_barrier
	s_setprio 1
	s_waitcnt lgkmcnt(0)
	v_mfma_f32_16x16x32_bf16 v[134:137], v[168:171], v[206:209], v[134:137]
	v_mfma_f32_16x16x32_bf16 v[130:133], v[176:179], v[206:209], v[130:133]
	v_mfma_f32_16x16x32_bf16 v[122:125], v[168:171], v[214:217], v[122:125]
	v_mfma_f32_16x16x32_bf16 v[106:109], v[176:179], v[214:217], v[106:109]
	v_mfma_f32_16x16x32_bf16 v[94:97], v[168:171], v[222:225], v[94:97]
	v_mfma_f32_16x16x32_bf16 v[86:89], v[176:179], v[222:225], v[86:89]
	v_mfma_f32_16x16x32_bf16 v[78:81], v[168:171], v[230:233], v[78:81]
	v_mfma_f32_16x16x32_bf16 v[70:73], v[176:179], v[230:233], v[70:73]
	v_mfma_f32_16x16x32_bf16 v[134:137], v[172:175], v[210:213], v[134:137]
	v_mfma_f32_16x16x32_bf16 v[130:133], v[186:189], v[210:213], v[130:133]
	v_mfma_f32_16x16x32_bf16 v[122:125], v[172:175], v[218:221], v[122:125]
	v_mfma_f32_16x16x32_bf16 v[106:109], v[186:189], v[218:221], v[106:109]
	v_mfma_f32_16x16x32_bf16 v[94:97], v[172:175], v[226:229], v[94:97]
	v_mfma_f32_16x16x32_bf16 v[86:89], v[186:189], v[226:229], v[86:89]
	v_mfma_f32_16x16x32_bf16 v[78:81], v[172:175], v[234:237], v[78:81]
	v_mfma_f32_16x16x32_bf16 v[70:73], v[186:189], v[234:237], v[70:73]
	v_mfma_f32_16x16x32_bf16 v[118:121], v[190:193], v[206:209], v[118:121]
	v_mfma_f32_16x16x32_bf16 v[126:129], v[198:201], v[206:209], v[126:129]
	v_mfma_f32_16x16x32_bf16 v[114:117], v[190:193], v[214:217], v[114:117]
	v_mfma_f32_16x16x32_bf16 v[102:105], v[198:201], v[214:217], v[102:105]
	v_mfma_f32_16x16x32_bf16 v[90:93], v[190:193], v[222:225], v[90:93]
	v_mfma_f32_16x16x32_bf16 v[82:85], v[198:201], v[222:225], v[82:85]
	v_mfma_f32_16x16x32_bf16 v[74:77], v[190:193], v[230:233], v[74:77]
	v_mfma_f32_16x16x32_bf16 v[66:69], v[198:201], v[230:233], v[66:69]
	v_mfma_f32_16x16x32_bf16 v[118:121], v[194:197], v[210:213], v[118:121]
	v_mfma_f32_16x16x32_bf16 v[126:129], v[202:205], v[210:213], v[126:129]
	v_mfma_f32_16x16x32_bf16 v[114:117], v[194:197], v[218:221], v[114:117]
	v_mfma_f32_16x16x32_bf16 v[102:105], v[202:205], v[218:221], v[102:105]
	v_mfma_f32_16x16x32_bf16 v[90:93], v[194:197], v[226:229], v[90:93]
	v_mfma_f32_16x16x32_bf16 v[82:85], v[202:205], v[226:229], v[82:85]
	v_mfma_f32_16x16x32_bf16 v[74:77], v[194:197], v[234:237], v[74:77]
	v_mfma_f32_16x16x32_bf16 v[66:69], v[202:205], v[234:237], v[66:69]
	s_setprio 0
	s_barrier
; #define G8_STAGE(bufoff, gbase, v0, v1) do { \
;         __builtin_amdgcn_global_load_lds((const unsigned*)((const char*)(gbase) + (v0)), (LAS unsigned*)(lds + (bufoff) + ldsw), 16, 0, 0); \
;         __builtin_amdgcn_global_load_lds((const unsigned*)((const char*)(gbase) + (v1)), (LAS unsigned*)(lds + (bufoff) + ldsw + 8192), 16, 0, 0); } while (0)
; #define G8_LDA(dst, b, h) do { _Pragma("unroll") for (int m = 0; m < 4; ++m) _Pragma("unroll") for (int k = 0; k < 2; ++k) dst[m][k] = *(const LAS bf16x8*)(lds + G8_SA(b, h) + aoff + m * 2048 + k * 1024); } while (0)
; #define G8_MMA(ai, bj, At, Bt) do { __builtin_amdgcn_s_setprio(1); _Pragma("unroll") for (int m = 0; m < 4; ++m) _Pragma("unroll") for (int n = 0; n < 2; ++n) _Pragma("unroll") for (int k = 0; k < 2; ++k) \
;         acc[ai][bj][m][n] = __builtin_amdgcn_mfma_f32_16x16x32_bf16(Bt[n][k], At[m][k], acc[ai][bj][m][n], 0, 0, 0); __builtin_amdgcn_s_setprio(0); } while (0)
; #define G8_WAIT_V(n) asm volatile("s_waitcnt vmcnt(" #n ")" ::: "memory")
; #define G8_WAIT_L(n) asm volatile("s_waitcnt lgkmcnt(" #n ")" ::: "memory")
; #define G8_BAR __builtin_amdgcn_s_barrier()
; #define G8_SCHED __builtin_amdgcn_sched_barrier(0)
; template <class Epi, class Sched, bool GATHER, bool ALIGN_EPI, bool PFB = false>
; __device__ __forceinline__ void gemm_phase(LAS unsigned char* lds, const int lda, const int K, const Sched& S, const Epi& E) {
;     ...
;             G8_LDA(At, 1, 1); G8_STAGE(G8_SB(1, 0), b3, voffB[0], voffB[1]); G8_STAGE(G8_SB(1, 1), b3 + hstepB, voffB[0], voffB[1]); G8_STAGE(G8_SA(1, 0), a3, x00, x01);
;             G8_WAIT_V(8); G8_WAIT_L(0); G8_BAR; G8_MMA(1, 0, At, B0); G8_MMA(1, 1, At, B1); G8_BAR; G8_SCHED;
;         }
	s_add_i32 s30, s33, s3
	v_lshl_add_u64 v[238:239], s[28:29], 0, v[138:139]
	s_mov_b32 m0, s30
	ds_read_b128 v[206:209], v162 offset:49152
	ds_read_b128 v[210:213], v162 offset:50176
	ds_read_b128 v[214:217], v162 offset:51200
	ds_read_b128 v[218:221], v162 offset:52224
	ds_read_b128 v[222:225], v162 offset:53248
	ds_read_b128 v[226:229], v162 offset:54272
	ds_read_b128 v[230:233], v162 offset:55296
	ds_read_b128 v[234:237], v162 offset:56320
	global_load_lds_dwordx4 v[238:239], off
	s_add_i32 m0, s30, 0x2000
	s_add_u32 s26, s26, 0xc000
	v_lshl_add_u64 v[238:239], s[28:29], 0, v[140:141]
	s_addc_u32 s27, s27, 0
	s_add_i32 s28, s64, s3
	global_load_lds_dwordx4 v[238:239], off
	v_lshl_add_u64 v[238:239], s[26:27], 0, v[138:139]
	s_mov_b32 m0, s28
	v_lshl_add_u64 v[180:181], v[180:181], 0, s[14:15]
	global_load_lds_dwordx4 v[238:239], off
	v_lshl_add_u64 v[238:239], s[26:27], 0, v[140:141]
	s_add_i32 m0, s28, 0x2000
	v_lshl_add_u64 v[150:151], v[150:151], 0, s[14:15]
	global_load_lds_dwordx4 v[238:239], off
	s_mov_b32 m0, s42
	s_nop 0
	global_load_lds_dwordx4 v[180:181], off
	s_mov_b32 m0, s43
	s_nop 0
	global_load_lds_dwordx4 v[150:151], off
	s_waitcnt vmcnt(8)
	s_waitcnt lgkmcnt(0)
	s_barrier
	s_setprio 1
	s_waitcnt lgkmcnt(0)
	v_mfma_f32_16x16x32_bf16 v[62:65], v[168:171], v[206:209], v[62:65]
	v_mfma_f32_16x16x32_bf16 v[54:57], v[176:179], v[206:209], v[54:57]
	v_mfma_f32_16x16x32_bf16 v[46:49], v[168:171], v[214:217], v[46:49]
	v_mfma_f32_16x16x32_bf16 v[38:41], v[176:179], v[214:217], v[38:41]
	v_mfma_f32_16x16x32_bf16 v[30:33], v[168:171], v[222:225], v[30:33]
	v_mfma_f32_16x16x32_bf16 v[22:25], v[176:179], v[222:225], v[22:25]
	v_mfma_f32_16x16x32_bf16 v[14:17], v[168:171], v[230:233], v[14:17]
	v_mfma_f32_16x16x32_bf16 v[6:9], v[176:179], v[230:233], v[6:9]
	v_mfma_f32_16x16x32_bf16 v[62:65], v[172:175], v[210:213], v[62:65]
	v_mfma_f32_16x16x32_bf16 v[54:57], v[186:189], v[210:213], v[54:57]
	v_mfma_f32_16x16x32_bf16 v[46:49], v[172:175], v[218:221], v[46:49]
	v_mfma_f32_16x16x32_bf16 v[38:41], v[186:189], v[218:221], v[38:41]
	v_mfma_f32_16x16x32_bf16 v[30:33], v[172:175], v[226:229], v[30:33]
	v_mfma_f32_16x16x32_bf16 v[22:25], v[186:189], v[226:229], v[22:25]
	v_mfma_f32_16x16x32_bf16 v[14:17], v[172:175], v[234:237], v[14:17]
	v_mfma_f32_16x16x32_bf16 v[6:9], v[186:189], v[234:237], v[6:9]
	v_mfma_f32_16x16x32_bf16 v[58:61], v[190:193], v[206:209], v[58:61]
	v_mfma_f32_16x16x32_bf16 v[50:53], v[198:201], v[206:209], v[50:53]
	v_mfma_f32_16x16x32_bf16 v[42:45], v[190:193], v[214:217], v[42:45]
	v_mfma_f32_16x16x32_bf16 v[34:37], v[198:201], v[214:217], v[34:37]
	v_mfma_f32_16x16x32_bf16 v[26:29], v[190:193], v[222:225], v[26:29]
	v_mfma_f32_16x16x32_bf16 v[18:21], v[198:201], v[222:225], v[18:21]
	v_mfma_f32_16x16x32_bf16 v[10:13], v[190:193], v[230:233], v[10:13]
	v_mfma_f32_16x16x32_bf16 v[2:5], v[198:201], v[230:233], v[2:5]
	v_mfma_f32_16x16x32_bf16 v[58:61], v[194:197], v[210:213], v[58:61]
	v_mfma_f32_16x16x32_bf16 v[50:53], v[202:205], v[210:213], v[50:53]
	v_mfma_f32_16x16x32_bf16 v[42:45], v[194:197], v[218:221], v[42:45]
	v_mfma_f32_16x16x32_bf16 v[34:37], v[202:205], v[218:221], v[34:37]
	v_mfma_f32_16x16x32_bf16 v[26:29], v[194:197], v[226:229], v[26:29]
	v_mfma_f32_16x16x32_bf16 v[18:21], v[202:205], v[226:229], v[18:21]
	v_mfma_f32_16x16x32_bf16 v[10:13], v[194:197], v[234:237], v[10:13]
	v_mfma_f32_16x16x32_bf16 v[2:5], v[202:205], v[234:237], v[2:5]
	s_setprio 0
	s_barrier
	s_add_i32 s63, s63, 2
	s_add_u32 s25, s25, 0x10000
	s_addc_u32 s61, s61, 0
	s_add_u32 s0, s0, 0x100
	s_addc_u32 s1, s1, 0
	s_cmp_gt_u32 s63, 13
	s_cbranch_scc0 .LBB0_2366
	s_and_b64 vcc, exec, s[10:11]
	s_cbranch_vccz .LBB0_2369
	s_barrier

; #define G8_STAGE(bufoff, gbase, v0, v1) do { \
;         __builtin_amdgcn_global_load_lds((const unsigned*)((const char*)(gbase) + (v0)), (LAS unsigned*)(lds + (bufoff) + ldsw), 16, 0, 0); \
;         __builtin_amdgcn_global_load_lds((const unsigned*)((const char*)(gbase) + (v1)), (LAS unsigned*)(lds + (bufoff) + ldsw + 8192), 16, 0, 0); } while (0)
; #define G8_LDA(dst, b, h) do { _Pragma("unroll") for (int m = 0; m < 4; ++m) _Pragma("unroll") for (int k = 0; k < 2; ++k) dst[m][k] = *(const LAS bf16x8*)(lds + G8_SA(b, h) + aoff + m * 2048 + k * 1024); } while (0)
; #define G8_LDB(dst, b, h) do { _Pragma("unroll") for (int n = 0; n < 2; ++n) _Pragma("unroll") for (int k = 0; k < 2; ++k) dst[n][k] = *(const LAS bf16x8*)(lds + G8_SB(b, h) + boff + n * 2048 + k * 1024); } while (0)
; #define G8_WAIT_V(n) asm volatile("s_waitcnt vmcnt(" #n ")" ::: "memory")
; #define G8_WAIT_L(n) asm volatile("s_waitcnt lgkmcnt(" #n ")" ::: "memory")
; #define G8_BAR __builtin_amdgcn_s_barrier()
; template <class Epi, class Sched, bool GATHER, bool ALIGN_EPI, bool PFB = false>
; __device__ __forceinline__ void gemm_phase(LAS unsigned char* lds, const int lda, const int K, const Sched& S, const Epi& E) {
;     ...
;         for (int t = 0; t < nt; t += 2) {
;             const bool last = (t == nt - 2);
;             const char* a1 = cA + (size_t)(t + 1) * kstep;
;             const char* a2 = last ? nA : cA + (size_t)(t + 2) * kstep; const char* b2 = last ? nB : cB + (size_t)(t + 2) * kstepB;
;             const char* a3 = a2 + kstep; const char* b3 = b2 + kstepB;
;             unsigned x00 = vA0[0], x01 = vA0[1], x10 = vA1[0], x11 = vA1[1];
;             if (GATHER) { x00 = last ? nA0[0] : vA0[0]; x01 = last ? nA0[1] : vA0[1]; x10 = last ? nA1[0] : vA1[0]; x11 = last ? nA1[1] : vA1[1]; }
;             G8_LDB(B0, 0, 0); G8_LDB(B1, 0, 1); G8_SCHED; G8_LDA(At, 0, 0); G8_STAGE(G8_SA(1, 1), a1, vA1[0], vA1[1]);
;             G8_WAIT_V(8); if (PFB) asm volatile("" : "+v"(pf_dummy)); G8_WAIT_L(0); G8_BAR; G8_MMA(0, 0, At, B0); G8_MMA(0, 1, At, B1); G8_BAR; G8_SCHED;
;             G8_LDA(At, 0, 1); G8_STAGE(G8_SB(0, 0), b2, voffB[0], voffB[1]); G8_STAGE(G8_SB(0, 1), b2 + hstepB, voffB[0], voffB[1]); G8_STAGE(G8_SA(0, 0), a2, x00, x01);
;             G8_WAIT_V(8); G8_WAIT_L(0); G8_BAR; G8_MMA(1, 0, At, B0); G8_MMA(1, 1, At, B1); G8_BAR; G8_SCHED;
.LBB0_2448:
	s_waitcnt vmcnt(0)
	ds_read_b128 v[130:133], v197
	ds_read_b128 v[134:137], v197 offset:1024
	ds_read_b128 v[138:141], v197 offset:2048
	ds_read_b128 v[142:145], v197 offset:3072
	ds_read_b128 v[166:169], v198
	ds_read_b128 v[176:179], v198 offset:1024
	ds_read_b128 v[190:193], v198 offset:2048
	ds_read_b128 v[200:203], v198 offset:3072
	s_add_u32 s22, s20, 0x80
	s_addc_u32 s23, s21, 0
	s_cmp_eq_u32 s52, 12
	s_cselect_b32 s25, s15, s23
	s_cselect_b32 s24, s14, s22
	s_cselect_b32 s23, s17, s51
	s_cselect_b32 s22, s16, s19
	v_lshl_add_u64 v[170:171], s[20:21], 0, v[160:161]
	s_add_i32 m0, s30, 0xc000
	ds_read_b128 v[204:207], v199
	ds_read_b128 v[208:211], v199 offset:1024
	ds_read_b128 v[212:215], v199 offset:2048
	ds_read_b128 v[216:219], v199 offset:3072
	ds_read_b128 v[220:223], v199 offset:4096
	ds_read_b128 v[224:227], v199 offset:5120
	ds_read_b128 v[228:231], v199 offset:6144
	ds_read_b128 v[232:235], v199 offset:7168
	global_load_lds_dwordx4 v[170:171], off
	v_lshl_add_u64 v[170:171], s[20:21], 0, v[162:163]
	s_add_i32 m0, s30, 0xe000
	s_nop 0
	global_load_lds_dwordx4 v[170:171], off
	s_waitcnt vmcnt(8)
	s_waitcnt lgkmcnt(0)
	s_barrier
	s_setprio 1
	s_waitcnt lgkmcnt(0)
	v_mfma_f32_16x16x32_bf16 v[126:129], v[130:133], v[204:207], v[126:129]
	v_mfma_f32_16x16x32_bf16 v[122:125], v[138:141], v[204:207], v[122:125]
	v_mfma_f32_16x16x32_bf16 v[110:113], v[130:133], v[212:215], v[110:113]
	v_mfma_f32_16x16x32_bf16 v[106:109], v[138:141], v[212:215], v[106:109]
	v_mfma_f32_16x16x32_bf16 v[94:97], v[130:133], v[220:223], v[94:97]
	v_mfma_f32_16x16x32_bf16 v[90:93], v[138:141], v[220:223], v[90:93]
	v_mfma_f32_16x16x32_bf16 v[78:81], v[130:133], v[228:231], v[78:81]
	v_mfma_f32_16x16x32_bf16 v[74:77], v[138:141], v[228:231], v[74:77]
	v_mfma_f32_16x16x32_bf16 v[126:129], v[134:137], v[208:211], v[126:129]
	v_mfma_f32_16x16x32_bf16 v[122:125], v[142:145], v[208:211], v[122:125]
	v_mfma_f32_16x16x32_bf16 v[110:113], v[134:137], v[216:219], v[110:113]
	v_mfma_f32_16x16x32_bf16 v[106:109], v[142:145], v[216:219], v[106:109]
	v_mfma_f32_16x16x32_bf16 v[94:97], v[134:137], v[224:227], v[94:97]
	v_mfma_f32_16x16x32_bf16 v[90:93], v[142:145], v[224:227], v[90:93]
	v_mfma_f32_16x16x32_bf16 v[78:81], v[134:137], v[232:235], v[78:81]
	v_mfma_f32_16x16x32_bf16 v[74:77], v[142:145], v[232:235], v[74:77]
	v_mfma_f32_16x16x32_bf16 v[118:121], v[166:169], v[204:207], v[118:121]
	v_mfma_f32_16x16x32_bf16 v[114:117], v[190:193], v[204:207], v[114:117]
	v_mfma_f32_16x16x32_bf16 v[102:105], v[166:169], v[212:215], v[102:105]
	v_mfma_f32_16x16x32_bf16 v[98:101], v[190:193], v[212:215], v[98:101]
	v_mfma_f32_16x16x32_bf16 v[86:89], v[166:169], v[220:223], v[86:89]
	v_mfma_f32_16x16x32_bf16 v[82:85], v[190:193], v[220:223], v[82:85]
	v_mfma_f32_16x16x32_bf16 v[70:73], v[166:169], v[228:231], v[70:73]
	v_mfma_f32_16x16x32_bf16 v[66:69], v[190:193], v[228:231], v[66:69]
	v_mfma_f32_16x16x32_bf16 v[118:121], v[176:179], v[208:211], v[118:121]
	v_mfma_f32_16x16x32_bf16 v[114:117], v[200:203], v[208:211], v[114:117]
	v_mfma_f32_16x16x32_bf16 v[102:105], v[176:179], v[216:219], v[102:105]
	v_mfma_f32_16x16x32_bf16 v[98:101], v[200:203], v[216:219], v[98:101]
	v_mfma_f32_16x16x32_bf16 v[86:89], v[176:179], v[224:227], v[86:89]
	v_mfma_f32_16x16x32_bf16 v[82:85], v[200:203], v[224:227], v[82:85]
	v_mfma_f32_16x16x32_bf16 v[70:73], v[176:179], v[232:235], v[70:73]
	v_mfma_f32_16x16x32_bf16 v[66:69], v[200:203], v[232:235], v[66:69]
	s_setprio 0
	s_barrier
	s_add_i32 s33, s43, s29
	v_lshl_add_u64 v[170:171], s[22:23], 0, v[146:147]
	s_mov_b32 m0, s33
	ds_read_b128 v[204:207], v199 offset:16384
	ds_read_b128 v[208:211], v199 offset:17408
	ds_read_b128 v[212:215], v199 offset:18432
	ds_read_b128 v[216:219], v199 offset:19456
	ds_read_b128 v[220:223], v199 offset:20480
	ds_read_b128 v[224:227], v199 offset:21504
	ds_read_b128 v[228:231], v199 offset:22528
	ds_read_b128 v[232:235], v199 offset:23552
	global_load_lds_dwordx4 v[170:171], off
	s_add_i32 m0, s33, 0x2000
	s_add_u32 s54, s22, 0x4000
	v_lshl_add_u64 v[170:171], s[22:23], 0, v[148:149]
	s_addc_u32 s55, s23, 0
	s_add_i32 s33, s44, s29
	global_load_lds_dwordx4 v[170:171], off
	v_lshl_add_u64 v[170:171], s[54:55], 0, v[146:147]
	s_mov_b32 m0, s33
	v_lshl_add_u64 v[182:183], s[24:25], 0, v[154:155]
	global_load_lds_dwordx4 v[170:171], off
	v_lshl_add_u64 v[170:171], s[54:55], 0, v[148:149]
	s_add_i32 m0, s33, 0x2000
	s_nop 0
	global_load_lds_dwordx4 v[170:171], off
	v_lshl_add_u64 v[170:171], s[24:25], 0, v[150:151]
	s_mov_b32 m0, s30
	s_nop 0
	global_load_lds_dwordx4 v[170:171], off
	s_mov_b32 m0, s31
	s_nop 0
	global_load_lds_dwordx4 v[182:183], off
	s_waitcnt vmcnt(8)
	s_waitcnt lgkmcnt(0)
	s_barrier
; #define G8_STAGE(bufoff, gbase, v0, v1) do { \
;         __builtin_amdgcn_global_load_lds((const unsigned*)((const char*)(gbase) + (v0)), (LAS unsigned*)(lds + (bufoff) + ldsw), 16, 0, 0); \
;         __builtin_amdgcn_global_load_lds((const unsigned*)((const char*)(gbase) + (v1)), (LAS unsigned*)(lds + (bufoff) + ldsw + 8192), 16, 0, 0); } while (0)
; #define G8_LDA(dst, b, h) do { _Pragma("unroll") for (int m = 0; m < 4; ++m) _Pragma("unroll") for (int k = 0; k < 2; ++k) dst[m][k] = *(const LAS bf16x8*)(lds + G8_SA(b, h) + aoff + m * 2048 + k * 1024); } while (0)
; #define G8_LDB(dst, b, h) do { _Pragma("unroll") for (int n = 0; n < 2; ++n) _Pragma("unroll") for (int k = 0; k < 2; ++k) dst[n][k] = *(const LAS bf16x8*)(lds + G8_SB(b, h) + boff + n * 2048 + k * 1024); } while (0)
; #define G8_MMA(ai, bj, At, Bt) do { __builtin_amdgcn_s_setprio(1); _Pragma("unroll") for (int m = 0; m < 4; ++m) _Pragma("unroll") for (int n = 0; n < 2; ++n) _Pragma("unroll") for (int k = 0; k < 2; ++k) \
;         acc[ai][bj][m][n] = __builtin_amdgcn_mfma_f32_16x16x32_bf16(Bt[n][k], At[m][k], acc[ai][bj][m][n], 0, 0, 0); __builtin_amdgcn_s_setprio(0); } while (0)
; #define G8_WAIT_V(n) asm volatile("s_waitcnt vmcnt(" #n ")" ::: "memory")
; #define G8_WAIT_L(n) asm volatile("s_waitcnt lgkmcnt(" #n ")" ::: "memory")
; #define G8_BAR __builtin_amdgcn_s_barrier()
; #define G8_SCHED __builtin_amdgcn_sched_barrier(0)
; template <class Epi, class Sched, bool GATHER, bool ALIGN_EPI, bool PFB = false>
; __device__ __forceinline__ void gemm_phase(LAS unsigned char* lds, const int lda, const int K, const Sched& S, const Epi& E) {
;     ...
;             G8_LDA(At, 0, 1); G8_STAGE(G8_SB(0, 0), b2, voffB[0], voffB[1]); G8_STAGE(G8_SB(0, 1), b2 + hstepB, voffB[0], voffB[1]); G8_STAGE(G8_SA(0, 0), a2, x00, x01);
;             G8_WAIT_V(8); G8_WAIT_L(0); G8_BAR; G8_MMA(1, 0, At, B0); G8_MMA(1, 1, At, B1); G8_BAR; G8_SCHED;
;             G8_LDB(B0, 1, 0); G8_LDB(B1, 1, 1); G8_SCHED; G8_LDA(At, 1, 0); G8_STAGE(G8_SA(0, 1), a2, x10, x11);
;             G8_WAIT_V(8); G8_WAIT_L(0); G8_BAR; G8_MMA(0, 0, At, B0); G8_MMA(0, 1, At, B1); G8_BAR; G8_SCHED;
	s_setprio 1
	s_waitcnt lgkmcnt(0)
	v_mfma_f32_16x16x32_bf16 v[62:65], v[130:133], v[204:207], v[62:65]
	v_mfma_f32_16x16x32_bf16 v[58:61], v[138:141], v[204:207], v[58:61]
	v_mfma_f32_16x16x32_bf16 v[46:49], v[130:133], v[212:215], v[46:49]
	v_mfma_f32_16x16x32_bf16 v[42:45], v[138:141], v[212:215], v[42:45]
	v_mfma_f32_16x16x32_bf16 v[30:33], v[130:133], v[220:223], v[30:33]
	v_mfma_f32_16x16x32_bf16 v[26:29], v[138:141], v[220:223], v[26:29]
	v_mfma_f32_16x16x32_bf16 v[14:17], v[130:133], v[228:231], v[14:17]
	v_mfma_f32_16x16x32_bf16 v[10:13], v[138:141], v[228:231], v[10:13]
	v_mfma_f32_16x16x32_bf16 v[62:65], v[134:137], v[208:211], v[62:65]
	v_mfma_f32_16x16x32_bf16 v[58:61], v[142:145], v[208:211], v[58:61]
	v_mfma_f32_16x16x32_bf16 v[46:49], v[134:137], v[216:219], v[46:49]
	v_mfma_f32_16x16x32_bf16 v[42:45], v[142:145], v[216:219], v[42:45]
	v_mfma_f32_16x16x32_bf16 v[30:33], v[134:137], v[224:227], v[30:33]
	v_mfma_f32_16x16x32_bf16 v[26:29], v[142:145], v[224:227], v[26:29]
	v_mfma_f32_16x16x32_bf16 v[14:17], v[134:137], v[232:235], v[14:17]
	v_mfma_f32_16x16x32_bf16 v[10:13], v[142:145], v[232:235], v[10:13]
	v_mfma_f32_16x16x32_bf16 v[54:57], v[166:169], v[204:207], v[54:57]
	v_mfma_f32_16x16x32_bf16 v[50:53], v[190:193], v[204:207], v[50:53]
	v_mfma_f32_16x16x32_bf16 v[38:41], v[166:169], v[212:215], v[38:41]
	v_mfma_f32_16x16x32_bf16 v[34:37], v[190:193], v[212:215], v[34:37]
	v_mfma_f32_16x16x32_bf16 v[22:25], v[166:169], v[220:223], v[22:25]
	v_mfma_f32_16x16x32_bf16 v[18:21], v[190:193], v[220:223], v[18:21]
	v_mfma_f32_16x16x32_bf16 v[6:9], v[166:169], v[228:231], v[6:9]
	v_mfma_f32_16x16x32_bf16 v[2:5], v[190:193], v[228:231], v[2:5]
	v_mfma_f32_16x16x32_bf16 v[54:57], v[176:179], v[208:211], v[54:57]
	v_mfma_f32_16x16x32_bf16 v[50:53], v[200:203], v[208:211], v[50:53]
	v_mfma_f32_16x16x32_bf16 v[38:41], v[176:179], v[216:219], v[38:41]
	v_mfma_f32_16x16x32_bf16 v[34:37], v[200:203], v[216:219], v[34:37]
	v_mfma_f32_16x16x32_bf16 v[22:25], v[176:179], v[224:227], v[22:25]
	v_mfma_f32_16x16x32_bf16 v[18:21], v[200:203], v[224:227], v[18:21]
	v_mfma_f32_16x16x32_bf16 v[6:9], v[176:179], v[232:235], v[6:9]
	v_mfma_f32_16x16x32_bf16 v[2:5], v[200:203], v[232:235], v[2:5]
	s_setprio 0
	s_barrier
	s_add_i32 s33, 0, 0x18000
	s_add_i32 s53, 0, 0x1c000
	v_add_u32_e32 v142, s33, v175
	v_add_u32_e32 v158, s53, v175
	ds_read_b128 v[130:133], v142
	ds_read_b128 v[134:137], v142 offset:1024
	ds_read_b128 v[138:141], v142 offset:2048
	ds_read_b128 v[142:145], v142 offset:3072
	ds_read_b128 v[166:169], v158
	ds_read_b128 v[176:179], v158 offset:1024
	ds_read_b128 v[190:193], v158 offset:2048
	ds_read_b128 v[200:203], v158 offset:3072
	s_mov_b32 m0, s34
	v_lshl_add_u64 v[186:187], s[24:25], 0, v[152:153]
	ds_read_b128 v[204:207], v199 offset:32768
	ds_read_b128 v[208:211], v199 offset:33792
	ds_read_b128 v[212:215], v199 offset:34816
	ds_read_b128 v[216:219], v199 offset:35840
	ds_read_b128 v[220:223], v199 offset:36864
	ds_read_b128 v[224:227], v199 offset:37888
	ds_read_b128 v[228:231], v199 offset:38912
	ds_read_b128 v[232:235], v199 offset:39936
	global_load_lds_dwordx4 v[186:187], off
	v_lshl_add_u64 v[186:187], s[24:25], 0, v[156:157]
	s_mov_b32 m0, s35
	s_nop 0
	global_load_lds_dwordx4 v[186:187], off
	s_waitcnt vmcnt(8)
	s_waitcnt lgkmcnt(0)
	s_barrier
	s_setprio 1
	s_waitcnt lgkmcnt(0)
	v_mfma_f32_16x16x32_bf16 v[126:129], v[130:133], v[204:207], v[126:129]
	v_mfma_f32_16x16x32_bf16 v[122:125], v[138:141], v[204:207], v[122:125]
	v_mfma_f32_16x16x32_bf16 v[110:113], v[130:133], v[212:215], v[110:113]
	v_mfma_f32_16x16x32_bf16 v[106:109], v[138:141], v[212:215], v[106:109]
	v_mfma_f32_16x16x32_bf16 v[94:97], v[130:133], v[220:223], v[94:97]
	v_mfma_f32_16x16x32_bf16 v[90:93], v[138:141], v[220:223], v[90:93]
	v_mfma_f32_16x16x32_bf16 v[78:81], v[130:133], v[228:231], v[78:81]
	v_mfma_f32_16x16x32_bf16 v[74:77], v[138:141], v[228:231], v[74:77]
	v_mfma_f32_16x16x32_bf16 v[126:129], v[134:137], v[208:211], v[126:129]
	v_mfma_f32_16x16x32_bf16 v[122:125], v[142:145], v[208:211], v[122:125]
	v_mfma_f32_16x16x32_bf16 v[110:113], v[134:137], v[216:219], v[110:113]
	v_mfma_f32_16x16x32_bf16 v[106:109], v[142:145], v[216:219], v[106:109]
	v_mfma_f32_16x16x32_bf16 v[94:97], v[134:137], v[224:227], v[94:97]
	v_mfma_f32_16x16x32_bf16 v[90:93], v[142:145], v[224:227], v[90:93]
	v_mfma_f32_16x16x32_bf16 v[78:81], v[134:137], v[232:235], v[78:81]
	v_mfma_f32_16x16x32_bf16 v[74:77], v[142:145], v[232:235], v[74:77]
	v_mfma_f32_16x16x32_bf16 v[118:121], v[166:169], v[204:207], v[118:121]
	v_mfma_f32_16x16x32_bf16 v[114:117], v[190:193], v[204:207], v[114:117]
	v_mfma_f32_16x16x32_bf16 v[102:105], v[166:169], v[212:215], v[102:105]
	v_mfma_f32_16x16x32_bf16 v[98:101], v[190:193], v[212:215], v[98:101]
	v_mfma_f32_16x16x32_bf16 v[86:89], v[166:169], v[220:223], v[86:89]
	v_mfma_f32_16x16x32_bf16 v[82:85], v[190:193], v[220:223], v[82:85]
	v_mfma_f32_16x16x32_bf16 v[70:73], v[166:169], v[228:231], v[70:73]
	v_mfma_f32_16x16x32_bf16 v[66:69], v[190:193], v[228:231], v[66:69]
	v_mfma_f32_16x16x32_bf16 v[118:121], v[176:179], v[208:211], v[118:121]
	v_mfma_f32_16x16x32_bf16 v[114:117], v[200:203], v[208:211], v[114:117]
	v_mfma_f32_16x16x32_bf16 v[102:105], v[176:179], v[216:219], v[102:105]
	v_mfma_f32_16x16x32_bf16 v[98:101], v[200:203], v[216:219], v[98:101]
	v_mfma_f32_16x16x32_bf16 v[86:89], v[176:179], v[224:227], v[86:89]
	v_mfma_f32_16x16x32_bf16 v[82:85], v[200:203], v[224:227], v[82:85]
	v_mfma_f32_16x16x32_bf16 v[70:73], v[176:179], v[232:235], v[70:73]
	v_mfma_f32_16x16x32_bf16 v[66:69], v[200:203], v[232:235], v[66:69]
	s_setprio 0
	s_barrier
; #define G8_STAGE(bufoff, gbase, v0, v1) do { \
;         __builtin_amdgcn_global_load_lds((const unsigned*)((const char*)(gbase) + (v0)), (LAS unsigned*)(lds + (bufoff) + ldsw), 16, 0, 0); \
;         __builtin_amdgcn_global_load_lds((const unsigned*)((const char*)(gbase) + (v1)), (LAS unsigned*)(lds + (bufoff) + ldsw + 8192), 16, 0, 0); } while (0)
; #define G8_LDA(dst, b, h) do { _Pragma("unroll") for (int m = 0; m < 4; ++m) _Pragma("unroll") for (int k = 0; k < 2; ++k) dst[m][k] = *(const LAS bf16x8*)(lds + G8_SA(b, h) + aoff + m * 2048 + k * 1024); } while (0)
; #define G8_MMA(ai, bj, At, Bt) do { __builtin_amdgcn_s_setprio(1); _Pragma("unroll") for (int m = 0; m < 4; ++m) _Pragma("unroll") for (int n = 0; n < 2; ++n) _Pragma("unroll") for (int k = 0; k < 2; ++k) \
;         acc[ai][bj][m][n] = __builtin_amdgcn_mfma_f32_16x16x32_bf16(Bt[n][k], At[m][k], acc[ai][bj][m][n], 0, 0, 0); __builtin_amdgcn_s_setprio(0); } while (0)
; #define G8_WAIT_V(n) asm volatile("s_waitcnt vmcnt(" #n ")" ::: "memory")
; #define G8_WAIT_L(n) asm volatile("s_waitcnt lgkmcnt(" #n ")" ::: "memory")
; #define G8_BAR __builtin_amdgcn_s_barrier()
; #define G8_SCHED __builtin_amdgcn_sched_barrier(0)
; template <class Epi, class Sched, bool GATHER, bool ALIGN_EPI, bool PFB = false>
; __device__ __forceinline__ void gemm_phase(LAS unsigned char* lds, const int lda, const int K, const Sched& S, const Epi& E) {
;     ...
;             G8_LDA(At, 1, 1); G8_STAGE(G8_SB(1, 0), b3, voffB[0], voffB[1]); G8_STAGE(G8_SB(1, 1), b3 + hstepB, voffB[0], voffB[1]); G8_STAGE(G8_SA(1, 0), a3, x00, x01);
;             G8_WAIT_V(8); G8_WAIT_L(0); G8_BAR; G8_MMA(1, 0, At, B0); G8_MMA(1, 1, At, B1); G8_BAR; G8_SCHED;
;         }
	s_add_u32 s24, s22, 0x8000
	s_addc_u32 s25, s23, 0
	s_add_i32 s33, s33, s29
	v_lshl_add_u64 v[186:187], s[24:25], 0, v[146:147]
	s_mov_b32 m0, s33
	ds_read_b128 v[204:207], v199 offset:49152
	ds_read_b128 v[208:211], v199 offset:50176
	ds_read_b128 v[212:215], v199 offset:51200
	ds_read_b128 v[216:219], v199 offset:52224
	ds_read_b128 v[220:223], v199 offset:53248
	ds_read_b128 v[224:227], v199 offset:54272
	ds_read_b128 v[228:231], v199 offset:55296
	ds_read_b128 v[232:235], v199 offset:56320
	global_load_lds_dwordx4 v[186:187], off
	s_add_i32 m0, s33, 0x2000
	s_add_u32 s22, s22, 0xc000
	v_lshl_add_u64 v[186:187], s[24:25], 0, v[148:149]
	s_addc_u32 s23, s23, 0
	s_add_i32 s24, s53, s29
	global_load_lds_dwordx4 v[186:187], off
	v_lshl_add_u64 v[186:187], s[22:23], 0, v[146:147]
	s_mov_b32 m0, s24
	v_lshl_add_u64 v[170:171], v[170:171], 0, s[6:7]
	global_load_lds_dwordx4 v[186:187], off
	v_lshl_add_u64 v[186:187], s[22:23], 0, v[148:149]
	s_add_i32 m0, s24, 0x2000
	s_nop 0
	global_load_lds_dwordx4 v[186:187], off
	s_mov_b32 m0, s37
	s_nop 0
	global_load_lds_dwordx4 v[170:171], off
	v_lshl_add_u64 v[170:171], v[182:183], 0, s[6:7]
	s_mov_b32 m0, s38
	s_nop 0
	global_load_lds_dwordx4 v[170:171], off
	s_waitcnt vmcnt(8)
	s_waitcnt lgkmcnt(0)
	s_barrier
	s_setprio 1
	s_waitcnt lgkmcnt(0)
	v_mfma_f32_16x16x32_bf16 v[62:65], v[130:133], v[204:207], v[62:65]
	v_mfma_f32_16x16x32_bf16 v[58:61], v[138:141], v[204:207], v[58:61]
	v_mfma_f32_16x16x32_bf16 v[46:49], v[130:133], v[212:215], v[46:49]
	v_mfma_f32_16x16x32_bf16 v[42:45], v[138:141], v[212:215], v[42:45]
	v_mfma_f32_16x16x32_bf16 v[30:33], v[130:133], v[220:223], v[30:33]
	v_mfma_f32_16x16x32_bf16 v[26:29], v[138:141], v[220:223], v[26:29]
	v_mfma_f32_16x16x32_bf16 v[14:17], v[130:133], v[228:231], v[14:17]
	v_mfma_f32_16x16x32_bf16 v[10:13], v[138:141], v[228:231], v[10:13]
	v_mfma_f32_16x16x32_bf16 v[62:65], v[134:137], v[208:211], v[62:65]
	v_mfma_f32_16x16x32_bf16 v[58:61], v[142:145], v[208:211], v[58:61]
	v_mfma_f32_16x16x32_bf16 v[46:49], v[134:137], v[216:219], v[46:49]
	v_mfma_f32_16x16x32_bf16 v[42:45], v[142:145], v[216:219], v[42:45]
	v_mfma_f32_16x16x32_bf16 v[30:33], v[134:137], v[224:227], v[30:33]
	v_mfma_f32_16x16x32_bf16 v[26:29], v[142:145], v[224:227], v[26:29]
	v_mfma_f32_16x16x32_bf16 v[14:17], v[134:137], v[232:235], v[14:17]
	v_mfma_f32_16x16x32_bf16 v[10:13], v[142:145], v[232:235], v[10:13]
	v_mfma_f32_16x16x32_bf16 v[54:57], v[166:169], v[204:207], v[54:57]
	v_mfma_f32_16x16x32_bf16 v[50:53], v[190:193], v[204:207], v[50:53]
	v_mfma_f32_16x16x32_bf16 v[38:41], v[166:169], v[212:215], v[38:41]
	v_mfma_f32_16x16x32_bf16 v[34:37], v[190:193], v[212:215], v[34:37]
	v_mfma_f32_16x16x32_bf16 v[22:25], v[166:169], v[220:223], v[22:25]
	v_mfma_f32_16x16x32_bf16 v[18:21], v[190:193], v[220:223], v[18:21]
	v_mfma_f32_16x16x32_bf16 v[6:9], v[166:169], v[228:231], v[6:9]
	v_mfma_f32_16x16x32_bf16 v[2:5], v[190:193], v[228:231], v[2:5]
	v_mfma_f32_16x16x32_bf16 v[54:57], v[176:179], v[208:211], v[54:57]
	v_mfma_f32_16x16x32_bf16 v[50:53], v[200:203], v[208:211], v[50:53]
	v_mfma_f32_16x16x32_bf16 v[38:41], v[176:179], v[216:219], v[38:41]
	v_mfma_f32_16x16x32_bf16 v[34:37], v[200:203], v[216:219], v[34:37]
	v_mfma_f32_16x16x32_bf16 v[22:25], v[176:179], v[224:227], v[22:25]
	v_mfma_f32_16x16x32_bf16 v[18:21], v[200:203], v[224:227], v[18:21]
	v_mfma_f32_16x16x32_bf16 v[6:9], v[176:179], v[232:235], v[6:9]
	v_mfma_f32_16x16x32_bf16 v[2:5], v[200:203], v[232:235], v[2:5]
	s_setprio 0
	s_barrier
	s_add_i32 s52, s52, 2
	s_add_u32 s19, s19, 0x10000
	s_addc_u32 s51, s51, 0
	s_add_u32 s20, s20, 0x100
	s_addc_u32 s21, s21, 0
	s_cmp_gt_u32 s52, 13
	s_cbranch_scc0 .LBB0_2448
	s_and_b64 vcc, exec, s[8:9]
	s_cbranch_vccz .LBB0_2451
	s_barrier
